# P8: the first two rows' x/y loads issued before the table barrier (prologue de-serialisation)
# speedup vs baseline: 1.0245x; 1.0033x over previous
.LBB0_1038:
	s_or_b64 exec, exec, s[8:9]
	s_and_saveexec_b64 s[0:1], s[4:5]
	ds_write_b32 v141, v123 offset:57344
	s_or_b64 exec, exec, s[0:1]
	s_ashr_i32 s3, s2, 31
	s_lshl_b64 s[0:1], s[2:3], 6
	s_add_u32 s0, s0, s34
	s_addc_u32 s1, s1, 0
	s_lshl_b64 s[8:9], s[0:1], 12
	v_lshl_add_u64 v[0:1], v[130:131], 0, s[8:9]
	global_load_dwordx4 v[80:83], v[0:1], off
	global_load_dwordx4 v[88:91], v[0:1], off offset:1024
	global_load_dwordx4 v[92:95], v[0:1], off offset:2048
	global_load_dwordx4 v[158:161], v[0:1], off offset:3072
	s_lshl_b64 s[20:21], s[0:1], 13
	v_readlane_b32 s36, v253, 10
	v_readlane_b32 s37, v253, 11
	s_add_u32 s20, s36, s20
	s_addc_u32 s21, s37, s21
	global_load_dwordx4 v[72:75], v122, s[20:21] offset:16
	global_load_dwordx4 v[76:79], v122, s[20:21]
	global_load_dwordx4 v[64:67], v122, s[20:21] offset:2064
	global_load_dwordx4 v[68:71], v122, s[20:21] offset:2048
	global_load_dwordx4 v[56:59], v149, s[20:21] offset:16
	global_load_dwordx4 v[60:63], v149, s[20:21]
	global_load_dwordx4 v[48:51], v150, s[20:21] offset:16
	global_load_dwordx4 v[52:55], v150, s[20:21]
	s_or_b32 s20, s0, 1
	s_mov_b32 s21, s1
	s_lshl_b64 s[22:23], s[20:21], 12
	s_lshl_b64 s[24:25], s[20:21], 13
	s_add_u32 s24, s36, s24
	v_lshl_add_u64 v[0:1], v[130:131], 0, s[22:23]
	s_addc_u32 s25, s37, s25
	global_load_dwordx4 v[44:47], v[0:1], off
	global_load_dwordx4 v[40:43], v[0:1], off offset:1024
	global_load_dwordx4 v[36:39], v[0:1], off offset:2048
	global_load_dwordx4 v[32:35], v[0:1], off offset:3072
	global_load_dwordx4 v[24:27], v122, s[24:25] offset:16
	global_load_dwordx4 v[28:31], v122, s[24:25]
	global_load_dwordx4 v[16:19], v122, s[24:25] offset:2064
	global_load_dwordx4 v[20:23], v122, s[24:25] offset:2048
	global_load_dwordx4 v[8:11], v149, s[24:25] offset:16
	global_load_dwordx4 v[12:15], v149, s[24:25]
	global_load_dwordx4 v[0:3], v150, s[24:25] offset:16
	global_load_dwordx4 v[4:7], v150, s[24:25]
	s_waitcnt lgkmcnt(0)
	s_barrier
	v_readlane_b32 s38, v253, 12
	v_readlane_b32 s39, v253, 13
	v_readlane_b32 s40, v253, 14
	v_readlane_b32 s41, v253, 15
	v_readlane_b32 s42, v253, 16
	v_readlane_b32 s43, v253, 17
	v_readlane_b32 s44, v253, 18
	v_readlane_b32 s45, v253, 19
	v_readlane_b32 s46, v253, 20
	v_readlane_b32 s47, v253, 21
	v_readlane_b32 s48, v253, 22
	v_readlane_b32 s49, v253, 23
	v_readlane_b32 s50, v253, 24
	v_readlane_b32 s51, v253, 25
	s_waitcnt vmcnt(23)
	v_and_b32_e32 v87, 0xffff0000, v80
	v_lshlrev_b32_e32 v116, 16, v80
	v_lshlrev_b32_e32 v84, 16, v82
	v_and_b32_e32 v115, 0xffff0000, v82
	v_mul_f32_e32 v82, v87, v87
	v_lshlrev_b32_e32 v86, 16, v81
	v_fmac_f32_e32 v82, v116, v116
	v_and_b32_e32 v85, 0xffff0000, v81
	v_fmac_f32_e32 v82, v86, v86
	v_fmac_f32_e32 v82, v85, v85
	v_fmac_f32_e32 v82, v84, v84
	v_lshlrev_b32_e32 v114, 16, v83
	v_fmac_f32_e32 v82, v115, v115
	v_and_b32_e32 v113, 0xffff0000, v83
	v_fmac_f32_e32 v82, v114, v114
	v_fmac_f32_e32 v82, v113, v113
	s_waitcnt vmcnt(22)
	v_lshlrev_b32_e32 v112, 16, v88
	v_and_b32_e32 v111, 0xffff0000, v88
	v_fmac_f32_e32 v82, v112, v112
	v_lshlrev_b32_e32 v110, 16, v89
	v_fmac_f32_e32 v82, v111, v111
	v_and_b32_e32 v109, 0xffff0000, v89
	v_fmac_f32_e32 v82, v110, v110
	v_lshlrev_b32_e32 v108, 16, v90
	v_fmac_f32_e32 v82, v109, v109
	v_and_b32_e32 v107, 0xffff0000, v90
	v_fmac_f32_e32 v82, v108, v108
	v_lshlrev_b32_e32 v106, 16, v91
	v_fmac_f32_e32 v82, v107, v107
	v_and_b32_e32 v105, 0xffff0000, v91
	v_fmac_f32_e32 v82, v106, v106
	v_fmac_f32_e32 v82, v105, v105
	s_waitcnt vmcnt(21)
	v_lshlrev_b32_e32 v104, 16, v92
	v_and_b32_e32 v103, 0xffff0000, v92
	v_fmac_f32_e32 v82, v104, v104
	v_lshlrev_b32_e32 v102, 16, v93
	v_fmac_f32_e32 v82, v103, v103
	v_and_b32_e32 v101, 0xffff0000, v93
	v_fmac_f32_e32 v82, v102, v102
	v_lshlrev_b32_e32 v100, 16, v94
	v_fmac_f32_e32 v82, v101, v101
	v_and_b32_e32 v99, 0xffff0000, v94
	v_fmac_f32_e32 v82, v100, v100
	v_lshlrev_b32_e32 v98, 16, v95
	v_fmac_f32_e32 v82, v99, v99
	v_and_b32_e32 v97, 0xffff0000, v95
	v_fmac_f32_e32 v82, v98, v98
	v_fmac_f32_e32 v82, v97, v97
	s_waitcnt vmcnt(20)
	v_lshlrev_b32_e32 v96, 16, v158
	v_and_b32_e32 v91, 0xffff0000, v158
	v_fmac_f32_e32 v82, v96, v96
	v_and_b32_e32 v94, 0xffff0000, v159
	v_lshlrev_b32_e32 v95, 16, v159
	v_fmac_f32_e32 v82, v91, v91
	v_pk_mul_f32 v[80:81], v[94:95], v[94:95]
	v_and_b32_e32 v92, 0xffff0000, v160
	v_add_f32_e32 v81, v81, v82
	v_lshlrev_b32_e32 v93, 16, v160
	v_add_f32_e32 v82, v80, v81
	v_pk_mul_f32 v[80:81], v[92:93], v[92:93]
	v_and_b32_e32 v88, 0xffff0000, v161
	v_add_f32_e32 v81, v81, v82
	v_lshlrev_b32_e32 v89, 16, v161
	v_add_f32_e32 v82, v80, v81
	v_pk_mul_f32 v[80:81], v[88:89], v[88:89]
	s_nop 0
	v_add_f32_e32 v81, v81, v82
	v_add_f32_e32 v80, v80, v81
	s_nop 1
	v_add_f32_dpp v80, v80, v80 quad_perm:[1,0,3,2] row_mask:0xf bank_mask:0xf bound_ctrl:1
	s_nop 1
	v_add_f32_dpp v80, v80, v80 quad_perm:[2,3,0,1] row_mask:0xf bank_mask:0xf bound_ctrl:1
	s_nop 1
	v_add_f32_dpp v80, v80, v80 row_ror:4 row_mask:0xf bank_mask:0xf bound_ctrl:1
	s_nop 1
	v_add_f32_dpp v80, v80, v80 row_ror:8 row_mask:0xf bank_mask:0xf bound_ctrl:1
	s_nop 0
	v_readlane_b32 s3, v80, 16
	v_readlane_b32 s26, v80, 48
	v_readlane_b32 s24, v80, 0
	v_readlane_b32 s25, v80, 32
	v_mov_b32_e32 v80, s3
	v_mov_b32_e32 v81, s26
	v_pk_add_f32 v[80:81], s[24:25], v[80:81]
	s_nop 0
	v_add_f32_e32 v80, v80, v81
	v_fmamk_f32 v80, v80, 0x3a000000, v151
	v_cmp_gt_f32_e32 vcc, s11, v80
	v_mul_f32_e32 v81, 0x4b800000, v80
	s_nop 0
	v_cndmask_b32_e32 v80, v80, v81, vcc
	v_rsq_f32_e32 v80, v80
	s_nop 0
	v_mul_f32_e32 v81, 0x45800000, v80
	v_cndmask_b32_e32 v90, v80, v81, vcc
	ds_read_b128 v[158:161], v144
	ds_read_b128 v[80:83], v144 offset:16
	v_mul_f32_e32 v129, v90, v116
	ds_read_b128 v[116:119], v144 offset:8192
	v_mul_f32_e32 v87, v90, v87
	v_mul_f32_e32 v86, v90, v86
	v_mul_f32_e32 v85, v90, v85
	s_waitcnt lgkmcnt(0)
	v_mul_f32_e32 v87, v117, v87
	v_mul_f32_e32 v86, v118, v86
	v_mul_f32_e32 v85, v119, v85
	s_waitcnt vmcnt(18)
	v_fma_f32 v77, v159, v87, v77
	v_fma_f32 v78, v160, v86, v78
	v_fmac_f32_e32 v79, v161, v85
	v_mul_f32_e32 v117, v90, v84
	ds_read_b128 v[84:87], v144 offset:8208
	v_mul_f32_e32 v116, v116, v129
	v_fma_f32 v76, v158, v116, v76
	v_mul_f32_e32 v116, v77, v77
	v_fmac_f32_e32 v116, v76, v76
	s_waitcnt lgkmcnt(0)
	v_mul_f32_e32 v84, v117, v84
	v_fma_f32 v80, v80, v84, v72
	v_mul_f32_e32 v72, v90, v115
	v_mul_f32_e32 v72, v72, v85
	v_fmac_f32_e32 v116, v78, v78
	v_fma_f32 v81, v81, v72, v73
	v_mul_f32_e32 v72, v90, v114
	v_fmac_f32_e32 v116, v79, v79
	v_mul_f32_e32 v72, v72, v86
	v_fmac_f32_e32 v116, v80, v80
	v_fma_f32 v82, v82, v72, v74
	v_mul_f32_e32 v72, v90, v113
	v_fmac_f32_e32 v116, v81, v81
	v_mul_f32_e32 v72, v72, v87
	v_fmac_f32_e32 v116, v82, v82
	v_fmac_f32_e32 v75, v83, v72
	v_cvt_pk_bf16_f32 v72, v76, v77
	v_lshl_add_u64 v[76:77], v[132:133], 0, s[8:9]
	v_fmac_f32_e32 v116, v75, v75
	v_cvt_pk_bf16_f32 v73, v78, v79
	v_cvt_pk_bf16_f32 v74, v80, v81
	v_cvt_pk_bf16_f32 v75, v82, v75
	global_store_dwordx4 v[76:77], v[72:75], off
	ds_read_b128 v[78:81], v144 offset:2048
	ds_read_b128 v[82:85], v144 offset:2064
	v_mul_f32_e32 v86, v90, v112
	ds_read_b128 v[112:115], v144 offset:10240
	s_waitcnt lgkmcnt(0)
	v_mul_f32_e32 v86, v86, v112
	s_waitcnt vmcnt(17)
	v_fma_f32 v68, v78, v86, v68
	v_mul_f32_e32 v78, v90, v111
	v_mul_f32_e32 v78, v78, v113
	v_fma_f32 v69, v79, v78, v69
	v_mul_f32_e32 v78, v90, v110
	v_mul_f32_e32 v78, v78, v114
	v_fma_f32 v70, v80, v78, v70
	v_mul_f32_e32 v78, v90, v109
	v_mul_f32_e32 v78, v78, v115
	v_fmac_f32_e32 v71, v81, v78
	ds_read_b128 v[78:81], v144 offset:10256
	v_mul_f32_e32 v86, v90, v108
	v_fmac_f32_e32 v116, v68, v68
	v_fmac_f32_e32 v116, v69, v69
	v_fmac_f32_e32 v116, v70, v70
	s_waitcnt lgkmcnt(0)
	v_mul_f32_e32 v78, v86, v78
	v_fma_f32 v78, v82, v78, v64
	v_mul_f32_e32 v64, v90, v107
	v_mul_f32_e32 v64, v64, v79
	v_fma_f32 v79, v83, v64, v65
	v_mul_f32_e32 v64, v90, v106
	v_fmac_f32_e32 v116, v71, v71
	v_mul_f32_e32 v64, v64, v80
	v_fmac_f32_e32 v116, v78, v78
	v_fma_f32 v80, v84, v64, v66
	v_mul_f32_e32 v64, v90, v105
	v_fmac_f32_e32 v116, v79, v79
	v_mul_f32_e32 v64, v64, v81
	v_fmac_f32_e32 v116, v80, v80
	v_fmac_f32_e32 v67, v85, v64
	v_fmac_f32_e32 v116, v67, v67
	v_cvt_pk_bf16_f32 v64, v68, v69
	v_cvt_pk_bf16_f32 v65, v70, v71
	v_cvt_pk_bf16_f32 v66, v78, v79
	v_cvt_pk_bf16_f32 v67, v80, v67
	global_store_dwordx4 v[76:77], v[64:67], off offset:1024
	ds_read_b128 v[68:71], v144 offset:4096
	ds_read_b128 v[78:81], v144 offset:4112
	ds_read_b128 v[82:85], v144 offset:12288
	v_mul_f32_e32 v86, v90, v104
	s_waitcnt lgkmcnt(0)
	v_mul_f32_e32 v82, v86, v82
	s_waitcnt vmcnt(16)
	v_fma_f32 v60, v68, v82, v60
	v_mul_f32_e32 v68, v90, v103
	v_mul_f32_e32 v68, v68, v83
	v_fma_f32 v61, v69, v68, v61
	v_mul_f32_e32 v68, v90, v102
	v_mul_f32_e32 v68, v68, v84
	v_fma_f32 v62, v70, v68, v62
	v_mul_f32_e32 v68, v90, v101
	v_mul_f32_e32 v68, v68, v85
	v_fmac_f32_e32 v63, v71, v68
	ds_read_b128 v[68:71], v144 offset:12304
	v_mul_f32_e32 v82, v90, v100
	v_fmac_f32_e32 v116, v60, v60
	v_fmac_f32_e32 v116, v61, v61
	v_fmac_f32_e32 v116, v62, v62
	s_waitcnt lgkmcnt(0)
	v_mul_f32_e32 v68, v82, v68
	v_fma_f32 v68, v78, v68, v56
	v_mul_f32_e32 v56, v90, v99
	v_mul_f32_e32 v56, v56, v69
	v_fma_f32 v69, v79, v56, v57
	v_mul_f32_e32 v56, v90, v98
	v_fmac_f32_e32 v116, v63, v63
	v_mul_f32_e32 v56, v56, v70
	v_fmac_f32_e32 v116, v68, v68
	v_fma_f32 v70, v80, v56, v58
	v_mul_f32_e32 v56, v90, v97
	v_fmac_f32_e32 v116, v69, v69
	v_mul_f32_e32 v56, v56, v71
	v_fmac_f32_e32 v116, v70, v70
	v_fmac_f32_e32 v59, v81, v56
	v_fmac_f32_e32 v116, v59, v59
	v_cvt_pk_bf16_f32 v56, v60, v61
	v_cvt_pk_bf16_f32 v57, v62, v63
	v_cvt_pk_bf16_f32 v58, v68, v69
	v_cvt_pk_bf16_f32 v59, v70, v59
	global_store_dwordx4 v[76:77], v[56:59], off offset:2048
	ds_read_b128 v[60:63], v144 offset:6144
	ds_read_b128 v[68:71], v144 offset:6160
	ds_read_b128 v[78:81], v144 offset:14336
	v_mul_f32_e32 v82, v90, v96
	s_waitcnt lgkmcnt(0)
	v_mul_f32_e32 v78, v82, v78
	s_waitcnt vmcnt(15)
	v_fma_f32 v78, v60, v78, v52
	v_mul_f32_e32 v52, v90, v91
	v_mul_f32_e32 v52, v52, v79
	v_fma_f32 v79, v61, v52, v53
	v_pk_mul_f32 v[52:53], v[90:91], v[94:95] op_sel_hi:[0,1]
	v_pk_mul_f32 v[52:53], v[52:53], v[80:81] op_sel:[1,0] op_sel_hi:[0,1]
	v_fmac_f32_e32 v116, v78, v78
	v_pk_fma_f32 v[60:61], v[62:63], v[52:53], v[54:55]
	v_fmac_f32_e32 v116, v79, v79
	v_pk_mul_f32 v[52:53], v[60:61], v[60:61]
	v_pk_mul_f32 v[62:63], v[90:91], v[92:93] op_sel_hi:[0,1]
	v_add_f32_e32 v52, v116, v52
	v_add_f32_e32 v80, v52, v53
	ds_read_b128 v[52:55], v144 offset:14352
	s_waitcnt lgkmcnt(0)
	v_pk_mul_f32 v[52:53], v[62:63], v[52:53] op_sel:[1,0] op_sel_hi:[0,1]
	v_pk_fma_f32 v[52:53], v[68:69], v[52:53], v[48:49]
	s_nop 0
	v_pk_mul_f32 v[48:49], v[52:53], v[52:53]
	s_nop 0
	v_add_f32_e32 v48, v80, v48
	v_add_f32_e32 v62, v48, v49
	v_pk_mul_f32 v[48:49], v[90:91], v[88:89] op_sel_hi:[0,1]
	v_pk_mul_f32 v[48:49], v[48:49], v[54:55] op_sel:[1,0] op_sel_hi:[0,1]
	v_pk_fma_f32 v[54:55], v[70:71], v[48:49], v[50:51]
	s_nop 0
	v_pk_mul_f32 v[48:49], v[54:55], v[54:55]
	s_nop 0
	v_add_f32_e32 v48, v62, v48
	v_add_f32_e32 v62, v48, v49
	v_cvt_pk_bf16_f32 v48, v78, v79
	v_cvt_pk_bf16_f32 v49, v60, v61
	v_cvt_pk_bf16_f32 v50, v52, v53
	v_cvt_pk_bf16_f32 v51, v54, v55
	global_store_dwordx4 v[76:77], v[48:51], off offset:3072
	s_nop 0
	v_add_f32_dpp v52, v62, v62 quad_perm:[1,0,3,2] row_mask:0xf bank_mask:0xf bound_ctrl:1
	s_nop 1
	v_add_f32_dpp v52, v52, v52 quad_perm:[2,3,0,1] row_mask:0xf bank_mask:0xf bound_ctrl:1
	s_nop 1
	v_add_f32_dpp v52, v52, v52 row_ror:4 row_mask:0xf bank_mask:0xf bound_ctrl:1
	s_nop 1
	v_add_f32_dpp v52, v52, v52 row_ror:8 row_mask:0xf bank_mask:0xf bound_ctrl:1
	s_nop 0
	v_readlane_b32 s3, v52, 16
	v_readlane_b32 s24, v52, 48
	v_readlane_b32 s8, v52, 0
	v_readlane_b32 s9, v52, 32
	v_mov_b32_e32 v52, s3
	v_mov_b32_e32 v53, s24
	v_pk_add_f32 v[52:53], s[8:9], v[52:53]
	s_nop 0
	v_add_f32_e32 v52, v52, v53
	v_fmamk_f32 v52, v52, 0x3a000000, v151
	v_cmp_gt_f32_e32 vcc, s11, v52
	v_mul_f32_e32 v53, 0x4b800000, v52
	s_nop 0
	v_cndmask_b32_e32 v52, v52, v53, vcc
	v_rsq_f32_e32 v52, v52
	s_nop 0
	v_mul_f32_e32 v53, 0x45800000, v52
	v_cndmask_b32_e32 v54, v52, v53, vcc
	s_and_saveexec_b64 s[8:9], s[6:7]
	v_mov_b32_e32 v52, s10
	ds_write_b32 v52, v54 offset:60672
	s_or_b64 exec, exec, s[8:9]
	v_lshlrev_b32_e32 v52, 16, v72
	v_and_b32_e32 v53, 0xffff0000, v72
	v_lshlrev_b32_e32 v55, 16, v73
	v_and_b32_e32 v76, 0xffff0000, v73
	v_lshlrev_b32_e32 v77, 16, v74
	v_and_b32_e32 v78, 0xffff0000, v74
	v_lshlrev_b32_e32 v79, 16, v75
	v_and_b32_e32 v80, 0xffff0000, v75
	ds_read_b128 v[60:63], v144 offset:16384
	ds_read_b128 v[68:71], v144 offset:16400
	ds_read_b128 v[72:75], v144 offset:32768
	v_mul_f32_e32 v52, v54, v52
	v_mul_f32_e32 v53, v54, v53
	v_mul_f32_e32 v55, v54, v55
	s_lshl_b64 s[8:9], s[0:1], 11
	s_waitcnt lgkmcnt(0)
	v_fma_f32 v52, v52, v60, v72
	v_mul_f32_e32 v60, v54, v76
	v_fma_f32 v53, v53, v61, v73
	v_fma_f32 v55, v55, v62, v74
	v_fmac_f32_e32 v75, v60, v63
	ds_read_b128 v[60:63], v144 offset:32784
	v_mul_f32_e32 v72, v54, v77
	v_med3_f32 v52, v52, s12, v154
	v_med3_f32 v53, v53, s12, v154
	v_med3_f32 v55, v55, s12, v154
	s_waitcnt lgkmcnt(0)
	v_fma_f32 v68, v72, v68, v60
	v_mul_f32_e32 v60, v54, v78
	v_fma_f32 v61, v60, v69, v61
	v_mul_f32_e32 v60, v54, v79
	v_fma_f32 v62, v60, v70, v62
	v_mul_f32_e32 v60, v54, v80
	v_fmac_f32_e32 v63, v60, v71
	v_mov_b32_e32 v60, 0
	v_cvt_pk_fp8_f32 v60, v52, v53
	v_med3_f32 v52, v68, s12, v154
	v_med3_f32 v53, v61, s12, v154
	v_mov_b32_e32 v61, 0
	v_cvt_pk_fp8_f32 v61, v52, v53
	v_med3_f32 v69, v75, s12, v154
	v_cvt_pk_fp8_f32 v60, v55, v69 op_sel:[0,0,1]
	v_med3_f32 v55, v62, s12, v154
	v_med3_f32 v62, v63, s12, v154
	v_cvt_pk_fp8_f32 v61, v55, v62 op_sel:[0,0,1]
	v_lshl_add_u64 v[52:53], v[134:135], 0, s[8:9]
	v_lshlrev_b32_e32 v55, 16, v64
	v_and_b32_e32 v68, 0xffff0000, v64
	global_store_dwordx2 v[52:53], v[60:61], off
	v_lshlrev_b32_e32 v69, 16, v65
	v_and_b32_e32 v70, 0xffff0000, v65
	v_lshlrev_b32_e32 v71, 16, v66
	v_and_b32_e32 v72, 0xffff0000, v66
	v_lshlrev_b32_e32 v73, 16, v67
	v_and_b32_e32 v74, 0xffff0000, v67
	ds_read_b128 v[60:63], v144 offset:18432
	ds_read_b128 v[64:67], v144 offset:34816
	v_mul_f32_e32 v55, v54, v55
	s_waitcnt vmcnt(16)
	v_and_b32_e32 v100, 0xffff0000, v44
	v_lshlrev_b32_e32 v92, 16, v44
	v_mul_f32_e32 v76, v100, v100
	s_waitcnt lgkmcnt(0)
	v_fma_f32 v55, v55, v60, v64
	v_mul_f32_e32 v60, v54, v68
	v_fma_f32 v64, v60, v61, v65
	v_mul_f32_e32 v60, v54, v69
	v_fma_f32 v65, v60, v62, v66
	v_mul_f32_e32 v60, v54, v70
	v_fmac_f32_e32 v67, v60, v63
	v_mul_f32_e32 v66, v54, v71
	ds_read_b128 v[60:63], v144 offset:18448
	ds_read_b128 v[68:71], v144 offset:34832
	v_med3_f32 v55, v55, s12, v154
	v_lshlrev_b32_e32 v101, 16, v45
	v_fmac_f32_e32 v76, v92, v92
	v_and_b32_e32 v45, 0xffff0000, v45
	s_waitcnt lgkmcnt(0)
	v_fma_f32 v66, v66, v60, v68
	v_mul_f32_e32 v60, v54, v72
	v_fma_f32 v61, v60, v61, v69
	v_mul_f32_e32 v60, v54, v73
	v_fma_f32 v62, v60, v62, v70
	v_mul_f32_e32 v60, v54, v74
	v_fmac_f32_e32 v71, v60, v63
	v_med3_f32 v63, v64, s12, v154
	v_mov_b32_e32 v60, 0
	v_cvt_pk_fp8_f32 v60, v55, v63
	v_med3_f32 v55, v66, s12, v154
	v_med3_f32 v63, v61, s12, v154
	v_mov_b32_e32 v61, 0
	v_cvt_pk_fp8_f32 v61, v55, v63
	v_med3_f32 v64, v65, s12, v154
	v_med3_f32 v65, v67, s12, v154
	v_cvt_pk_fp8_f32 v60, v64, v65 op_sel:[0,0,1]
	v_med3_f32 v62, v62, s12, v154
	v_med3_f32 v64, v71, s12, v154
	v_cvt_pk_fp8_f32 v61, v62, v64 op_sel:[0,0,1]
	v_lshlrev_b32_e32 v55, 16, v56
	v_and_b32_e32 v64, 0xffff0000, v56
	v_lshlrev_b32_e32 v65, 16, v57
	global_store_dwordx2 v[52:53], v[60:61], off offset:512
	v_and_b32_e32 v66, 0xffff0000, v57
	v_lshlrev_b32_e32 v67, 16, v58
	v_and_b32_e32 v68, 0xffff0000, v58
	v_lshlrev_b32_e32 v69, 16, v59
	v_and_b32_e32 v70, 0xffff0000, v59
	ds_read_b128 v[56:59], v144 offset:20480
	ds_read_b128 v[60:63], v144 offset:36864
	v_mul_f32_e32 v55, v54, v55
	v_fmac_f32_e32 v76, v101, v101
	v_lshlrev_b32_e32 v102, 16, v46
	v_fmac_f32_e32 v76, v45, v45
	s_waitcnt lgkmcnt(0)
	v_fma_f32 v55, v55, v56, v60
	v_mul_f32_e32 v56, v54, v64
	v_fma_f32 v60, v56, v57, v61
	v_mul_f32_e32 v56, v54, v65
	v_fma_f32 v61, v56, v58, v62
	v_mul_f32_e32 v56, v54, v66
	v_fmac_f32_e32 v63, v56, v59
	v_mul_f32_e32 v62, v54, v67
	ds_read_b128 v[56:59], v144 offset:20496
	ds_read_b128 v[64:67], v144 offset:36880
	v_med3_f32 v55, v55, s12, v154
	v_and_b32_e32 v46, 0xffff0000, v46
	v_fmac_f32_e32 v76, v102, v102
	v_lshlrev_b32_e32 v103, 16, v47
	s_waitcnt lgkmcnt(0)
	v_fma_f32 v62, v62, v56, v64
	v_mul_f32_e32 v56, v54, v68
	v_fma_f32 v57, v56, v57, v65
	v_mul_f32_e32 v56, v54, v69
	v_fma_f32 v58, v56, v58, v66
	v_mul_f32_e32 v56, v54, v70
	v_fmac_f32_e32 v67, v56, v59
	v_med3_f32 v59, v60, s12, v154
	v_mov_b32_e32 v56, 0
	v_cvt_pk_fp8_f32 v56, v55, v59
	v_med3_f32 v55, v62, s12, v154
	v_med3_f32 v59, v57, s12, v154
	v_mov_b32_e32 v57, 0
	v_cvt_pk_fp8_f32 v57, v55, v59
	v_med3_f32 v60, v61, s12, v154
	v_med3_f32 v61, v63, s12, v154
	v_cvt_pk_fp8_f32 v56, v60, v61 op_sel:[0,0,1]
	v_med3_f32 v58, v58, s12, v154
	v_med3_f32 v60, v67, s12, v154
	v_fmac_f32_e32 v76, v46, v46
	v_cvt_pk_fp8_f32 v57, v58, v60 op_sel:[0,0,1]
	v_and_b32_e32 v47, 0xffff0000, v47
	v_fmac_f32_e32 v76, v103, v103
	v_fmac_f32_e32 v76, v47, v47
	s_waitcnt vmcnt(16)
	v_lshlrev_b32_e32 v108, 16, v40
	v_and_b32_e32 v109, 0xffff0000, v40
	v_fmac_f32_e32 v76, v108, v108
	v_lshlrev_b32_e32 v110, 16, v41
	v_fmac_f32_e32 v76, v109, v109
	global_store_dwordx2 v[52:53], v[56:57], off offset:1024
	v_and_b32_e32 v111, 0xffff0000, v41
	v_fmac_f32_e32 v76, v110, v110
	v_lshlrev_b32_e32 v55, 16, v48
	v_and_b32_e32 v60, 0xffff0000, v48
	v_lshlrev_b32_e32 v61, 16, v49
	v_and_b32_e32 v62, 0xffff0000, v49
	v_lshlrev_b32_e32 v63, 16, v50
	v_and_b32_e32 v64, 0xffff0000, v50
	v_lshlrev_b32_e32 v65, 16, v51
	v_and_b32_e32 v66, 0xffff0000, v51
	ds_read_b128 v[48:51], v144 offset:22528
	ds_read_b128 v[56:59], v144 offset:38912
	v_lshlrev_b32_e32 v116, 16, v42
	v_fmac_f32_e32 v76, v111, v111
	v_and_b32_e32 v117, 0xffff0000, v42
	v_fmac_f32_e32 v76, v116, v116
	v_lshlrev_b32_e32 v118, 16, v43
	v_fmac_f32_e32 v76, v117, v117
	v_and_b32_e32 v119, 0xffff0000, v43
	v_fmac_f32_e32 v76, v118, v118
	v_mul_f32_e32 v55, v54, v55
	v_fmac_f32_e32 v76, v119, v119
	s_waitcnt vmcnt(16)
	v_lshlrev_b32_e32 v129, 16, v36
	s_waitcnt lgkmcnt(0)
	v_fma_f32 v55, v55, v48, v56
	v_mul_f32_e32 v48, v54, v60
	v_and_b32_e32 v157, 0xffff0000, v36
	v_fmac_f32_e32 v76, v129, v129
	v_fma_f32 v56, v48, v49, v57
	v_mul_f32_e32 v48, v54, v61
	v_lshlrev_b32_e32 v158, 16, v37
	v_fmac_f32_e32 v76, v157, v157
	v_fma_f32 v57, v48, v50, v58
	v_mul_f32_e32 v48, v54, v62
	v_and_b32_e32 v159, 0xffff0000, v37
	v_fmac_f32_e32 v76, v158, v158
	v_fmac_f32_e32 v59, v48, v51
	v_mul_f32_e32 v58, v54, v63
	ds_read_b128 v[48:51], v144 offset:22544
	ds_read_b128 v[60:63], v144 offset:38928
	v_lshlrev_b32_e32 v160, 16, v38
	v_fmac_f32_e32 v76, v159, v159
	v_and_b32_e32 v44, 0xffff0000, v38
	v_fmac_f32_e32 v76, v160, v160
	v_lshlrev_b32_e32 v42, 16, v39
	v_fmac_f32_e32 v76, v44, v44
	v_and_b32_e32 v41, 0xffff0000, v39
	v_fmac_f32_e32 v76, v42, v42
	v_fmac_f32_e32 v76, v41, v41
	s_waitcnt vmcnt(15)
	v_lshlrev_b32_e32 v43, 16, v32
	s_waitcnt lgkmcnt(0)
	v_fma_f32 v58, v58, v48, v60
	v_mul_f32_e32 v48, v54, v64
	v_and_b32_e32 v40, 0xffff0000, v32
	v_fmac_f32_e32 v76, v43, v43
	v_and_b32_e32 v36, 0xffff0000, v33
	v_lshlrev_b32_e32 v37, 16, v33
	v_fma_f32 v49, v48, v49, v61
	v_mul_f32_e32 v48, v54, v65
	v_fmac_f32_e32 v76, v40, v40
	v_pk_mul_f32 v[32:33], v[36:37], v[36:37]
	v_fma_f32 v50, v48, v50, v62
	v_mul_f32_e32 v48, v54, v66
	v_add_f32_e32 v33, v33, v76
	v_and_b32_e32 v38, 0xffff0000, v34
	v_lshlrev_b32_e32 v39, 16, v34
	v_fmac_f32_e32 v63, v48, v51
	v_med3_f32 v51, v55, s12, v154
	v_med3_f32 v54, v56, s12, v154
	v_mov_b32_e32 v48, 0
	v_add_f32_e32 v76, v32, v33
	v_pk_mul_f32 v[32:33], v[38:39], v[38:39]
	v_cvt_pk_fp8_f32 v48, v51, v54
	v_med3_f32 v51, v58, s12, v154
	v_med3_f32 v54, v49, s12, v154
	v_mov_b32_e32 v49, 0
	v_add_f32_e32 v33, v33, v76
	v_cvt_pk_fp8_f32 v49, v51, v54
	v_add_f32_e32 v76, v32, v33
	v_and_b32_e32 v32, 0xffff0000, v35
	v_lshlrev_b32_e32 v33, 16, v35
	v_pk_mul_f32 v[34:35], v[32:33], v[32:33]
	v_med3_f32 v55, v57, s12, v154
	v_med3_f32 v56, v59, s12, v154
	v_add_f32_e32 v35, v35, v76
	v_cvt_pk_fp8_f32 v48, v55, v56 op_sel:[0,0,1]
	v_med3_f32 v50, v50, s12, v154
	v_med3_f32 v55, v63, s12, v154
	v_add_f32_e32 v34, v34, v35
	v_cvt_pk_fp8_f32 v49, v50, v55 op_sel:[0,0,1]
	s_or_b32 s24, s0, 2
	v_add_f32_dpp v34, v34, v34 quad_perm:[1,0,3,2] row_mask:0xf bank_mask:0xf bound_ctrl:1
	s_mov_b32 s25, s1
	s_lshl_b64 s[8:9], s[24:25], 12
	v_add_f32_dpp v34, v34, v34 quad_perm:[2,3,0,1] row_mask:0xf bank_mask:0xf bound_ctrl:1
	s_lshl_b64 s[26:27], s[24:25], 13
	v_readlane_b32 s36, v253, 10
	v_add_f32_dpp v34, v34, v34 row_ror:4 row_mask:0xf bank_mask:0xf bound_ctrl:1
	v_readlane_b32 s37, v253, 11
	s_add_u32 s26, s36, s26
	v_add_f32_dpp v34, v34, v34 row_ror:8 row_mask:0xf bank_mask:0xf bound_ctrl:1
	global_store_dwordx2 v[52:53], v[48:49], off offset:1536
	v_lshl_add_u64 v[48:49], v[130:131], 0, s[8:9]
	s_addc_u32 s27, s37, s27
	v_readlane_b32 s3, v34, 16
	v_readlane_b32 s28, v34, 48
	global_load_dwordx4 v[112:115], v[48:49], off
	global_load_dwordx4 v[104:107], v[48:49], off offset:1024
	global_load_dwordx4 v[96:99], v[48:49], off offset:2048
	global_load_dwordx4 v[88:91], v[48:49], off offset:3072
	global_load_dwordx4 v[72:75], v122, s[26:27] offset:16
	global_load_dwordx4 v[80:83], v122, s[26:27]
	global_load_dwordx4 v[64:67], v122, s[26:27] offset:2064
	global_load_dwordx4 v[68:71], v122, s[26:27] offset:2048
	global_load_dwordx4 v[56:59], v149, s[26:27] offset:16
	global_load_dwordx4 v[60:63], v149, s[26:27]
	global_load_dwordx4 v[48:51], v150, s[26:27] offset:16
	global_load_dwordx4 v[52:55], v150, s[26:27]
	v_readlane_b32 s26, v34, 0
	v_readlane_b32 s27, v34, 32
	v_mov_b32_e32 v34, s3
	v_mov_b32_e32 v35, s28
	v_pk_add_f32 v[34:35], s[26:27], v[34:35]
	ds_read_b128 v[76:79], v144
	ds_read_b128 v[84:87], v144 offset:16
	v_add_f32_e32 v34, v34, v35
	v_fmamk_f32 v34, v34, 0x3a000000, v151
	v_cmp_gt_f32_e32 vcc, s11, v34
	v_mul_f32_e32 v35, 0x4b800000, v34
	v_readlane_b32 s38, v253, 12
	v_cndmask_b32_e32 v34, v34, v35, vcc
	v_rsq_f32_e32 v34, v34
	v_readlane_b32 s39, v253, 13
	v_readlane_b32 s40, v253, 14
	v_readlane_b32 s41, v253, 15
	v_mul_f32_e32 v35, 0x45800000, v34
	v_cndmask_b32_e32 v34, v34, v35, vcc
	v_mul_f32_e32 v35, v34, v92
	ds_read_b128 v[92:95], v144 offset:8192
	v_mul_f32_e32 v45, v34, v45
	v_readlane_b32 s42, v253, 16
	v_readlane_b32 s43, v253, 17
	v_readlane_b32 s44, v253, 18
	s_waitcnt lgkmcnt(0)
	v_mul_f32_e32 v35, v92, v35
	s_waitcnt vmcnt(26)
	v_fma_f32 v28, v76, v35, v28
	v_mul_f32_e32 v35, v34, v100
	v_mul_f32_e32 v76, v34, v101
	v_mul_f32_e32 v35, v93, v35
	v_mul_f32_e32 v76, v94, v76
	v_mul_f32_e32 v45, v95, v45
	v_fma_f32 v29, v77, v35, v29
	v_fma_f32 v30, v78, v76, v30
	v_fmac_f32_e32 v31, v79, v45
	ds_read_b128 v[76:79], v144 offset:8208
	v_mul_f32_e32 v45, v34, v102
	v_mul_f32_e32 v35, v29, v29
	v_fmac_f32_e32 v35, v28, v28
	v_fmac_f32_e32 v35, v30, v30
	s_waitcnt lgkmcnt(0)
	v_mul_f32_e32 v45, v45, v76
	v_fma_f32 v45, v84, v45, v24
	v_mul_f32_e32 v24, v34, v46
	v_mul_f32_e32 v24, v24, v77
	v_fma_f32 v46, v85, v24, v25
	v_mul_f32_e32 v24, v34, v103
	v_fmac_f32_e32 v35, v31, v31
	v_mul_f32_e32 v24, v24, v78
	v_fmac_f32_e32 v35, v45, v45
	v_fma_f32 v76, v86, v24, v26
	v_mul_f32_e32 v24, v34, v47
	v_fmac_f32_e32 v35, v46, v46
	v_mul_f32_e32 v24, v24, v79
	v_fmac_f32_e32 v35, v76, v76
	v_fmac_f32_e32 v27, v87, v24
	v_cvt_pk_bf16_f32 v24, v28, v29
	v_lshl_add_u64 v[28:29], v[132:133], 0, s[22:23]
	v_fmac_f32_e32 v35, v27, v27
	v_cvt_pk_bf16_f32 v25, v30, v31
	v_cvt_pk_bf16_f32 v26, v45, v46
	v_cvt_pk_bf16_f32 v27, v76, v27
	global_store_dwordx4 v[28:29], v[24:27], off
	ds_read_b128 v[76:79], v144 offset:2048
	ds_read_b128 v[84:87], v144 offset:2064
	ds_read_b128 v[92:95], v144 offset:10240
	v_mul_f32_e32 v30, v34, v108
	v_readlane_b32 s45, v253, 19
	v_readlane_b32 s46, v253, 20
	v_readlane_b32 s47, v253, 21
	s_waitcnt lgkmcnt(0)
	v_mul_f32_e32 v30, v30, v92
	s_waitcnt vmcnt(25)
	v_fma_f32 v20, v76, v30, v20
	v_mul_f32_e32 v30, v34, v109
	v_mul_f32_e32 v30, v30, v93
	v_fma_f32 v21, v77, v30, v21
	v_mul_f32_e32 v30, v34, v110
	v_mul_f32_e32 v30, v30, v94
	v_fma_f32 v22, v78, v30, v22
	v_mul_f32_e32 v30, v34, v111
	v_mul_f32_e32 v30, v30, v95
	v_fmac_f32_e32 v23, v79, v30
	ds_read_b128 v[76:79], v144 offset:10256
	v_mul_f32_e32 v30, v34, v116
	v_fmac_f32_e32 v35, v20, v20
	v_fmac_f32_e32 v35, v21, v21
	v_fmac_f32_e32 v35, v22, v22
	s_waitcnt lgkmcnt(0)
	v_mul_f32_e32 v30, v30, v76
	v_fma_f32 v30, v84, v30, v16
	v_mul_f32_e32 v16, v34, v117
	v_mul_f32_e32 v16, v16, v77
	v_fma_f32 v31, v85, v16, v17
	v_mul_f32_e32 v16, v34, v118
	v_fmac_f32_e32 v35, v23, v23
	v_mul_f32_e32 v16, v16, v78
	v_fmac_f32_e32 v35, v30, v30
	v_fma_f32 v45, v86, v16, v18
	v_mul_f32_e32 v16, v34, v119
	v_fmac_f32_e32 v35, v31, v31
	v_mul_f32_e32 v16, v16, v79
	v_fmac_f32_e32 v35, v45, v45
	v_fmac_f32_e32 v19, v87, v16
	v_fmac_f32_e32 v35, v19, v19
	v_cvt_pk_bf16_f32 v16, v20, v21
	v_cvt_pk_bf16_f32 v17, v22, v23
	v_cvt_pk_bf16_f32 v18, v30, v31
	v_cvt_pk_bf16_f32 v19, v45, v19
	global_store_dwordx4 v[28:29], v[16:19], off offset:1024
	ds_read_b128 v[20:23], v144 offset:4096
	ds_read_b128 v[76:79], v144 offset:4112
	ds_read_b128 v[84:87], v144 offset:12288
	v_mul_f32_e32 v30, v34, v129
	v_readlane_b32 s48, v253, 22
	v_readlane_b32 s49, v253, 23
	v_readlane_b32 s50, v253, 24
	s_waitcnt lgkmcnt(0)
	v_mul_f32_e32 v30, v30, v84
	s_waitcnt vmcnt(24)
	v_fma_f32 v12, v20, v30, v12
	v_mul_f32_e32 v20, v34, v157
	v_mul_f32_e32 v20, v20, v85
	v_fma_f32 v13, v21, v20, v13
	v_mul_f32_e32 v20, v34, v158
	v_mul_f32_e32 v20, v20, v86
	v_fma_f32 v14, v22, v20, v14
	v_mul_f32_e32 v20, v34, v159
	v_mul_f32_e32 v20, v20, v87
	v_fmac_f32_e32 v15, v23, v20
	ds_read_b128 v[20:23], v144 offset:12304
	v_mul_f32_e32 v30, v34, v160
	v_fmac_f32_e32 v35, v12, v12
	v_fmac_f32_e32 v35, v13, v13
	v_fmac_f32_e32 v35, v14, v14
	s_waitcnt lgkmcnt(0)
	v_mul_f32_e32 v20, v30, v20
	v_fma_f32 v20, v76, v20, v8
	v_mul_f32_e32 v8, v34, v44
	v_mul_f32_e32 v8, v8, v21
	v_fma_f32 v21, v77, v8, v9
	v_mul_f32_e32 v8, v34, v42
	v_fmac_f32_e32 v35, v15, v15
	v_mul_f32_e32 v8, v8, v22
	v_fmac_f32_e32 v35, v20, v20
	v_fma_f32 v22, v78, v8, v10
	v_mul_f32_e32 v8, v34, v41
	v_fmac_f32_e32 v35, v21, v21
	v_mul_f32_e32 v8, v8, v23
	v_fmac_f32_e32 v35, v22, v22
	v_fmac_f32_e32 v11, v79, v8
	v_fmac_f32_e32 v35, v11, v11
	v_cvt_pk_bf16_f32 v8, v12, v13
	v_cvt_pk_bf16_f32 v9, v14, v15
	v_cvt_pk_bf16_f32 v10, v20, v21
	v_cvt_pk_bf16_f32 v11, v22, v11
	global_store_dwordx4 v[28:29], v[8:11], off offset:2048
	ds_read_b128 v[12:15], v144 offset:6144
	ds_read_b128 v[20:23], v144 offset:6160
	v_mul_f32_e32 v30, v34, v43
	ds_read_b128 v[42:45], v144 offset:14336
	v_readlane_b32 s51, v253, 25
	s_waitcnt lgkmcnt(0)
	v_mul_f32_e32 v30, v30, v42
	s_waitcnt vmcnt(23)
	v_fma_f32 v30, v12, v30, v4
	v_mul_f32_e32 v4, v34, v40
	v_mul_f32_e32 v4, v4, v43
	v_fmac_f32_e32 v35, v30, v30
	v_fma_f32 v31, v13, v4, v5
	v_fmac_f32_e32 v35, v31, v31
	v_pk_mul_f32 v[4:5], v[34:35], v[36:37] op_sel_hi:[0,1]
	v_pk_mul_f32 v[4:5], v[4:5], v[44:45] op_sel:[1,0] op_sel_hi:[0,1]
	v_pk_fma_f32 v[12:13], v[14:15], v[4:5], v[6:7]
	s_nop 0
	v_pk_mul_f32 v[4:5], v[12:13], v[12:13]
	s_nop 0
	v_add_f32_e32 v4, v35, v4
	v_add_f32_e32 v35, v4, v5
	ds_read_b128 v[4:7], v144 offset:14352
	v_pk_mul_f32 v[14:15], v[34:35], v[38:39] op_sel_hi:[0,1]
	s_waitcnt lgkmcnt(0)
	v_pk_mul_f32 v[4:5], v[14:15], v[4:5] op_sel:[1,0] op_sel_hi:[0,1]
	v_pk_fma_f32 v[4:5], v[20:21], v[4:5], v[0:1]
	s_nop 0
	v_pk_mul_f32 v[0:1], v[4:5], v[4:5]
	s_nop 0
	v_add_f32_e32 v0, v35, v0
	v_add_f32_e32 v14, v0, v1
	v_pk_mul_f32 v[0:1], v[34:35], v[32:33] op_sel_hi:[0,1]
	v_pk_mul_f32 v[0:1], v[0:1], v[6:7] op_sel:[1,0] op_sel_hi:[0,1]
	v_pk_fma_f32 v[6:7], v[22:23], v[0:1], v[2:3]
	s_nop 0
	v_pk_mul_f32 v[0:1], v[6:7], v[6:7]
	s_nop 0
	v_add_f32_e32 v0, v14, v0
	v_add_f32_e32 v14, v0, v1
	v_cvt_pk_bf16_f32 v0, v30, v31
	v_cvt_pk_bf16_f32 v1, v12, v13
	v_cvt_pk_bf16_f32 v2, v4, v5
	v_cvt_pk_bf16_f32 v3, v6, v7
	global_store_dwordx4 v[28:29], v[0:3], off offset:3072
	s_nop 0
	v_add_f32_dpp v4, v14, v14 quad_perm:[1,0,3,2] row_mask:0xf bank_mask:0xf bound_ctrl:1
	s_nop 1
	v_add_f32_dpp v4, v4, v4 quad_perm:[2,3,0,1] row_mask:0xf bank_mask:0xf bound_ctrl:1
	s_nop 1
	v_add_f32_dpp v4, v4, v4 row_ror:4 row_mask:0xf bank_mask:0xf bound_ctrl:1
	s_nop 1
	v_add_f32_dpp v4, v4, v4 row_ror:8 row_mask:0xf bank_mask:0xf bound_ctrl:1
	s_nop 0
	v_readlane_b32 s3, v4, 16
	v_readlane_b32 s26, v4, 48
	v_readlane_b32 s22, v4, 0
	v_readlane_b32 s23, v4, 32
	v_mov_b32_e32 v4, s3
	v_mov_b32_e32 v5, s26
	v_pk_add_f32 v[4:5], s[22:23], v[4:5]
	s_nop 0
	v_add_f32_e32 v4, v4, v5
	v_fmamk_f32 v4, v4, 0x3a000000, v151
	v_cmp_gt_f32_e32 vcc, s11, v4
	v_mul_f32_e32 v5, 0x4b800000, v4
	s_nop 0
	v_cndmask_b32_e32 v4, v4, v5, vcc
	v_rsq_f32_e32 v4, v4
	s_nop 0
	v_mul_f32_e32 v5, 0x45800000, v4
	v_cndmask_b32_e32 v6, v4, v5, vcc
	s_and_saveexec_b64 s[22:23], s[6:7]
	v_mov_b32_e32 v4, s10
	ds_write_b32 v4, v6 offset:60676
	s_or_b64 exec, exec, s[22:23]
	v_lshlrev_b32_e32 v4, 16, v24
	v_and_b32_e32 v5, 0xffff0000, v24
	v_lshlrev_b32_e32 v7, 16, v25
	v_and_b32_e32 v28, 0xffff0000, v25
	v_lshlrev_b32_e32 v29, 16, v26
	v_and_b32_e32 v30, 0xffff0000, v26
	v_lshlrev_b32_e32 v31, 16, v27
	v_and_b32_e32 v32, 0xffff0000, v27
	ds_read_b128 v[12:15], v144 offset:16384
	ds_read_b128 v[20:23], v144 offset:16400
	ds_read_b128 v[24:27], v144 offset:32768
	v_mul_f32_e32 v4, v6, v4
	v_mul_f32_e32 v5, v6, v5
	v_mul_f32_e32 v7, v6, v7
	s_lshl_b64 s[20:21], s[20:21], 11
	s_waitcnt lgkmcnt(0)
	v_fma_f32 v4, v4, v12, v24
	v_mul_f32_e32 v12, v6, v28
	v_fma_f32 v5, v5, v13, v25
	v_fma_f32 v7, v7, v14, v26
	v_fmac_f32_e32 v27, v12, v15
	ds_read_b128 v[12:15], v144 offset:32784
	v_mul_f32_e32 v24, v6, v29
	v_med3_f32 v4, v4, s12, v154
	v_med3_f32 v5, v5, s12, v154
	v_med3_f32 v7, v7, s12, v154
	s_waitcnt lgkmcnt(0)
	v_fma_f32 v20, v24, v20, v12
	v_mul_f32_e32 v12, v6, v30
	v_fma_f32 v13, v12, v21, v13
	v_mul_f32_e32 v12, v6, v31
	v_fma_f32 v14, v12, v22, v14
	v_mul_f32_e32 v12, v6, v32
	v_fmac_f32_e32 v15, v12, v23
	v_mov_b32_e32 v12, 0
	v_cvt_pk_fp8_f32 v12, v4, v5
	v_med3_f32 v4, v20, s12, v154
	v_med3_f32 v5, v13, s12, v154
	v_mov_b32_e32 v13, 0
	v_cvt_pk_fp8_f32 v13, v4, v5
	v_med3_f32 v21, v27, s12, v154
	v_cvt_pk_fp8_f32 v12, v7, v21 op_sel:[0,0,1]
	v_med3_f32 v7, v14, s12, v154
	v_med3_f32 v14, v15, s12, v154
	v_cvt_pk_fp8_f32 v13, v7, v14 op_sel:[0,0,1]
	v_lshl_add_u64 v[4:5], v[134:135], 0, s[20:21]
	v_lshlrev_b32_e32 v7, 16, v16
	v_and_b32_e32 v20, 0xffff0000, v16
	global_store_dwordx2 v[4:5], v[12:13], off
	v_lshlrev_b32_e32 v21, 16, v17
	v_and_b32_e32 v22, 0xffff0000, v17
	v_lshlrev_b32_e32 v23, 16, v18
	v_and_b32_e32 v24, 0xffff0000, v18
	v_lshlrev_b32_e32 v25, 16, v19
	v_and_b32_e32 v26, 0xffff0000, v19
	ds_read_b128 v[12:15], v144 offset:18432
	ds_read_b128 v[16:19], v144 offset:34816
	v_mul_f32_e32 v7, v6, v7
	s_waitcnt vmcnt(16)
	v_and_b32_e32 v44, 0xffff0000, v112
	v_lshlrev_b32_e32 v45, 16, v113
	v_lshlrev_b32_e32 v129, 16, v115
	s_waitcnt lgkmcnt(0)
	v_fma_f32 v7, v7, v12, v16
	v_mul_f32_e32 v12, v6, v20
	v_fma_f32 v16, v12, v13, v17
	v_mul_f32_e32 v12, v6, v21
	v_fma_f32 v17, v12, v14, v18
	v_mul_f32_e32 v12, v6, v22
	v_fmac_f32_e32 v19, v12, v15
	v_mul_f32_e32 v18, v6, v23
	ds_read_b128 v[12:15], v144 offset:18448
	ds_read_b128 v[20:23], v144 offset:34832
	v_med3_f32 v7, v7, s12, v154
	v_and_b32_e32 v115, 0xffff0000, v115
	s_waitcnt vmcnt(15)
	v_lshlrev_b32_e32 v157, 16, v104
	v_and_b32_e32 v104, 0xffff0000, v104
	s_waitcnt lgkmcnt(0)
	v_fma_f32 v18, v18, v12, v20
	v_mul_f32_e32 v12, v6, v24
	v_fma_f32 v13, v12, v13, v21
	v_mul_f32_e32 v12, v6, v25
	v_fma_f32 v14, v12, v14, v22
	v_mul_f32_e32 v12, v6, v26
	v_fmac_f32_e32 v23, v12, v15
	v_med3_f32 v15, v16, s12, v154
	v_mov_b32_e32 v12, 0
	v_cvt_pk_fp8_f32 v12, v7, v15
	v_med3_f32 v7, v18, s12, v154
	v_med3_f32 v15, v13, s12, v154
	v_mov_b32_e32 v13, 0
	v_cvt_pk_fp8_f32 v13, v7, v15
	v_med3_f32 v16, v17, s12, v154
	v_med3_f32 v17, v19, s12, v154
	v_cvt_pk_fp8_f32 v12, v16, v17 op_sel:[0,0,1]
	v_med3_f32 v14, v14, s12, v154
	v_med3_f32 v16, v23, s12, v154
	v_cvt_pk_fp8_f32 v13, v14, v16 op_sel:[0,0,1]
	v_lshlrev_b32_e32 v7, 16, v8
	v_and_b32_e32 v16, 0xffff0000, v8
	v_lshlrev_b32_e32 v17, 16, v9
	global_store_dwordx2 v[4:5], v[12:13], off offset:512
	v_and_b32_e32 v18, 0xffff0000, v9
	v_lshlrev_b32_e32 v19, 16, v10
	v_and_b32_e32 v20, 0xffff0000, v10
	v_lshlrev_b32_e32 v21, 16, v11
	v_and_b32_e32 v22, 0xffff0000, v11
	ds_read_b128 v[8:11], v144 offset:20480
	ds_read_b128 v[12:15], v144 offset:36864
	v_mul_f32_e32 v7, v6, v7
	v_lshlrev_b32_e32 v23, 16, v112
	v_and_b32_e32 v112, 0xffff0000, v113
	v_lshlrev_b32_e32 v113, 16, v114
	s_waitcnt lgkmcnt(0)
	v_fma_f32 v7, v7, v8, v12
	v_mul_f32_e32 v8, v6, v16
	v_fma_f32 v12, v8, v9, v13
	v_mul_f32_e32 v8, v6, v17
	v_fma_f32 v13, v8, v10, v14
	v_mul_f32_e32 v8, v6, v18
	v_fmac_f32_e32 v15, v8, v11
	v_mul_f32_e32 v14, v6, v19
	ds_read_b128 v[8:11], v144 offset:20496
	ds_read_b128 v[16:19], v144 offset:36880
	v_med3_f32 v7, v7, s12, v154
	v_and_b32_e32 v114, 0xffff0000, v114
	v_lshlrev_b32_e32 v158, 16, v105
	v_and_b32_e32 v105, 0xffff0000, v105
	s_waitcnt lgkmcnt(0)
	v_fma_f32 v14, v14, v8, v16
	v_mul_f32_e32 v8, v6, v20
	v_fma_f32 v9, v8, v9, v17
	v_mul_f32_e32 v8, v6, v21
	v_fma_f32 v10, v8, v10, v18
	v_mul_f32_e32 v8, v6, v22
	v_fmac_f32_e32 v19, v8, v11
	v_med3_f32 v11, v12, s12, v154
	v_mov_b32_e32 v8, 0
	v_cvt_pk_fp8_f32 v8, v7, v11
	v_med3_f32 v7, v14, s12, v154
	v_med3_f32 v11, v9, s12, v154
	v_mov_b32_e32 v9, 0
	v_cvt_pk_fp8_f32 v9, v7, v11
	v_med3_f32 v12, v13, s12, v154
	v_med3_f32 v13, v15, s12, v154
	v_cvt_pk_fp8_f32 v8, v12, v13 op_sel:[0,0,1]
	v_med3_f32 v10, v10, s12, v154
	v_med3_f32 v12, v19, s12, v154
	v_cvt_pk_fp8_f32 v9, v10, v12 op_sel:[0,0,1]
	v_lshlrev_b32_e32 v7, 16, v0
	v_and_b32_e32 v12, 0xffff0000, v0
	v_lshlrev_b32_e32 v13, 16, v1
	global_store_dwordx2 v[4:5], v[8:9], off offset:1024
	v_and_b32_e32 v14, 0xffff0000, v1
	v_lshlrev_b32_e32 v15, 16, v2
	v_and_b32_e32 v16, 0xffff0000, v2
	v_lshlrev_b32_e32 v17, 16, v3
	v_and_b32_e32 v18, 0xffff0000, v3
	ds_read_b128 v[0:3], v144 offset:22528
	ds_read_b128 v[8:11], v144 offset:38912
	v_mul_f32_e32 v7, v6, v7
	v_lshlrev_b32_e32 v159, 16, v106
	v_and_b32_e32 v106, 0xffff0000, v106
	v_lshlrev_b32_e32 v160, 16, v107
	s_waitcnt lgkmcnt(0)
	v_fma_f32 v7, v7, v0, v8
	v_mul_f32_e32 v0, v6, v12
	v_fma_f32 v8, v0, v1, v9
	v_mul_f32_e32 v0, v6, v13
	v_fma_f32 v9, v0, v2, v10
	v_mul_f32_e32 v0, v6, v14
	v_fmac_f32_e32 v11, v0, v3
	v_mul_f32_e32 v10, v6, v15
	ds_read_b128 v[0:3], v144 offset:22544
	ds_read_b128 v[12:15], v144 offset:38928
	v_and_b32_e32 v107, 0xffff0000, v107
	s_waitcnt vmcnt(16)
	v_lshlrev_b32_e32 v161, 16, v96
	v_and_b32_e32 v96, 0xffff0000, v96
	v_lshlrev_b32_e32 v162, 16, v97
	s_waitcnt lgkmcnt(0)
	v_fma_f32 v10, v10, v0, v12
	v_mul_f32_e32 v0, v6, v16
	v_fma_f32 v1, v0, v1, v13
	v_mul_f32_e32 v0, v6, v17
	v_fma_f32 v2, v0, v2, v14
	v_mul_f32_e32 v0, v6, v18
	v_fmac_f32_e32 v15, v0, v3
	v_med3_f32 v3, v7, s12, v154
	v_med3_f32 v6, v8, s12, v154
	v_mov_b32_e32 v0, 0
	v_cvt_pk_fp8_f32 v0, v3, v6
	v_med3_f32 v3, v10, s12, v154
	v_med3_f32 v6, v1, s12, v154
	v_mov_b32_e32 v1, 0
	v_cvt_pk_fp8_f32 v1, v3, v6
	v_mul_f32_e32 v6, v44, v44
	v_fmac_f32_e32 v6, v23, v23
	v_fmac_f32_e32 v6, v45, v45
	v_fmac_f32_e32 v6, v112, v112
	v_fmac_f32_e32 v6, v113, v113
	v_fmac_f32_e32 v6, v114, v114
	v_fmac_f32_e32 v6, v129, v129
	v_fmac_f32_e32 v6, v115, v115
	v_fmac_f32_e32 v6, v157, v157
	v_fmac_f32_e32 v6, v104, v104
	v_fmac_f32_e32 v6, v158, v158
	v_fmac_f32_e32 v6, v105, v105
	v_fmac_f32_e32 v6, v159, v159
	v_fmac_f32_e32 v6, v106, v106
	v_fmac_f32_e32 v6, v160, v160
	v_fmac_f32_e32 v6, v107, v107
	v_fmac_f32_e32 v6, v161, v161
	v_fmac_f32_e32 v6, v96, v96
	v_and_b32_e32 v97, 0xffff0000, v97
	v_fmac_f32_e32 v6, v162, v162
	v_med3_f32 v7, v9, s12, v154
	v_med3_f32 v8, v11, s12, v154
	v_lshlrev_b32_e32 v163, 16, v98
	v_fmac_f32_e32 v6, v97, v97
	v_cvt_pk_fp8_f32 v0, v7, v8 op_sel:[0,0,1]
	v_med3_f32 v2, v2, s12, v154
	v_med3_f32 v7, v15, s12, v154
	v_and_b32_e32 v22, 0xffff0000, v98
	v_fmac_f32_e32 v6, v163, v163
	v_cvt_pk_fp8_f32 v1, v2, v7 op_sel:[0,0,1]
	v_lshlrev_b32_e32 v21, 16, v99
	v_fmac_f32_e32 v6, v22, v22
	v_and_b32_e32 v20, 0xffff0000, v99
	v_fmac_f32_e32 v6, v21, v21
	v_fmac_f32_e32 v6, v20, v20
	s_waitcnt vmcnt(15)
	v_lshlrev_b32_e32 v46, 16, v88
	v_and_b32_e32 v31, 0xffff0000, v88
	v_fmac_f32_e32 v6, v46, v46
	v_and_b32_e32 v36, 0xffff0000, v89
	v_lshlrev_b32_e32 v37, 16, v89
	global_store_dwordx2 v[4:5], v[0:1], off offset:1536
	v_fmac_f32_e32 v6, v31, v31
	v_pk_mul_f32 v[4:5], v[36:37], v[36:37]
	v_and_b32_e32 v38, 0xffff0000, v90
	v_add_f32_e32 v5, v5, v6
	v_lshlrev_b32_e32 v39, 16, v90
	v_add_f32_e32 v6, v4, v5
	v_pk_mul_f32 v[4:5], v[38:39], v[38:39]
	v_and_b32_e32 v28, 0xffff0000, v91
	v_add_f32_e32 v5, v5, v6
	v_lshlrev_b32_e32 v29, 16, v91
	v_add_f32_e32 v6, v4, v5
	v_pk_mul_f32 v[4:5], v[28:29], v[28:29]
	s_or_b32 s20, s0, 3
	v_add_f32_e32 v5, v5, v6
	v_add_f32_e32 v4, v4, v5
	s_mov_b32 s21, s1
	s_lshl_b64 s[26:27], s[20:21], 12
	v_add_f32_dpp v4, v4, v4 quad_perm:[1,0,3,2] row_mask:0xf bank_mask:0xf bound_ctrl:1
	s_lshl_b64 s[22:23], s[20:21], 13
	v_readlane_b32 s36, v253, 10
	v_add_f32_dpp v4, v4, v4 quad_perm:[2,3,0,1] row_mask:0xf bank_mask:0xf bound_ctrl:1
	v_readlane_b32 s37, v253, 11
	s_add_u32 s22, s36, s22
	v_add_f32_dpp v4, v4, v4 row_ror:4 row_mask:0xf bank_mask:0xf bound_ctrl:1
	v_lshl_add_u64 v[0:1], v[130:131], 0, s[26:27]
	s_addc_u32 s23, s37, s23
	v_add_f32_dpp v4, v4, v4 row_ror:8 row_mask:0xf bank_mask:0xf bound_ctrl:1
	global_load_dwordx4 v[116:119], v[0:1], off
	global_load_dwordx4 v[108:111], v[0:1], off offset:1024
	global_load_dwordx4 v[100:103], v[0:1], off offset:2048
	global_load_dwordx4 v[92:95], v[0:1], off offset:3072
	v_readlane_b32 s3, v4, 16
	v_readlane_b32 s28, v4, 48
	global_load_dwordx4 v[76:79], v122, s[22:23] offset:16
	global_load_dwordx4 v[84:87], v122, s[22:23]
	global_load_dwordx4 v[32:35], v122, s[22:23] offset:2064
	global_load_dwordx4 v[40:43], v122, s[22:23] offset:2048
	global_load_dwordx4 v[16:19], v149, s[22:23] offset:16
	global_load_dwordx4 v[24:27], v149, s[22:23]
	global_load_dwordx4 v[0:3], v150, s[22:23] offset:16
	global_load_dwordx4 v[8:11], v150, s[22:23]
	v_readlane_b32 s22, v4, 0
	v_readlane_b32 s23, v4, 32
	v_mov_b32_e32 v4, s3
	v_mov_b32_e32 v5, s28
	v_pk_add_f32 v[4:5], s[22:23], v[4:5]
	v_readlane_b32 s38, v253, 12
	v_add_f32_e32 v4, v4, v5
	v_fmamk_f32 v4, v4, 0x3a000000, v151
	v_cmp_gt_f32_e32 vcc, s11, v4
	v_mul_f32_e32 v5, 0x4b800000, v4
	v_readlane_b32 s39, v253, 13
	v_cndmask_b32_e32 v4, v4, v5, vcc
	v_rsq_f32_e32 v4, v4
	v_readlane_b32 s40, v253, 14
	v_readlane_b32 s41, v253, 15
	v_readlane_b32 s42, v253, 16
	v_mul_f32_e32 v5, 0x45800000, v4
	v_cndmask_b32_e32 v30, v4, v5, vcc
	ds_read_b128 v[4:7], v144
	ds_read_b128 v[12:15], v144 offset:16
	ds_read_b128 v[88:91], v144 offset:8192
	v_mul_f32_e32 v23, v30, v23
	v_mul_f32_e32 v22, v30, v22
	v_mul_f32_e32 v21, v30, v21
	v_mul_f32_e32 v20, v30, v20
	s_waitcnt lgkmcnt(0)
	v_mul_f32_e32 v23, v88, v23
	s_waitcnt vmcnt(26)
	v_fma_f32 v23, v4, v23, v80
	v_mul_f32_e32 v4, v30, v44
	v_mul_f32_e32 v4, v89, v4
	v_fma_f32 v44, v5, v4, v81
	v_mul_f32_e32 v4, v30, v45
	v_mul_f32_e32 v4, v90, v4
	v_fma_f32 v45, v6, v4, v82
	v_mul_f32_e32 v4, v30, v112
	v_mul_f32_e32 v4, v91, v4
	v_fmac_f32_e32 v83, v7, v4
	ds_read_b128 v[4:7], v144 offset:8208
	v_mul_f32_e32 v80, v30, v113
	v_mul_f32_e32 v47, v44, v44
	v_fmac_f32_e32 v47, v23, v23
	v_fmac_f32_e32 v47, v45, v45
	s_waitcnt lgkmcnt(0)
	v_mul_f32_e32 v4, v80, v4
	v_fma_f32 v12, v12, v4, v72
	v_mul_f32_e32 v4, v30, v114
	v_mul_f32_e32 v4, v4, v5
	v_fma_f32 v13, v13, v4, v73
	v_mul_f32_e32 v4, v30, v129
	v_mul_f32_e32 v4, v4, v6
	v_fmac_f32_e32 v47, v83, v83
	v_fma_f32 v14, v14, v4, v74
	v_mul_f32_e32 v4, v30, v115
	v_fmac_f32_e32 v47, v12, v12
	v_mul_f32_e32 v4, v4, v7
	v_fmac_f32_e32 v47, v13, v13
	v_fmac_f32_e32 v75, v15, v4
	v_cvt_pk_bf16_f32 v4, v23, v44
	v_cvt_pk_bf16_f32 v5, v45, v83
	v_lshl_add_u64 v[44:45], v[132:133], 0, s[8:9]
	v_fmac_f32_e32 v47, v14, v14
	v_cvt_pk_bf16_f32 v6, v12, v13
	v_cvt_pk_bf16_f32 v7, v14, v75
	global_store_dwordx4 v[44:45], v[4:7], off
	v_fmac_f32_e32 v47, v75, v75
	ds_read_b128 v[12:15], v144 offset:2048
	ds_read_b128 v[72:75], v144 offset:2064
	ds_read_b128 v[80:83], v144 offset:10240
	v_mul_f32_e32 v23, v30, v157
	v_mul_f32_e32 v31, v30, v31
	v_mul_f32_e32 v46, v30, v46
	v_readlane_b32 s43, v253, 17
	s_waitcnt lgkmcnt(0)
	v_mul_f32_e32 v23, v23, v80
	s_waitcnt vmcnt(25)
	v_fma_f32 v23, v12, v23, v68
	v_mul_f32_e32 v12, v30, v104
	v_mul_f32_e32 v12, v12, v81
	v_fma_f32 v68, v13, v12, v69
	v_mul_f32_e32 v12, v30, v158
	v_mul_f32_e32 v12, v12, v82
	v_fma_f32 v69, v14, v12, v70
	v_mul_f32_e32 v12, v30, v105
	v_mul_f32_e32 v12, v12, v83
	v_fmac_f32_e32 v71, v15, v12
	ds_read_b128 v[12:15], v144 offset:10256
	v_mul_f32_e32 v70, v30, v159
	v_fmac_f32_e32 v47, v23, v23
	v_fmac_f32_e32 v47, v68, v68
	v_fmac_f32_e32 v47, v69, v69
	s_waitcnt lgkmcnt(0)
	v_mul_f32_e32 v12, v70, v12
	v_fma_f32 v64, v72, v12, v64
	v_mul_f32_e32 v12, v30, v106
	v_mul_f32_e32 v12, v12, v13
	v_fma_f32 v65, v73, v12, v65
	v_mul_f32_e32 v12, v30, v160
	v_fmac_f32_e32 v47, v71, v71
	v_mul_f32_e32 v12, v12, v14
	v_fmac_f32_e32 v47, v64, v64
	v_fma_f32 v66, v74, v12, v66
	v_mul_f32_e32 v12, v30, v107
	v_fmac_f32_e32 v47, v65, v65
	v_mul_f32_e32 v12, v12, v15
	v_fmac_f32_e32 v47, v66, v66
	v_fmac_f32_e32 v67, v75, v12
	v_cvt_pk_bf16_f32 v12, v23, v68
	v_cvt_pk_bf16_f32 v13, v69, v71
	v_cvt_pk_bf16_f32 v14, v64, v65
	v_cvt_pk_bf16_f32 v15, v66, v67
	global_store_dwordx4 v[44:45], v[12:15], off offset:1024
	v_fmac_f32_e32 v47, v67, v67
	ds_read_b128 v[64:67], v144 offset:4096
	ds_read_b128 v[68:71], v144 offset:4112
	ds_read_b128 v[72:75], v144 offset:12288
	v_mul_f32_e32 v23, v30, v161
	v_readlane_b32 s44, v253, 18
	v_readlane_b32 s45, v253, 19
	v_readlane_b32 s46, v253, 20
	s_waitcnt lgkmcnt(0)
	v_mul_f32_e32 v23, v23, v72
	s_waitcnt vmcnt(24)
	v_fma_f32 v23, v64, v23, v60
	v_mul_f32_e32 v60, v30, v96
	v_mul_f32_e32 v60, v60, v73
	v_fma_f32 v60, v65, v60, v61
	v_mul_f32_e32 v61, v30, v162
	v_mul_f32_e32 v61, v61, v74
	v_fma_f32 v61, v66, v61, v62
	v_mul_f32_e32 v62, v30, v97
	v_mul_f32_e32 v62, v62, v75
	v_fmac_f32_e32 v63, v67, v62
	ds_read_b128 v[64:67], v144 offset:12304
	v_fmac_f32_e32 v47, v23, v23
	v_fmac_f32_e32 v47, v60, v60
	v_mul_f32_e32 v62, v30, v163
	v_fmac_f32_e32 v47, v61, v61
	s_waitcnt lgkmcnt(0)
	v_mul_f32_e32 v62, v62, v64
	v_fmac_f32_e32 v47, v63, v63
	v_fma_f32 v56, v68, v62, v56
	v_mul_f32_e32 v22, v22, v65
	v_fmac_f32_e32 v47, v56, v56
	v_fma_f32 v22, v69, v22, v57
	v_mul_f32_e32 v21, v21, v66
	v_fmac_f32_e32 v47, v22, v22
	v_fma_f32 v57, v70, v21, v58
	v_mul_f32_e32 v20, v20, v67
	v_fmac_f32_e32 v47, v57, v57
	v_fmac_f32_e32 v59, v71, v20
	v_cvt_pk_bf16_f32 v20, v23, v60
	v_cvt_pk_bf16_f32 v21, v61, v63
	v_cvt_pk_bf16_f32 v22, v56, v22
	v_cvt_pk_bf16_f32 v23, v57, v59
	global_store_dwordx4 v[44:45], v[20:23], off offset:2048
	v_fmac_f32_e32 v47, v59, v59
	ds_read_b128 v[56:59], v144 offset:6144
	ds_read_b128 v[60:63], v144 offset:6160
	ds_read_b128 v[64:67], v144 offset:14336
	v_readlane_b32 s47, v253, 21
	v_readlane_b32 s48, v253, 22
	v_readlane_b32 s49, v253, 23
	v_readlane_b32 s50, v253, 24
	s_waitcnt lgkmcnt(0)
	v_mul_f32_e32 v31, v31, v65
	s_waitcnt vmcnt(23)
	v_fma_f32 v31, v57, v31, v53
	v_mul_f32_e32 v46, v46, v64
	v_pk_mul_f32 v[36:37], v[30:31], v[36:37] op_sel_hi:[0,1]
	v_fma_f32 v56, v56, v46, v52
	v_pk_mul_f32 v[36:37], v[36:37], v[66:67] op_sel:[1,0] op_sel_hi:[0,1]
	v_fmac_f32_e32 v47, v56, v56
	v_pk_fma_f32 v[52:53], v[58:59], v[36:37], v[54:55]
	v_fmac_f32_e32 v47, v31, v31
	v_pk_mul_f32 v[36:37], v[52:53], v[52:53]
	v_pk_mul_f32 v[28:29], v[30:31], v[28:29] op_sel_hi:[0,1]
	v_add_f32_e32 v36, v47, v36
	v_add_f32_e32 v54, v36, v37
	v_pk_mul_f32 v[46:47], v[30:31], v[38:39] op_sel_hi:[0,1]
	ds_read_b128 v[36:39], v144 offset:14352
	v_readlane_b32 s51, v253, 25
	s_waitcnt lgkmcnt(0)
	v_pk_mul_f32 v[36:37], v[46:47], v[36:37] op_sel:[1,0] op_sel_hi:[0,1]
	v_pk_fma_f32 v[36:37], v[60:61], v[36:37], v[48:49]
	v_pk_mul_f32 v[28:29], v[28:29], v[38:39] op_sel:[1,0] op_sel_hi:[0,1]
	v_pk_mul_f32 v[46:47], v[36:37], v[36:37]
	v_pk_fma_f32 v[38:39], v[62:63], v[28:29], v[50:51]
	v_add_f32_e32 v46, v54, v46
	v_add_f32_e32 v46, v46, v47
	v_pk_mul_f32 v[28:29], v[38:39], v[38:39]
	s_nop 0
	v_add_f32_e32 v28, v46, v28
	v_add_f32_e32 v46, v28, v29
	v_cvt_pk_bf16_f32 v28, v56, v31
	v_cvt_pk_bf16_f32 v29, v52, v53
	v_cvt_pk_bf16_f32 v30, v36, v37
	v_cvt_pk_bf16_f32 v31, v38, v39
	global_store_dwordx4 v[44:45], v[28:31], off offset:3072
	s_nop 0
	v_add_f32_dpp v36, v46, v46 quad_perm:[1,0,3,2] row_mask:0xf bank_mask:0xf bound_ctrl:1
	s_nop 1
	v_add_f32_dpp v36, v36, v36 quad_perm:[2,3,0,1] row_mask:0xf bank_mask:0xf bound_ctrl:1
	s_nop 1
	v_add_f32_dpp v36, v36, v36 row_ror:4 row_mask:0xf bank_mask:0xf bound_ctrl:1
	s_nop 1
	v_add_f32_dpp v36, v36, v36 row_ror:8 row_mask:0xf bank_mask:0xf bound_ctrl:1
	s_nop 0
	v_readlane_b32 s3, v36, 16
	v_readlane_b32 s22, v36, 48
	v_readlane_b32 s8, v36, 0
	v_readlane_b32 s9, v36, 32
	v_mov_b32_e32 v36, s3
	v_mov_b32_e32 v37, s22
	v_pk_add_f32 v[36:37], s[8:9], v[36:37]
	s_nop 0
	v_add_f32_e32 v36, v36, v37
	v_fmamk_f32 v36, v36, 0x3a000000, v151
	v_cmp_gt_f32_e32 vcc, s11, v36
	v_mul_f32_e32 v37, 0x4b800000, v36
	s_nop 0
	v_cndmask_b32_e32 v36, v36, v37, vcc
	v_rsq_f32_e32 v36, v36
	s_nop 0
	v_mul_f32_e32 v37, 0x45800000, v36
	v_cndmask_b32_e32 v36, v36, v37, vcc
	s_and_saveexec_b64 s[8:9], s[6:7]
	v_mov_b32_e32 v37, s10
	ds_write_b32 v37, v36 offset:60680
	s_or_b64 exec, exec, s[8:9]
	v_lshlrev_b32_e32 v37, 16, v4
	v_and_b32_e32 v38, 0xffff0000, v4
	v_lshlrev_b32_e32 v39, 16, v5
	v_and_b32_e32 v52, 0xffff0000, v5
	v_lshlrev_b32_e32 v53, 16, v6
	v_and_b32_e32 v54, 0xffff0000, v6
	v_lshlrev_b32_e32 v55, 16, v7
	v_and_b32_e32 v56, 0xffff0000, v7
	ds_read_b128 v[4:7], v144 offset:16384
	ds_read_b128 v[44:47], v144 offset:16400
	ds_read_b128 v[48:51], v144 offset:32768
	v_mul_f32_e32 v37, v36, v37
	s_lshl_b64 s[8:9], s[24:25], 11
	s_waitcnt vmcnt(15)
	v_and_b32_e32 v105, 0xffff0000, v116
	v_lshlrev_b32_e32 v104, 16, v116
	s_waitcnt lgkmcnt(0)
	v_fma_f32 v37, v37, v4, v48
	v_mul_f32_e32 v4, v36, v38
	v_fma_f32 v38, v4, v5, v49
	v_mul_f32_e32 v4, v36, v39
	v_fma_f32 v39, v4, v6, v50
	v_mul_f32_e32 v4, v36, v52
	v_fmac_f32_e32 v51, v4, v7
	ds_read_b128 v[4:7], v144 offset:32784
	v_mul_f32_e32 v48, v36, v53
	v_med3_f32 v37, v37, s12, v154
	v_med3_f32 v38, v38, s12, v154
	v_med3_f32 v39, v39, s12, v154
	s_waitcnt lgkmcnt(0)
	v_fma_f32 v4, v48, v44, v4
	v_mul_f32_e32 v44, v36, v54
	v_fma_f32 v5, v44, v45, v5
	v_mul_f32_e32 v44, v36, v55
	v_fma_f32 v44, v44, v46, v6
	v_mul_f32_e32 v6, v36, v56
	v_fmac_f32_e32 v7, v6, v47
	v_mov_b32_e32 v6, 0
	v_cvt_pk_fp8_f32 v6, v37, v38
	v_med3_f32 v4, v4, s12, v154
	v_med3_f32 v5, v5, s12, v154
	v_med3_f32 v38, v7, s12, v154
	v_mov_b32_e32 v7, 0
	v_cvt_pk_fp8_f32 v7, v4, v5
	v_med3_f32 v45, v51, s12, v154
	v_med3_f32 v37, v44, s12, v154
	v_cvt_pk_fp8_f32 v6, v39, v45 op_sel:[0,0,1]
	v_cvt_pk_fp8_f32 v7, v37, v38 op_sel:[0,0,1]
	v_lshl_add_u64 v[4:5], v[134:135], 0, s[8:9]
	v_lshlrev_b32_e32 v37, 16, v13
	v_and_b32_e32 v38, 0xffff0000, v13
	global_store_dwordx2 v[4:5], v[6:7], off
	v_lshlrev_b32_e32 v6, 16, v12
	v_and_b32_e32 v7, 0xffff0000, v12
	v_lshlrev_b32_e32 v39, 16, v14
	v_and_b32_e32 v52, 0xffff0000, v14
	v_lshlrev_b32_e32 v53, 16, v15
	v_and_b32_e32 v54, 0xffff0000, v15
	ds_read_b128 v[12:15], v144 offset:18432
	ds_read_b128 v[44:47], v144 offset:34816
	v_mul_f32_e32 v6, v36, v6
	v_mul_f32_e32 v7, v36, v7
	v_lshlrev_b32_e32 v106, 16, v117
	v_and_b32_e32 v107, 0xffff0000, v117
	s_waitcnt lgkmcnt(0)
	v_fma_f32 v6, v6, v12, v44
	v_mul_f32_e32 v12, v36, v37
	v_fma_f32 v37, v12, v14, v46
	v_mul_f32_e32 v12, v36, v38
	v_fma_f32 v7, v7, v13, v45
	v_fmac_f32_e32 v47, v12, v15
	ds_read_b128 v[12:15], v144 offset:18448
	ds_read_b128 v[48:51], v144 offset:34832
	v_mul_f32_e32 v38, v36, v39
	v_med3_f32 v7, v7, s12, v154
	v_med3_f32 v37, v37, s12, v154
	v_lshlrev_b32_e32 v39, 16, v22
	s_waitcnt lgkmcnt(0)
	v_fma_f32 v12, v38, v12, v48
	v_mul_f32_e32 v38, v36, v52
	v_fma_f32 v13, v38, v13, v49
	v_mul_f32_e32 v38, v36, v53
	v_fma_f32 v14, v38, v14, v50
	v_mul_f32_e32 v38, v36, v54
	v_fmac_f32_e32 v51, v38, v15
	v_med3_f32 v15, v6, s12, v154
	v_mov_b32_e32 v6, 0
	v_cvt_pk_fp8_f32 v6, v15, v7
	v_med3_f32 v12, v12, s12, v154
	v_med3_f32 v13, v13, s12, v154
	v_mov_b32_e32 v7, 0
	v_cvt_pk_fp8_f32 v7, v12, v13
	v_med3_f32 v38, v47, s12, v154
	v_med3_f32 v14, v14, s12, v154
	v_med3_f32 v15, v51, s12, v154
	v_cvt_pk_fp8_f32 v6, v37, v38 op_sel:[0,0,1]
	v_cvt_pk_fp8_f32 v7, v14, v15 op_sel:[0,0,1]
	v_lshlrev_b32_e32 v37, 16, v21
	v_and_b32_e32 v38, 0xffff0000, v21
	v_and_b32_e32 v48, 0xffff0000, v22
	global_store_dwordx2 v[4:5], v[6:7], off offset:512
	v_lshlrev_b32_e32 v6, 16, v20
	v_and_b32_e32 v7, 0xffff0000, v20
	v_lshlrev_b32_e32 v49, 16, v23
	v_and_b32_e32 v50, 0xffff0000, v23
	ds_read_b128 v[12:15], v144 offset:20480
	ds_read_b128 v[20:23], v144 offset:36864
	v_mul_f32_e32 v6, v36, v6
	v_mul_f32_e32 v7, v36, v7
	v_mul_f32_e32 v54, v105, v105
	v_fmac_f32_e32 v54, v104, v104
	s_waitcnt lgkmcnt(0)
	v_fma_f32 v6, v6, v12, v20
	v_mul_f32_e32 v12, v36, v37
	v_fma_f32 v20, v12, v14, v22
	v_mul_f32_e32 v12, v36, v38
	v_fma_f32 v7, v7, v13, v21
	v_fmac_f32_e32 v23, v12, v15
	ds_read_b128 v[12:15], v144 offset:20496
	ds_read_b128 v[44:47], v144 offset:36880
	v_mul_f32_e32 v21, v36, v39
	v_med3_f32 v7, v7, s12, v154
	v_fmac_f32_e32 v54, v106, v106
	v_lshlrev_b32_e32 v112, 16, v118
	s_waitcnt lgkmcnt(0)
	v_fma_f32 v12, v21, v12, v44
	v_mul_f32_e32 v21, v36, v48
	v_fma_f32 v13, v21, v13, v45
	v_mul_f32_e32 v21, v36, v49
	v_fma_f32 v14, v21, v14, v46
	v_mul_f32_e32 v21, v36, v50
	v_fmac_f32_e32 v47, v21, v15
	v_med3_f32 v15, v6, s12, v154
	v_mov_b32_e32 v6, 0
	v_cvt_pk_fp8_f32 v6, v15, v7
	v_med3_f32 v12, v12, s12, v154
	v_med3_f32 v13, v13, s12, v154
	v_mov_b32_e32 v7, 0
	v_cvt_pk_fp8_f32 v7, v12, v13
	v_fmac_f32_e32 v54, v107, v107
	v_and_b32_e32 v113, 0xffff0000, v118
	v_fmac_f32_e32 v54, v112, v112
	v_med3_f32 v20, v20, s12, v154
	v_med3_f32 v21, v23, s12, v154
	v_med3_f32 v14, v14, s12, v154
	v_med3_f32 v15, v47, s12, v154
	v_lshlrev_b32_e32 v114, 16, v119
	v_fmac_f32_e32 v54, v113, v113
	v_cvt_pk_fp8_f32 v6, v20, v21 op_sel:[0,0,1]
	v_cvt_pk_fp8_f32 v7, v14, v15 op_sel:[0,0,1]
	v_and_b32_e32 v115, 0xffff0000, v119
	v_fmac_f32_e32 v54, v114, v114
	v_fmac_f32_e32 v54, v115, v115
	s_waitcnt vmcnt(16)
	v_lshlrev_b32_e32 v116, 16, v108
	v_and_b32_e32 v108, 0xffff0000, v108
	v_fmac_f32_e32 v54, v116, v116
	v_lshlrev_b32_e32 v117, 16, v109
	v_fmac_f32_e32 v54, v108, v108
	global_store_dwordx2 v[4:5], v[6:7], off offset:1024
	v_and_b32_e32 v109, 0xffff0000, v109
	v_fmac_f32_e32 v54, v117, v117
	ds_read_b128 v[12:15], v144 offset:22528
	ds_read_b128 v[20:23], v144 offset:38912
	v_lshlrev_b32_e32 v118, 16, v110
	v_fmac_f32_e32 v54, v109, v109
	v_and_b32_e32 v110, 0xffff0000, v110
	v_fmac_f32_e32 v54, v118, v118
	v_lshlrev_b32_e32 v119, 16, v111
	v_fmac_f32_e32 v54, v110, v110
	v_lshlrev_b32_e32 v6, 16, v28
	v_and_b32_e32 v111, 0xffff0000, v111
	v_fmac_f32_e32 v54, v119, v119
	v_and_b32_e32 v7, 0xffff0000, v28
	v_lshlrev_b32_e32 v28, 16, v29
	v_mul_f32_e32 v6, v36, v6
	v_fmac_f32_e32 v54, v111, v111
	s_waitcnt vmcnt(16)
	v_lshlrev_b32_e32 v129, 16, v100
	v_and_b32_e32 v29, 0xffff0000, v29
	s_waitcnt lgkmcnt(0)
	v_fma_f32 v6, v6, v12, v20
	v_mul_f32_e32 v12, v36, v28
	v_and_b32_e32 v157, 0xffff0000, v100
	v_fmac_f32_e32 v54, v129, v129
	v_mul_f32_e32 v7, v36, v7
	v_fma_f32 v20, v12, v14, v22
	v_mul_f32_e32 v12, v36, v29
	v_lshlrev_b32_e32 v158, 16, v101
	v_fmac_f32_e32 v54, v157, v157
	v_lshlrev_b32_e32 v37, 16, v30
	v_and_b32_e32 v38, 0xffff0000, v30
	v_lshlrev_b32_e32 v39, 16, v31
	v_and_b32_e32 v44, 0xffff0000, v31
	v_fma_f32 v7, v7, v13, v21
	v_fmac_f32_e32 v23, v12, v15
	ds_read_b128 v[12:15], v144 offset:22544
	ds_read_b128 v[28:31], v144 offset:38928
	v_and_b32_e32 v159, 0xffff0000, v101
	v_fmac_f32_e32 v54, v158, v158
	v_lshlrev_b32_e32 v160, 16, v102
	v_fmac_f32_e32 v54, v159, v159
	v_and_b32_e32 v99, 0xffff0000, v102
	v_fmac_f32_e32 v54, v160, v160
	v_lshlrev_b32_e32 v97, 16, v103
	v_fmac_f32_e32 v54, v99, v99
	v_mul_f32_e32 v21, v36, v37
	v_and_b32_e32 v96, 0xffff0000, v103
	v_fmac_f32_e32 v54, v97, v97
	s_waitcnt lgkmcnt(0)
	v_fma_f32 v12, v21, v12, v28
	v_mul_f32_e32 v21, v36, v38
	v_fmac_f32_e32 v54, v96, v96
	s_waitcnt vmcnt(15)
	v_lshlrev_b32_e32 v98, 16, v92
	v_fma_f32 v13, v21, v13, v29
	v_mul_f32_e32 v21, v36, v39
	v_and_b32_e32 v63, 0xffff0000, v92
	v_fmac_f32_e32 v54, v98, v98
	v_and_b32_e32 v68, 0xffff0000, v93
	v_lshlrev_b32_e32 v69, 16, v93
	v_fma_f32 v14, v21, v14, v30
	v_mul_f32_e32 v21, v36, v44
	v_fmac_f32_e32 v54, v63, v63
	v_pk_mul_f32 v[52:53], v[68:69], v[68:69]
	v_fmac_f32_e32 v31, v21, v15
	v_med3_f32 v15, v6, s12, v154
	v_med3_f32 v7, v7, s12, v154
	v_mov_b32_e32 v6, 0
	v_add_f32_e32 v53, v53, v54
	v_and_b32_e32 v70, 0xffff0000, v94
	v_lshlrev_b32_e32 v71, 16, v94
	v_cvt_pk_fp8_f32 v6, v15, v7
	v_med3_f32 v12, v12, s12, v154
	v_med3_f32 v13, v13, s12, v154
	v_mov_b32_e32 v7, 0
	v_add_f32_e32 v54, v52, v53
	v_pk_mul_f32 v[52:53], v[70:71], v[70:71]
	v_cvt_pk_fp8_f32 v7, v12, v13
	v_add_f32_e32 v53, v53, v54
	v_and_b32_e32 v60, 0xffff0000, v95
	v_lshlrev_b32_e32 v61, 16, v95
	v_add_f32_e32 v54, v52, v53
	v_pk_mul_f32 v[52:53], v[60:61], v[60:61]
	v_med3_f32 v20, v20, s12, v154
	v_add_f32_e32 v53, v53, v54
	v_med3_f32 v21, v23, s12, v154
	v_med3_f32 v14, v14, s12, v154
	v_med3_f32 v15, v31, s12, v154
	v_add_f32_e32 v52, v52, v53
	v_cvt_pk_fp8_f32 v6, v20, v21 op_sel:[0,0,1]
	v_cvt_pk_fp8_f32 v7, v14, v15 op_sel:[0,0,1]
	v_add_f32_dpp v52, v52, v52 quad_perm:[1,0,3,2] row_mask:0xf bank_mask:0xf bound_ctrl:1
	s_or_b32 s22, s0, 4
	s_mov_b32 s23, s1
	v_add_f32_dpp v52, v52, v52 quad_perm:[2,3,0,1] row_mask:0xf bank_mask:0xf bound_ctrl:1
	s_lshl_b64 s[8:9], s[22:23], 12
	s_lshl_b64 s[24:25], s[22:23], 13
	v_readlane_b32 s36, v253, 10
	v_add_f32_dpp v52, v52, v52 row_ror:4 row_mask:0xf bank_mask:0xf bound_ctrl:1
	v_readlane_b32 s37, v253, 11
	s_add_u32 s24, s36, s24
	v_add_f32_dpp v52, v52, v52 row_ror:8 row_mask:0xf bank_mask:0xf bound_ctrl:1
	global_store_dwordx2 v[4:5], v[6:7], off offset:1536
	v_lshl_add_u64 v[4:5], v[130:131], 0, s[8:9]
	s_addc_u32 s25, s37, s25
	v_readlane_b32 s3, v52, 16
	v_readlane_b32 s28, v52, 48
	global_load_dwordx4 v[88:91], v[4:5], off
	global_load_dwordx4 v[80:83], v[4:5], off offset:1024
	global_load_dwordx4 v[72:75], v[4:5], off offset:2048
	global_load_dwordx4 v[64:67], v[4:5], off offset:3072
	global_load_dwordx4 v[48:51], v122, s[24:25] offset:16
	global_load_dwordx4 v[56:59], v122, s[24:25]
	global_load_dwordx4 v[36:39], v122, s[24:25] offset:2064
	global_load_dwordx4 v[44:47], v122, s[24:25] offset:2048
	global_load_dwordx4 v[20:23], v149, s[24:25] offset:16
	global_load_dwordx4 v[28:31], v149, s[24:25]
	global_load_dwordx4 v[4:7], v150, s[24:25] offset:16
	global_load_dwordx4 v[12:15], v150, s[24:25]
	v_readlane_b32 s24, v52, 0
	v_readlane_b32 s25, v52, 32
	v_mov_b32_e32 v52, s3
	v_mov_b32_e32 v53, s28
	v_pk_add_f32 v[52:53], s[24:25], v[52:53]
	v_readlane_b32 s38, v253, 12
	v_add_f32_e32 v52, v52, v53
	v_fmamk_f32 v52, v52, 0x3a000000, v151
	v_cmp_gt_f32_e32 vcc, s11, v52
	v_mul_f32_e32 v53, 0x4b800000, v52
	v_readlane_b32 s39, v253, 13
	v_cndmask_b32_e32 v52, v52, v53, vcc
	v_rsq_f32_e32 v52, v52
	v_readlane_b32 s40, v253, 14
	v_readlane_b32 s41, v253, 15
	v_readlane_b32 s42, v253, 16
	v_mul_f32_e32 v53, 0x45800000, v52
	v_cndmask_b32_e32 v62, v52, v53, vcc
	ds_read_b128 v[52:55], v144
	ds_read_b128 v[92:95], v144 offset:16
	ds_read_b128 v[100:103], v144 offset:8192
	v_mul_f32_e32 v104, v62, v104
	v_readlane_b32 s43, v253, 17
	v_readlane_b32 s44, v253, 18
	v_readlane_b32 s45, v253, 19
	s_waitcnt lgkmcnt(0)
	v_mul_f32_e32 v100, v100, v104
	s_waitcnt vmcnt(26)
	v_fma_f32 v100, v52, v100, v84
	v_mul_f32_e32 v52, v62, v105
	v_mul_f32_e32 v52, v101, v52
	v_fma_f32 v85, v53, v52, v85
	v_mul_f32_e32 v52, v62, v106
	v_mul_f32_e32 v52, v102, v52
	v_fma_f32 v86, v54, v52, v86
	v_mul_f32_e32 v52, v62, v107
	v_mul_f32_e32 v52, v103, v52
	v_fmac_f32_e32 v87, v55, v52
	ds_read_b128 v[52:55], v144 offset:8208
	v_mul_f32_e32 v101, v62, v112
	v_mul_f32_e32 v84, v85, v85
	v_fmac_f32_e32 v84, v100, v100
	v_fmac_f32_e32 v84, v86, v86
	s_waitcnt lgkmcnt(0)
	v_mul_f32_e32 v52, v101, v52
	v_fma_f32 v76, v92, v52, v76
	v_mul_f32_e32 v52, v62, v113
	v_mul_f32_e32 v52, v52, v53
	v_fma_f32 v77, v93, v52, v77
	v_mul_f32_e32 v52, v62, v114
	v_mul_f32_e32 v52, v52, v54
	v_fmac_f32_e32 v84, v87, v87
	v_fma_f32 v78, v94, v52, v78
	v_mul_f32_e32 v52, v62, v115
	v_fmac_f32_e32 v84, v76, v76
	v_mul_f32_e32 v52, v52, v55
	v_fmac_f32_e32 v84, v77, v77
	v_fmac_f32_e32 v79, v95, v52
	v_cvt_pk_bf16_f32 v52, v100, v85
	v_cvt_pk_bf16_f32 v53, v86, v87
	v_cvt_pk_bf16_f32 v54, v76, v77
	v_lshl_add_u64 v[76:77], v[132:133], 0, s[26:27]
	v_cvt_pk_bf16_f32 v55, v78, v79
	global_store_dwordx4 v[76:77], v[52:55], off
	ds_read_b128 v[92:95], v144 offset:2048
	ds_read_b128 v[100:103], v144 offset:2064
	ds_read_b128 v[104:107], v144 offset:10240
	v_fmac_f32_e32 v84, v78, v78
	v_mul_f32_e32 v78, v62, v116
	v_fmac_f32_e32 v84, v79, v79
	v_readlane_b32 s46, v253, 20
	s_waitcnt lgkmcnt(0)
	v_mul_f32_e32 v78, v78, v104
	s_waitcnt vmcnt(25)
	v_fma_f32 v40, v92, v78, v40
	v_mul_f32_e32 v78, v62, v108
	v_mul_f32_e32 v78, v78, v105
	v_fma_f32 v41, v93, v78, v41
	v_mul_f32_e32 v78, v62, v117
	v_mul_f32_e32 v78, v78, v106
	v_fma_f32 v42, v94, v78, v42
	v_mul_f32_e32 v78, v62, v109
	v_mul_f32_e32 v78, v78, v107
	v_fmac_f32_e32 v43, v95, v78
	ds_read_b128 v[92:95], v144 offset:10256
	v_mul_f32_e32 v78, v62, v118
	v_fmac_f32_e32 v84, v40, v40
	v_fmac_f32_e32 v84, v41, v41
	v_fmac_f32_e32 v84, v42, v42
	s_waitcnt lgkmcnt(0)
	v_mul_f32_e32 v78, v78, v92
	v_fma_f32 v78, v100, v78, v32
	v_mul_f32_e32 v32, v62, v110
	v_mul_f32_e32 v32, v32, v93
	v_fma_f32 v79, v101, v32, v33
	v_mul_f32_e32 v32, v62, v119
	v_fmac_f32_e32 v84, v43, v43
	v_mul_f32_e32 v32, v32, v94
	v_fmac_f32_e32 v84, v78, v78
	v_fma_f32 v85, v102, v32, v34
	v_mul_f32_e32 v32, v62, v111
	v_fmac_f32_e32 v84, v79, v79
	v_mul_f32_e32 v32, v32, v95
	v_fmac_f32_e32 v84, v85, v85
	v_fmac_f32_e32 v35, v103, v32
	v_fmac_f32_e32 v84, v35, v35
	v_cvt_pk_bf16_f32 v32, v40, v41
	v_cvt_pk_bf16_f32 v33, v42, v43
	v_cvt_pk_bf16_f32 v34, v78, v79
	v_cvt_pk_bf16_f32 v35, v85, v35
	global_store_dwordx4 v[76:77], v[32:35], off offset:1024
	ds_read_b128 v[40:43], v144 offset:4096
	ds_read_b128 v[92:95], v144 offset:4112
	ds_read_b128 v[100:103], v144 offset:12288
	v_mul_f32_e32 v78, v62, v129
	v_readlane_b32 s47, v253, 21
	v_readlane_b32 s48, v253, 22
	v_readlane_b32 s49, v253, 23
	s_waitcnt lgkmcnt(0)
	v_mul_f32_e32 v78, v78, v100
	s_waitcnt vmcnt(24)
	v_fma_f32 v24, v40, v78, v24
	v_mul_f32_e32 v40, v62, v157
	v_mul_f32_e32 v40, v40, v101
	v_fma_f32 v25, v41, v40, v25
	v_mul_f32_e32 v40, v62, v158
	v_mul_f32_e32 v40, v40, v102
	v_fma_f32 v26, v42, v40, v26
	v_mul_f32_e32 v40, v62, v159
	v_mul_f32_e32 v40, v40, v103
	v_fmac_f32_e32 v27, v43, v40
	ds_read_b128 v[40:43], v144 offset:12304
	v_mul_f32_e32 v78, v62, v160
	v_fmac_f32_e32 v84, v24, v24
	v_fmac_f32_e32 v84, v25, v25
	v_fmac_f32_e32 v84, v26, v26
	s_waitcnt lgkmcnt(0)
	v_mul_f32_e32 v40, v78, v40
	v_fma_f32 v40, v92, v40, v16
	v_mul_f32_e32 v16, v62, v99
	v_mul_f32_e32 v16, v16, v41
	v_fma_f32 v41, v93, v16, v17
	v_mul_f32_e32 v16, v62, v97
	v_fmac_f32_e32 v84, v27, v27
	v_mul_f32_e32 v16, v16, v42
	v_fmac_f32_e32 v84, v40, v40
	v_fma_f32 v42, v94, v16, v18
	v_mul_f32_e32 v16, v62, v96
	v_fmac_f32_e32 v84, v41, v41
	v_mul_f32_e32 v16, v16, v43
	v_fmac_f32_e32 v84, v42, v42
	v_fmac_f32_e32 v19, v95, v16
	v_fmac_f32_e32 v84, v19, v19
	v_cvt_pk_bf16_f32 v16, v24, v25
	v_cvt_pk_bf16_f32 v17, v26, v27
	v_cvt_pk_bf16_f32 v18, v40, v41
	v_cvt_pk_bf16_f32 v19, v42, v19
	global_store_dwordx4 v[76:77], v[16:19], off offset:2048
	ds_read_b128 v[24:27], v144 offset:6144
	ds_read_b128 v[40:43], v144 offset:6160
	ds_read_b128 v[92:95], v144 offset:14336
	v_mul_f32_e32 v78, v62, v98
	v_readlane_b32 s50, v253, 24
	v_readlane_b32 s51, v253, 25
	s_waitcnt lgkmcnt(0)
	v_mul_f32_e32 v78, v78, v92
	s_waitcnt vmcnt(23)
	v_fma_f32 v78, v24, v78, v8
	v_mul_f32_e32 v8, v62, v63
	v_mul_f32_e32 v8, v8, v93
	v_fma_f32 v63, v25, v8, v9
	v_pk_mul_f32 v[8:9], v[62:63], v[68:69] op_sel_hi:[0,1]
	v_pk_mul_f32 v[8:9], v[8:9], v[94:95] op_sel:[1,0] op_sel_hi:[0,1]
	v_fmac_f32_e32 v84, v78, v78
	v_pk_fma_f32 v[24:25], v[26:27], v[8:9], v[10:11]
	v_fmac_f32_e32 v84, v63, v63
	v_pk_mul_f32 v[8:9], v[24:25], v[24:25]
	v_pk_mul_f32 v[26:27], v[62:63], v[70:71] op_sel_hi:[0,1]
	v_add_f32_e32 v8, v84, v8
	v_add_f32_e32 v68, v8, v9
	ds_read_b128 v[8:11], v144 offset:14352
	s_waitcnt lgkmcnt(0)
	v_pk_mul_f32 v[8:9], v[26:27], v[8:9] op_sel:[1,0] op_sel_hi:[0,1]
	v_pk_fma_f32 v[8:9], v[40:41], v[8:9], v[0:1]
	s_nop 0
	v_pk_mul_f32 v[0:1], v[8:9], v[8:9]
	s_nop 0
	v_add_f32_e32 v0, v68, v0
	v_add_f32_e32 v26, v0, v1
	v_pk_mul_f32 v[0:1], v[62:63], v[60:61] op_sel_hi:[0,1]
	v_pk_mul_f32 v[0:1], v[0:1], v[10:11] op_sel:[1,0] op_sel_hi:[0,1]
	v_pk_fma_f32 v[10:11], v[42:43], v[0:1], v[2:3]
	s_nop 0
	v_pk_mul_f32 v[0:1], v[10:11], v[10:11]
	s_nop 0
	v_add_f32_e32 v0, v26, v0
	v_add_f32_e32 v26, v0, v1
	v_cvt_pk_bf16_f32 v0, v78, v63
	v_cvt_pk_bf16_f32 v1, v24, v25
	v_cvt_pk_bf16_f32 v2, v8, v9
	v_cvt_pk_bf16_f32 v3, v10, v11
	global_store_dwordx4 v[76:77], v[0:3], off offset:3072
	s_nop 0
	v_add_f32_dpp v8, v26, v26 quad_perm:[1,0,3,2] row_mask:0xf bank_mask:0xf bound_ctrl:1
	s_nop 1
	v_add_f32_dpp v8, v8, v8 quad_perm:[2,3,0,1] row_mask:0xf bank_mask:0xf bound_ctrl:1
	s_nop 1
	v_add_f32_dpp v8, v8, v8 row_ror:4 row_mask:0xf bank_mask:0xf bound_ctrl:1
	s_nop 1
	v_add_f32_dpp v8, v8, v8 row_ror:8 row_mask:0xf bank_mask:0xf bound_ctrl:1
	s_nop 0
	v_readlane_b32 s3, v8, 16
	v_readlane_b32 s26, v8, 48
	v_readlane_b32 s24, v8, 0
	v_readlane_b32 s25, v8, 32
	v_mov_b32_e32 v8, s3
	v_mov_b32_e32 v9, s26
	v_pk_add_f32 v[8:9], s[24:25], v[8:9]
	s_nop 0
	v_add_f32_e32 v8, v8, v9
	v_fmamk_f32 v8, v8, 0x3a000000, v151
	v_cmp_gt_f32_e32 vcc, s11, v8
	v_mul_f32_e32 v9, 0x4b800000, v8
	s_nop 0
	v_cndmask_b32_e32 v8, v8, v9, vcc
	v_rsq_f32_e32 v8, v8
	s_nop 0
	v_mul_f32_e32 v9, 0x45800000, v8
	v_cndmask_b32_e32 v10, v8, v9, vcc
	s_and_saveexec_b64 s[24:25], s[6:7]
	v_mov_b32_e32 v8, s10
	ds_write_b32 v8, v10 offset:60684
	s_or_b64 exec, exec, s[24:25]
	v_lshlrev_b32_e32 v8, 16, v52
	v_and_b32_e32 v9, 0xffff0000, v52
	v_lshlrev_b32_e32 v11, 16, v53
	v_and_b32_e32 v60, 0xffff0000, v53
	v_lshlrev_b32_e32 v61, 16, v54
	v_and_b32_e32 v62, 0xffff0000, v54
	v_lshlrev_b32_e32 v63, 16, v55
	v_and_b32_e32 v68, 0xffff0000, v55
	ds_read_b128 v[24:27], v144 offset:16384
	ds_read_b128 v[40:43], v144 offset:16400
	ds_read_b128 v[52:55], v144 offset:32768
	v_mul_f32_e32 v8, v10, v8
	v_mul_f32_e32 v9, v10, v9
	v_mul_f32_e32 v11, v10, v11
	s_lshl_b64 s[20:21], s[20:21], 11
	s_waitcnt lgkmcnt(0)
	v_fma_f32 v8, v8, v24, v52
	v_mul_f32_e32 v24, v10, v60
	v_fma_f32 v9, v9, v25, v53
	v_fma_f32 v11, v11, v26, v54
	v_fmac_f32_e32 v55, v24, v27
	ds_read_b128 v[24:27], v144 offset:32784
	v_mul_f32_e32 v52, v10, v61
	v_med3_f32 v8, v8, s12, v154
	v_med3_f32 v9, v9, s12, v154
	v_med3_f32 v11, v11, s12, v154
	s_waitcnt lgkmcnt(0)
	v_fma_f32 v40, v52, v40, v24
	v_mul_f32_e32 v24, v10, v62
	v_fma_f32 v25, v24, v41, v25
	v_mul_f32_e32 v24, v10, v63
	v_fma_f32 v26, v24, v42, v26
	v_mul_f32_e32 v24, v10, v68
	v_fmac_f32_e32 v27, v24, v43
	v_mov_b32_e32 v24, 0
	v_cvt_pk_fp8_f32 v24, v8, v9
	v_med3_f32 v8, v40, s12, v154
	v_med3_f32 v9, v25, s12, v154
	v_mov_b32_e32 v25, 0
	v_cvt_pk_fp8_f32 v25, v8, v9
	v_med3_f32 v41, v55, s12, v154
	v_cvt_pk_fp8_f32 v24, v11, v41 op_sel:[0,0,1]
	v_med3_f32 v11, v26, s12, v154
	v_med3_f32 v26, v27, s12, v154
	v_cvt_pk_fp8_f32 v25, v11, v26 op_sel:[0,0,1]
	v_lshl_add_u64 v[8:9], v[134:135], 0, s[20:21]
	v_lshlrev_b32_e32 v11, 16, v32
	v_and_b32_e32 v40, 0xffff0000, v32
	global_store_dwordx2 v[8:9], v[24:25], off
	v_lshlrev_b32_e32 v41, 16, v33
	v_and_b32_e32 v42, 0xffff0000, v33
	v_lshlrev_b32_e32 v43, 16, v34
	v_and_b32_e32 v52, 0xffff0000, v34
	v_lshlrev_b32_e32 v53, 16, v35
	v_and_b32_e32 v54, 0xffff0000, v35
	ds_read_b128 v[24:27], v144 offset:18432
	ds_read_b128 v[32:35], v144 offset:34816
	v_mul_f32_e32 v11, v10, v11
	s_waitcnt vmcnt(16)
	v_and_b32_e32 v108, 0xffff0000, v88
	v_lshlrev_b32_e32 v104, 16, v88
	v_mul_f32_e32 v96, v108, v108
	s_waitcnt lgkmcnt(0)
	v_fma_f32 v11, v11, v24, v32
	v_mul_f32_e32 v24, v10, v40
	v_fma_f32 v32, v24, v25, v33
	v_mul_f32_e32 v24, v10, v41
	v_fma_f32 v33, v24, v26, v34
	v_mul_f32_e32 v24, v10, v42
	v_fmac_f32_e32 v35, v24, v27
	v_mul_f32_e32 v34, v10, v43
	ds_read_b128 v[24:27], v144 offset:18448
	ds_read_b128 v[40:43], v144 offset:34832
	v_med3_f32 v11, v11, s12, v154
	v_lshlrev_b32_e32 v109, 16, v89
	v_fmac_f32_e32 v96, v104, v104
	v_and_b32_e32 v89, 0xffff0000, v89
	s_waitcnt lgkmcnt(0)
	v_fma_f32 v34, v34, v24, v40
	v_mul_f32_e32 v24, v10, v52
	v_fma_f32 v25, v24, v25, v41
	v_mul_f32_e32 v24, v10, v53
	v_fma_f32 v26, v24, v26, v42
	v_mul_f32_e32 v24, v10, v54
	v_fmac_f32_e32 v43, v24, v27
	v_med3_f32 v27, v32, s12, v154
	v_mov_b32_e32 v24, 0
	v_cvt_pk_fp8_f32 v24, v11, v27
	v_med3_f32 v11, v34, s12, v154
	v_med3_f32 v27, v25, s12, v154
	v_mov_b32_e32 v25, 0
	v_cvt_pk_fp8_f32 v25, v11, v27
	v_med3_f32 v32, v33, s12, v154
	v_med3_f32 v33, v35, s12, v154
	v_cvt_pk_fp8_f32 v24, v32, v33 op_sel:[0,0,1]
	v_med3_f32 v26, v26, s12, v154
	v_med3_f32 v32, v43, s12, v154
	v_cvt_pk_fp8_f32 v25, v26, v32 op_sel:[0,0,1]
	v_lshlrev_b32_e32 v11, 16, v16
	v_and_b32_e32 v32, 0xffff0000, v16
	v_lshlrev_b32_e32 v33, 16, v17
	global_store_dwordx2 v[8:9], v[24:25], off offset:512
	v_and_b32_e32 v34, 0xffff0000, v17
	v_lshlrev_b32_e32 v35, 16, v18
	v_and_b32_e32 v40, 0xffff0000, v18
	v_lshlrev_b32_e32 v41, 16, v19
	v_and_b32_e32 v42, 0xffff0000, v19
	ds_read_b128 v[16:19], v144 offset:20480
	ds_read_b128 v[24:27], v144 offset:36864
	v_mul_f32_e32 v11, v10, v11
	v_fmac_f32_e32 v96, v109, v109
	v_lshlrev_b32_e32 v110, 16, v90
	v_fmac_f32_e32 v96, v89, v89
	s_waitcnt lgkmcnt(0)
	v_fma_f32 v11, v11, v16, v24
	v_mul_f32_e32 v16, v10, v32
	v_fma_f32 v24, v16, v17, v25
	v_mul_f32_e32 v16, v10, v33
	v_fma_f32 v25, v16, v18, v26
	v_mul_f32_e32 v16, v10, v34
	v_fmac_f32_e32 v27, v16, v19
	v_mul_f32_e32 v26, v10, v35
	ds_read_b128 v[16:19], v144 offset:20496
	ds_read_b128 v[32:35], v144 offset:36880
	v_med3_f32 v11, v11, s12, v154
	v_and_b32_e32 v90, 0xffff0000, v90
	v_fmac_f32_e32 v96, v110, v110
	v_lshlrev_b32_e32 v111, 16, v91
	s_waitcnt lgkmcnt(0)
	v_fma_f32 v26, v26, v16, v32
	v_mul_f32_e32 v16, v10, v40
	v_fma_f32 v17, v16, v17, v33
	v_mul_f32_e32 v16, v10, v41
	v_fma_f32 v18, v16, v18, v34
	v_mul_f32_e32 v16, v10, v42
	v_fmac_f32_e32 v35, v16, v19
	v_med3_f32 v19, v24, s12, v154
	v_mov_b32_e32 v16, 0
	v_cvt_pk_fp8_f32 v16, v11, v19
	v_med3_f32 v11, v26, s12, v154
	v_med3_f32 v19, v17, s12, v154
	v_mov_b32_e32 v17, 0
	v_cvt_pk_fp8_f32 v17, v11, v19
	v_med3_f32 v24, v25, s12, v154
	v_med3_f32 v25, v27, s12, v154
	v_cvt_pk_fp8_f32 v16, v24, v25 op_sel:[0,0,1]
	v_med3_f32 v18, v18, s12, v154
	v_med3_f32 v24, v35, s12, v154
	v_fmac_f32_e32 v96, v90, v90
	v_cvt_pk_fp8_f32 v17, v18, v24 op_sel:[0,0,1]
	v_and_b32_e32 v91, 0xffff0000, v91
	v_fmac_f32_e32 v96, v111, v111
	v_fmac_f32_e32 v96, v91, v91
	s_waitcnt vmcnt(16)
	v_lshlrev_b32_e32 v112, 16, v80
	v_and_b32_e32 v113, 0xffff0000, v80
	v_fmac_f32_e32 v96, v112, v112
	v_lshlrev_b32_e32 v114, 16, v81
	v_fmac_f32_e32 v96, v113, v113
	global_store_dwordx2 v[8:9], v[16:17], off offset:1024
	v_and_b32_e32 v115, 0xffff0000, v81
	v_fmac_f32_e32 v96, v114, v114
	v_lshlrev_b32_e32 v11, 16, v0
	v_and_b32_e32 v24, 0xffff0000, v0
	v_lshlrev_b32_e32 v25, 16, v1
	v_and_b32_e32 v26, 0xffff0000, v1
	v_lshlrev_b32_e32 v27, 16, v2
	v_and_b32_e32 v32, 0xffff0000, v2
	v_lshlrev_b32_e32 v33, 16, v3
	v_and_b32_e32 v34, 0xffff0000, v3
	ds_read_b128 v[0:3], v144 offset:22528
	ds_read_b128 v[16:19], v144 offset:38912
	v_lshlrev_b32_e32 v116, 16, v82
	v_fmac_f32_e32 v96, v115, v115
	v_and_b32_e32 v117, 0xffff0000, v82
	v_fmac_f32_e32 v96, v116, v116
	v_lshlrev_b32_e32 v118, 16, v83
	v_fmac_f32_e32 v96, v117, v117
	v_and_b32_e32 v119, 0xffff0000, v83
	v_fmac_f32_e32 v96, v118, v118
	v_mul_f32_e32 v11, v10, v11
	v_fmac_f32_e32 v96, v119, v119
	s_waitcnt vmcnt(16)
	v_lshlrev_b32_e32 v129, 16, v72
	s_waitcnt lgkmcnt(0)
	v_fma_f32 v11, v11, v0, v16
	v_mul_f32_e32 v0, v10, v24
	v_and_b32_e32 v157, 0xffff0000, v72
	v_fmac_f32_e32 v96, v129, v129
	v_fma_f32 v16, v0, v1, v17
	v_mul_f32_e32 v0, v10, v25
	v_lshlrev_b32_e32 v158, 16, v73
	v_fmac_f32_e32 v96, v157, v157
	v_fma_f32 v17, v0, v2, v18
	v_mul_f32_e32 v0, v10, v26
	v_and_b32_e32 v159, 0xffff0000, v73
	v_fmac_f32_e32 v96, v158, v158
	v_fmac_f32_e32 v19, v0, v3
	v_mul_f32_e32 v18, v10, v27
	ds_read_b128 v[0:3], v144 offset:22544
	ds_read_b128 v[24:27], v144 offset:38928
	v_lshlrev_b32_e32 v160, 16, v74
	v_fmac_f32_e32 v96, v159, v159
	v_and_b32_e32 v88, 0xffff0000, v74
	v_fmac_f32_e32 v96, v160, v160
	v_lshlrev_b32_e32 v82, 16, v75
	v_fmac_f32_e32 v96, v88, v88
	v_and_b32_e32 v81, 0xffff0000, v75
	v_fmac_f32_e32 v96, v82, v82
	v_fmac_f32_e32 v96, v81, v81
	s_waitcnt vmcnt(15)
	v_lshlrev_b32_e32 v83, 16, v64
	s_waitcnt lgkmcnt(0)
	v_fma_f32 v18, v18, v0, v24
	v_mul_f32_e32 v0, v10, v32
	v_and_b32_e32 v80, 0xffff0000, v64
	v_fmac_f32_e32 v96, v83, v83
	v_and_b32_e32 v72, 0xffff0000, v65
	v_lshlrev_b32_e32 v73, 16, v65
	v_fma_f32 v1, v0, v1, v25
	v_mul_f32_e32 v0, v10, v33
	v_fmac_f32_e32 v96, v80, v80
	v_pk_mul_f32 v[64:65], v[72:73], v[72:73]
	v_fma_f32 v2, v0, v2, v26
	v_mul_f32_e32 v0, v10, v34
	v_add_f32_e32 v65, v65, v96
	v_and_b32_e32 v74, 0xffff0000, v66
	v_lshlrev_b32_e32 v75, 16, v66
	v_fmac_f32_e32 v27, v0, v3
	v_med3_f32 v3, v11, s12, v154
	v_med3_f32 v10, v16, s12, v154
	v_mov_b32_e32 v0, 0
	v_add_f32_e32 v96, v64, v65
	v_pk_mul_f32 v[64:65], v[74:75], v[74:75]
	v_cvt_pk_fp8_f32 v0, v3, v10
	v_med3_f32 v3, v18, s12, v154
	v_med3_f32 v10, v1, s12, v154
	v_mov_b32_e32 v1, 0
	v_add_f32_e32 v65, v65, v96
	v_cvt_pk_fp8_f32 v1, v3, v10
	v_add_f32_e32 v96, v64, v65
	v_and_b32_e32 v64, 0xffff0000, v67
	v_lshlrev_b32_e32 v65, 16, v67
	v_pk_mul_f32 v[66:67], v[64:65], v[64:65]
	v_med3_f32 v11, v17, s12, v154
	v_med3_f32 v16, v19, s12, v154
	v_add_f32_e32 v67, v67, v96
	v_cvt_pk_fp8_f32 v0, v11, v16 op_sel:[0,0,1]
	v_med3_f32 v2, v2, s12, v154
	v_med3_f32 v11, v27, s12, v154
	v_add_f32_e32 v66, v66, v67
	v_cvt_pk_fp8_f32 v1, v2, v11 op_sel:[0,0,1]
	s_or_b32 s24, s0, 5
	v_add_f32_dpp v66, v66, v66 quad_perm:[1,0,3,2] row_mask:0xf bank_mask:0xf bound_ctrl:1
	s_mov_b32 s25, s1
	s_lshl_b64 s[26:27], s[24:25], 12
	v_add_f32_dpp v66, v66, v66 quad_perm:[2,3,0,1] row_mask:0xf bank_mask:0xf bound_ctrl:1
	s_lshl_b64 s[20:21], s[24:25], 13
	v_readlane_b32 s36, v253, 10
	v_add_f32_dpp v66, v66, v66 row_ror:4 row_mask:0xf bank_mask:0xf bound_ctrl:1
	v_readlane_b32 s37, v253, 11
	s_add_u32 s20, s36, s20
	v_add_f32_dpp v66, v66, v66 row_ror:8 row_mask:0xf bank_mask:0xf bound_ctrl:1
	global_store_dwordx2 v[8:9], v[0:1], off offset:1536
	v_lshl_add_u64 v[0:1], v[130:131], 0, s[26:27]
	s_addc_u32 s21, s37, s21
	v_readlane_b32 s3, v66, 16
	v_readlane_b32 s28, v66, 48
	global_load_dwordx4 v[92:95], v[0:1], off
	global_load_dwordx4 v[84:87], v[0:1], off offset:1024
	global_load_dwordx4 v[76:79], v[0:1], off offset:2048
	global_load_dwordx4 v[68:71], v[0:1], off offset:3072
	global_load_dwordx4 v[52:55], v122, s[20:21] offset:16
	global_load_dwordx4 v[60:63], v122, s[20:21]
	global_load_dwordx4 v[32:35], v122, s[20:21] offset:2064
	global_load_dwordx4 v[40:43], v122, s[20:21] offset:2048
	global_load_dwordx4 v[16:19], v149, s[20:21] offset:16
	global_load_dwordx4 v[24:27], v149, s[20:21]
	global_load_dwordx4 v[0:3], v150, s[20:21] offset:16
	global_load_dwordx4 v[8:11], v150, s[20:21]
	v_readlane_b32 s20, v66, 0
	v_readlane_b32 s21, v66, 32
	v_mov_b32_e32 v66, s3
	v_mov_b32_e32 v67, s28
	v_pk_add_f32 v[66:67], s[20:21], v[66:67]
	ds_read_b128 v[96:99], v144
	ds_read_b128 v[100:103], v144 offset:16
	v_add_f32_e32 v66, v66, v67
	v_fmamk_f32 v66, v66, 0x3a000000, v151
	v_cmp_gt_f32_e32 vcc, s11, v66
	v_mul_f32_e32 v67, 0x4b800000, v66
	v_readlane_b32 s38, v253, 12
	v_cndmask_b32_e32 v66, v66, v67, vcc
	v_rsq_f32_e32 v66, v66
	v_readlane_b32 s39, v253, 13
	v_readlane_b32 s40, v253, 14
	v_readlane_b32 s41, v253, 15
	v_mul_f32_e32 v67, 0x45800000, v66
	v_cndmask_b32_e32 v66, v66, v67, vcc
	v_mul_f32_e32 v67, v66, v104
	ds_read_b128 v[104:107], v144 offset:8192
	v_mul_f32_e32 v89, v66, v89
	v_readlane_b32 s42, v253, 16
	v_readlane_b32 s43, v253, 17
	v_readlane_b32 s44, v253, 18
	s_waitcnt lgkmcnt(0)
	v_mul_f32_e32 v67, v104, v67
	s_waitcnt vmcnt(26)
	v_fma_f32 v56, v96, v67, v56
	v_mul_f32_e32 v67, v66, v108
	v_mul_f32_e32 v96, v66, v109
	v_mul_f32_e32 v67, v105, v67
	v_mul_f32_e32 v96, v106, v96
	v_mul_f32_e32 v89, v107, v89
	v_fma_f32 v57, v97, v67, v57
	v_fma_f32 v58, v98, v96, v58
	v_fmac_f32_e32 v59, v99, v89
	ds_read_b128 v[96:99], v144 offset:8208
	v_mul_f32_e32 v89, v66, v110
	v_mul_f32_e32 v67, v57, v57
	v_fmac_f32_e32 v67, v56, v56
	v_fmac_f32_e32 v67, v58, v58
	s_waitcnt lgkmcnt(0)
	v_mul_f32_e32 v89, v89, v96
	v_fma_f32 v89, v100, v89, v48
	v_mul_f32_e32 v48, v66, v90
	v_mul_f32_e32 v48, v48, v97
	v_fma_f32 v90, v101, v48, v49
	v_mul_f32_e32 v48, v66, v111
	v_fmac_f32_e32 v67, v59, v59
	v_mul_f32_e32 v48, v48, v98
	v_fmac_f32_e32 v67, v89, v89
	v_fma_f32 v96, v102, v48, v50
	v_mul_f32_e32 v48, v66, v91
	v_fmac_f32_e32 v67, v90, v90
	v_mul_f32_e32 v48, v48, v99
	v_fmac_f32_e32 v67, v96, v96
	v_fmac_f32_e32 v51, v103, v48
	v_cvt_pk_bf16_f32 v48, v56, v57
	v_lshl_add_u64 v[56:57], v[132:133], 0, s[8:9]
	v_fmac_f32_e32 v67, v51, v51
	v_cvt_pk_bf16_f32 v49, v58, v59
	v_cvt_pk_bf16_f32 v50, v89, v90
	v_cvt_pk_bf16_f32 v51, v96, v51
	global_store_dwordx4 v[56:57], v[48:51], off
	ds_read_b128 v[96:99], v144 offset:2048
	ds_read_b128 v[100:103], v144 offset:2064
	ds_read_b128 v[104:107], v144 offset:10240
	v_mul_f32_e32 v58, v66, v112
	v_readlane_b32 s45, v253, 19
	v_readlane_b32 s46, v253, 20
	v_readlane_b32 s47, v253, 21
	s_waitcnt lgkmcnt(0)
	v_mul_f32_e32 v58, v58, v104
	s_waitcnt vmcnt(25)
	v_fma_f32 v44, v96, v58, v44
	v_mul_f32_e32 v58, v66, v113
	v_mul_f32_e32 v58, v58, v105
	v_fma_f32 v45, v97, v58, v45
	v_mul_f32_e32 v58, v66, v114
	v_mul_f32_e32 v58, v58, v106
	v_fma_f32 v46, v98, v58, v46
	v_mul_f32_e32 v58, v66, v115
	v_mul_f32_e32 v58, v58, v107
	v_fmac_f32_e32 v47, v99, v58
	ds_read_b128 v[96:99], v144 offset:10256
	v_mul_f32_e32 v58, v66, v116
	v_fmac_f32_e32 v67, v44, v44
	v_fmac_f32_e32 v67, v45, v45
	v_fmac_f32_e32 v67, v46, v46
	s_waitcnt lgkmcnt(0)
	v_mul_f32_e32 v58, v58, v96
	v_fma_f32 v58, v100, v58, v36
	v_mul_f32_e32 v36, v66, v117
	v_mul_f32_e32 v36, v36, v97
	v_fma_f32 v59, v101, v36, v37
	v_mul_f32_e32 v36, v66, v118
	v_fmac_f32_e32 v67, v47, v47
	v_mul_f32_e32 v36, v36, v98
	v_fmac_f32_e32 v67, v58, v58
	v_fma_f32 v89, v102, v36, v38
	v_mul_f32_e32 v36, v66, v119
	v_fmac_f32_e32 v67, v59, v59
	v_mul_f32_e32 v36, v36, v99
	v_fmac_f32_e32 v67, v89, v89
	v_fmac_f32_e32 v39, v103, v36
	v_fmac_f32_e32 v67, v39, v39
	v_cvt_pk_bf16_f32 v36, v44, v45
	v_cvt_pk_bf16_f32 v37, v46, v47
	v_cvt_pk_bf16_f32 v38, v58, v59
	v_cvt_pk_bf16_f32 v39, v89, v39
	global_store_dwordx4 v[56:57], v[36:39], off offset:1024
	ds_read_b128 v[44:47], v144 offset:4096
	ds_read_b128 v[96:99], v144 offset:4112
	ds_read_b128 v[100:103], v144 offset:12288
	v_mul_f32_e32 v58, v66, v129
	v_readlane_b32 s48, v253, 22
	v_readlane_b32 s49, v253, 23
	v_readlane_b32 s50, v253, 24
	s_waitcnt lgkmcnt(0)
	v_mul_f32_e32 v58, v58, v100
	s_waitcnt vmcnt(24)
	v_fma_f32 v28, v44, v58, v28
	v_mul_f32_e32 v44, v66, v157
	v_mul_f32_e32 v44, v44, v101
	v_fma_f32 v29, v45, v44, v29
	v_mul_f32_e32 v44, v66, v158
	v_mul_f32_e32 v44, v44, v102
	v_fma_f32 v30, v46, v44, v30
	v_mul_f32_e32 v44, v66, v159
	v_mul_f32_e32 v44, v44, v103
	v_fmac_f32_e32 v31, v47, v44
	ds_read_b128 v[44:47], v144 offset:12304
	v_mul_f32_e32 v58, v66, v160
	v_fmac_f32_e32 v67, v28, v28
	v_fmac_f32_e32 v67, v29, v29
	v_fmac_f32_e32 v67, v30, v30
	s_waitcnt lgkmcnt(0)
	v_mul_f32_e32 v44, v58, v44
	v_fma_f32 v44, v96, v44, v20
	v_mul_f32_e32 v20, v66, v88
	v_mul_f32_e32 v20, v20, v45
	v_fma_f32 v45, v97, v20, v21
	v_mul_f32_e32 v20, v66, v82
	v_fmac_f32_e32 v67, v31, v31
	v_mul_f32_e32 v20, v20, v46
	v_fmac_f32_e32 v67, v44, v44
	v_fma_f32 v46, v98, v20, v22
	v_mul_f32_e32 v20, v66, v81
	v_fmac_f32_e32 v67, v45, v45
	v_mul_f32_e32 v20, v20, v47
	v_fmac_f32_e32 v67, v46, v46
	v_fmac_f32_e32 v23, v99, v20
	v_fmac_f32_e32 v67, v23, v23
	v_cvt_pk_bf16_f32 v20, v28, v29
	v_cvt_pk_bf16_f32 v21, v30, v31
	v_cvt_pk_bf16_f32 v22, v44, v45
	v_cvt_pk_bf16_f32 v23, v46, v23
	global_store_dwordx4 v[56:57], v[20:23], off offset:2048
	ds_read_b128 v[28:31], v144 offset:6144
	ds_read_b128 v[44:47], v144 offset:6160
	ds_read_b128 v[88:91], v144 offset:14336
	v_mul_f32_e32 v58, v66, v83
	v_readlane_b32 s51, v253, 25
	s_waitcnt lgkmcnt(0)
	v_mul_f32_e32 v58, v58, v88
	s_waitcnt vmcnt(23)
	v_fma_f32 v58, v28, v58, v12
	v_mul_f32_e32 v12, v66, v80
	v_mul_f32_e32 v12, v12, v89
	v_fmac_f32_e32 v67, v58, v58
	v_fma_f32 v59, v29, v12, v13
	v_fmac_f32_e32 v67, v59, v59
	v_pk_mul_f32 v[12:13], v[66:67], v[72:73] op_sel_hi:[0,1]
	v_pk_mul_f32 v[12:13], v[12:13], v[90:91] op_sel:[1,0] op_sel_hi:[0,1]
	v_pk_fma_f32 v[28:29], v[30:31], v[12:13], v[14:15]
	s_nop 0
	v_pk_mul_f32 v[12:13], v[28:29], v[28:29]
	s_nop 0
	v_add_f32_e32 v12, v67, v12
	v_add_f32_e32 v67, v12, v13
	ds_read_b128 v[12:15], v144 offset:14352
	v_pk_mul_f32 v[30:31], v[66:67], v[74:75] op_sel_hi:[0,1]
	s_waitcnt lgkmcnt(0)
	v_pk_mul_f32 v[12:13], v[30:31], v[12:13] op_sel:[1,0] op_sel_hi:[0,1]
	v_pk_fma_f32 v[12:13], v[44:45], v[12:13], v[4:5]
	s_nop 0
	v_pk_mul_f32 v[4:5], v[12:13], v[12:13]
	s_nop 0
	v_add_f32_e32 v4, v67, v4
	v_add_f32_e32 v30, v4, v5
	v_pk_mul_f32 v[4:5], v[66:67], v[64:65] op_sel_hi:[0,1]
	v_pk_mul_f32 v[4:5], v[4:5], v[14:15] op_sel:[1,0] op_sel_hi:[0,1]
	v_pk_fma_f32 v[14:15], v[46:47], v[4:5], v[6:7]
	s_nop 0
	v_pk_mul_f32 v[4:5], v[14:15], v[14:15]
	s_nop 0
	v_add_f32_e32 v4, v30, v4
	v_add_f32_e32 v30, v4, v5
	v_cvt_pk_bf16_f32 v4, v58, v59
	v_cvt_pk_bf16_f32 v5, v28, v29
	v_cvt_pk_bf16_f32 v6, v12, v13
	v_cvt_pk_bf16_f32 v7, v14, v15
	global_store_dwordx4 v[56:57], v[4:7], off offset:3072
	s_nop 0
	v_add_f32_dpp v12, v30, v30 quad_perm:[1,0,3,2] row_mask:0xf bank_mask:0xf bound_ctrl:1
	s_nop 1
	v_add_f32_dpp v12, v12, v12 quad_perm:[2,3,0,1] row_mask:0xf bank_mask:0xf bound_ctrl:1
	s_nop 1
	v_add_f32_dpp v12, v12, v12 row_ror:4 row_mask:0xf bank_mask:0xf bound_ctrl:1
	s_nop 1
	v_add_f32_dpp v12, v12, v12 row_ror:8 row_mask:0xf bank_mask:0xf bound_ctrl:1
	s_nop 0
	v_readlane_b32 s3, v12, 16
	v_readlane_b32 s20, v12, 48
	v_readlane_b32 s8, v12, 0
	v_readlane_b32 s9, v12, 32
	v_mov_b32_e32 v12, s3
	v_mov_b32_e32 v13, s20
	v_pk_add_f32 v[12:13], s[8:9], v[12:13]
	s_nop 0
	v_add_f32_e32 v12, v12, v13
	v_fmamk_f32 v12, v12, 0x3a000000, v151
	v_cmp_gt_f32_e32 vcc, s11, v12
	v_mul_f32_e32 v13, 0x4b800000, v12
	s_nop 0
	v_cndmask_b32_e32 v12, v12, v13, vcc
	v_rsq_f32_e32 v12, v12
	s_nop 0
	v_mul_f32_e32 v13, 0x45800000, v12
	v_cndmask_b32_e32 v14, v12, v13, vcc
	s_and_saveexec_b64 s[8:9], s[6:7]
	v_mov_b32_e32 v12, s10
	ds_write_b32 v12, v14 offset:60688
	s_or_b64 exec, exec, s[8:9]
	v_lshlrev_b32_e32 v12, 16, v48
	v_and_b32_e32 v13, 0xffff0000, v48
	v_lshlrev_b32_e32 v15, 16, v49
	v_and_b32_e32 v56, 0xffff0000, v49
	v_lshlrev_b32_e32 v57, 16, v50
	v_and_b32_e32 v58, 0xffff0000, v50
	v_lshlrev_b32_e32 v59, 16, v51
	v_and_b32_e32 v64, 0xffff0000, v51
	ds_read_b128 v[28:31], v144 offset:16384
	ds_read_b128 v[44:47], v144 offset:16400
	ds_read_b128 v[48:51], v144 offset:32768
	v_mul_f32_e32 v12, v14, v12
	v_mul_f32_e32 v13, v14, v13
	v_mul_f32_e32 v15, v14, v15
	s_lshl_b64 s[8:9], s[22:23], 11
	s_waitcnt lgkmcnt(0)
	v_fma_f32 v12, v12, v28, v48
	v_mul_f32_e32 v28, v14, v56
	v_fma_f32 v13, v13, v29, v49
	v_fma_f32 v15, v15, v30, v50
	v_fmac_f32_e32 v51, v28, v31
	ds_read_b128 v[28:31], v144 offset:32784
	v_mul_f32_e32 v48, v14, v57
	v_med3_f32 v12, v12, s12, v154
	v_med3_f32 v13, v13, s12, v154
	v_med3_f32 v15, v15, s12, v154
	s_waitcnt lgkmcnt(0)
	v_fma_f32 v44, v48, v44, v28
	v_mul_f32_e32 v28, v14, v58
	v_fma_f32 v29, v28, v45, v29
	v_mul_f32_e32 v28, v14, v59
	v_fma_f32 v30, v28, v46, v30
	v_mul_f32_e32 v28, v14, v64
	v_fmac_f32_e32 v31, v28, v47
	v_mov_b32_e32 v28, 0
	v_cvt_pk_fp8_f32 v28, v12, v13
	v_med3_f32 v12, v44, s12, v154
	v_med3_f32 v13, v29, s12, v154
	v_mov_b32_e32 v29, 0
	v_cvt_pk_fp8_f32 v29, v12, v13
	v_med3_f32 v45, v51, s12, v154
	v_cvt_pk_fp8_f32 v28, v15, v45 op_sel:[0,0,1]
	v_med3_f32 v15, v30, s12, v154
	v_med3_f32 v30, v31, s12, v154
	v_cvt_pk_fp8_f32 v29, v15, v30 op_sel:[0,0,1]
	v_lshl_add_u64 v[12:13], v[134:135], 0, s[8:9]
	v_lshlrev_b32_e32 v15, 16, v36
	v_and_b32_e32 v44, 0xffff0000, v36
	global_store_dwordx2 v[12:13], v[28:29], off
	v_lshlrev_b32_e32 v45, 16, v37
	v_and_b32_e32 v46, 0xffff0000, v37
	v_lshlrev_b32_e32 v47, 16, v38
	v_and_b32_e32 v48, 0xffff0000, v38
	v_lshlrev_b32_e32 v49, 16, v39
	v_and_b32_e32 v50, 0xffff0000, v39
	ds_read_b128 v[28:31], v144 offset:18432
	ds_read_b128 v[36:39], v144 offset:34816
	v_mul_f32_e32 v15, v14, v15
	s_waitcnt vmcnt(16)
	v_and_b32_e32 v106, 0xffff0000, v92
	v_lshlrev_b32_e32 v102, 16, v92
	v_lshlrev_b32_e32 v108, 16, v94
	s_waitcnt lgkmcnt(0)
	v_fma_f32 v15, v15, v28, v36
	v_mul_f32_e32 v28, v14, v44
	v_fma_f32 v36, v28, v29, v37
	v_mul_f32_e32 v28, v14, v45
	v_fma_f32 v37, v28, v30, v38
	v_mul_f32_e32 v28, v14, v46
	v_fmac_f32_e32 v39, v28, v31
	v_mul_f32_e32 v38, v14, v47
	ds_read_b128 v[28:31], v144 offset:18448
	ds_read_b128 v[44:47], v144 offset:34832
	v_med3_f32 v15, v15, s12, v154
	v_and_b32_e32 v109, 0xffff0000, v94
	v_mul_f32_e32 v94, v106, v106
	v_lshlrev_b32_e32 v107, 16, v93
	s_waitcnt lgkmcnt(0)
	v_fma_f32 v38, v38, v28, v44
	v_mul_f32_e32 v28, v14, v48
	v_fma_f32 v29, v28, v29, v45
	v_mul_f32_e32 v28, v14, v49
	v_fma_f32 v30, v28, v30, v46
	v_mul_f32_e32 v28, v14, v50
	v_fmac_f32_e32 v47, v28, v31
	v_med3_f32 v31, v36, s12, v154
	v_mov_b32_e32 v28, 0
	v_cvt_pk_fp8_f32 v28, v15, v31
	v_med3_f32 v15, v38, s12, v154
	v_med3_f32 v31, v29, s12, v154
	v_mov_b32_e32 v29, 0
	v_cvt_pk_fp8_f32 v29, v15, v31
	v_med3_f32 v36, v37, s12, v154
	v_med3_f32 v37, v39, s12, v154
	v_cvt_pk_fp8_f32 v28, v36, v37 op_sel:[0,0,1]
	v_med3_f32 v30, v30, s12, v154
	v_med3_f32 v36, v47, s12, v154
	v_cvt_pk_fp8_f32 v29, v30, v36 op_sel:[0,0,1]
	v_lshlrev_b32_e32 v15, 16, v20
	v_and_b32_e32 v36, 0xffff0000, v20
	v_lshlrev_b32_e32 v37, 16, v21
	global_store_dwordx2 v[12:13], v[28:29], off offset:512
	v_and_b32_e32 v38, 0xffff0000, v21
	v_lshlrev_b32_e32 v39, 16, v22
	v_and_b32_e32 v44, 0xffff0000, v22
	v_lshlrev_b32_e32 v45, 16, v23
	v_and_b32_e32 v46, 0xffff0000, v23
	ds_read_b128 v[20:23], v144 offset:20480
	ds_read_b128 v[28:31], v144 offset:36864
	v_mul_f32_e32 v15, v14, v15
	v_fmac_f32_e32 v94, v102, v102
	v_and_b32_e32 v93, 0xffff0000, v93
	v_fmac_f32_e32 v94, v107, v107
	s_waitcnt lgkmcnt(0)
	v_fma_f32 v15, v15, v20, v28
	v_mul_f32_e32 v20, v14, v36
	v_fma_f32 v28, v20, v21, v29
	v_mul_f32_e32 v20, v14, v37
	v_fma_f32 v29, v20, v22, v30
	v_mul_f32_e32 v20, v14, v38
	v_fmac_f32_e32 v31, v20, v23
	v_mul_f32_e32 v30, v14, v39
	ds_read_b128 v[20:23], v144 offset:20496
	ds_read_b128 v[36:39], v144 offset:36880
	v_med3_f32 v15, v15, s12, v154
	v_fmac_f32_e32 v94, v93, v93
	v_fmac_f32_e32 v94, v108, v108
	v_lshlrev_b32_e32 v110, 16, v95
	s_waitcnt lgkmcnt(0)
	v_fma_f32 v30, v30, v20, v36
	v_mul_f32_e32 v20, v14, v44
	v_fma_f32 v21, v20, v21, v37
	v_mul_f32_e32 v20, v14, v45
	v_fma_f32 v22, v20, v22, v38
	v_mul_f32_e32 v20, v14, v46
	v_fmac_f32_e32 v39, v20, v23
	v_med3_f32 v23, v28, s12, v154
	v_mov_b32_e32 v20, 0
	v_cvt_pk_fp8_f32 v20, v15, v23
	v_med3_f32 v15, v30, s12, v154
	v_med3_f32 v23, v21, s12, v154
	v_mov_b32_e32 v21, 0
	v_cvt_pk_fp8_f32 v21, v15, v23
	v_med3_f32 v28, v29, s12, v154
	v_med3_f32 v29, v31, s12, v154
	v_cvt_pk_fp8_f32 v20, v28, v29 op_sel:[0,0,1]
	v_med3_f32 v22, v22, s12, v154
	v_med3_f32 v28, v39, s12, v154
	v_fmac_f32_e32 v94, v109, v109
	v_cvt_pk_fp8_f32 v21, v22, v28 op_sel:[0,0,1]
	v_and_b32_e32 v111, 0xffff0000, v95
	v_fmac_f32_e32 v94, v110, v110
	v_fmac_f32_e32 v94, v111, v111
	s_waitcnt vmcnt(16)
	v_lshlrev_b32_e32 v112, 16, v84
	v_and_b32_e32 v113, 0xffff0000, v84
	v_fmac_f32_e32 v94, v112, v112
	v_lshlrev_b32_e32 v114, 16, v85
	v_fmac_f32_e32 v94, v113, v113
	global_store_dwordx2 v[12:13], v[20:21], off offset:1024
	v_and_b32_e32 v115, 0xffff0000, v85
	v_fmac_f32_e32 v94, v114, v114
	v_lshlrev_b32_e32 v15, 16, v4
	v_and_b32_e32 v28, 0xffff0000, v4
	v_lshlrev_b32_e32 v29, 16, v5
	v_and_b32_e32 v30, 0xffff0000, v5
	v_lshlrev_b32_e32 v31, 16, v6
	v_and_b32_e32 v36, 0xffff0000, v6
	v_lshlrev_b32_e32 v37, 16, v7
	v_and_b32_e32 v38, 0xffff0000, v7
	ds_read_b128 v[4:7], v144 offset:22528
	ds_read_b128 v[20:23], v144 offset:38912
	v_lshlrev_b32_e32 v116, 16, v86
	v_fmac_f32_e32 v94, v115, v115
	v_and_b32_e32 v117, 0xffff0000, v86
	v_fmac_f32_e32 v94, v116, v116
	v_lshlrev_b32_e32 v118, 16, v87
	v_fmac_f32_e32 v94, v117, v117
	v_and_b32_e32 v119, 0xffff0000, v87
	v_fmac_f32_e32 v94, v118, v118
	v_mul_f32_e32 v15, v14, v15
	v_fmac_f32_e32 v94, v119, v119
	s_waitcnt vmcnt(16)
	v_lshlrev_b32_e32 v129, 16, v76
	s_waitcnt lgkmcnt(0)
	v_fma_f32 v15, v15, v4, v20
	v_mul_f32_e32 v4, v14, v28
	v_and_b32_e32 v157, 0xffff0000, v76
	v_fmac_f32_e32 v94, v129, v129
	v_fma_f32 v20, v4, v5, v21
	v_mul_f32_e32 v4, v14, v29
	v_lshlrev_b32_e32 v158, 16, v77
	v_fmac_f32_e32 v94, v157, v157
	v_fma_f32 v21, v4, v6, v22
	v_mul_f32_e32 v4, v14, v30
	v_and_b32_e32 v159, 0xffff0000, v77
	v_fmac_f32_e32 v94, v158, v158
	v_fmac_f32_e32 v23, v4, v7
	v_mul_f32_e32 v22, v14, v31
	ds_read_b128 v[4:7], v144 offset:22544
	ds_read_b128 v[28:31], v144 offset:38928
	v_lshlrev_b32_e32 v160, 16, v78
	v_fmac_f32_e32 v94, v159, v159
	v_and_b32_e32 v92, 0xffff0000, v78
	v_fmac_f32_e32 v94, v160, v160
	v_lshlrev_b32_e32 v86, 16, v79
	v_fmac_f32_e32 v94, v92, v92
	v_and_b32_e32 v85, 0xffff0000, v79
	v_fmac_f32_e32 v94, v86, v86
	v_fmac_f32_e32 v94, v85, v85
	s_waitcnt vmcnt(15)
	v_lshlrev_b32_e32 v87, 16, v68
	s_waitcnt lgkmcnt(0)
	v_fma_f32 v22, v22, v4, v28
	v_mul_f32_e32 v4, v14, v36
	v_and_b32_e32 v84, 0xffff0000, v68
	v_fmac_f32_e32 v94, v87, v87
	v_and_b32_e32 v76, 0xffff0000, v69
	v_lshlrev_b32_e32 v77, 16, v69
	v_fma_f32 v5, v4, v5, v29
	v_mul_f32_e32 v4, v14, v37
	v_fmac_f32_e32 v94, v84, v84
	v_pk_mul_f32 v[68:69], v[76:77], v[76:77]
	v_fma_f32 v6, v4, v6, v30
	v_mul_f32_e32 v4, v14, v38
	v_add_f32_e32 v69, v69, v94
	v_and_b32_e32 v78, 0xffff0000, v70
	v_lshlrev_b32_e32 v79, 16, v70
	v_fmac_f32_e32 v31, v4, v7
	v_med3_f32 v7, v15, s12, v154
	v_med3_f32 v14, v20, s12, v154
	v_mov_b32_e32 v4, 0
	v_add_f32_e32 v94, v68, v69
	v_pk_mul_f32 v[68:69], v[78:79], v[78:79]
	v_cvt_pk_fp8_f32 v4, v7, v14
	v_med3_f32 v7, v22, s12, v154
	v_med3_f32 v14, v5, s12, v154
	v_mov_b32_e32 v5, 0
	v_add_f32_e32 v69, v69, v94
	v_cvt_pk_fp8_f32 v5, v7, v14
	v_add_f32_e32 v94, v68, v69
	v_and_b32_e32 v68, 0xffff0000, v71
	v_lshlrev_b32_e32 v69, 16, v71
	v_pk_mul_f32 v[70:71], v[68:69], v[68:69]
	v_med3_f32 v15, v21, s12, v154
	v_med3_f32 v20, v23, s12, v154
	v_add_f32_e32 v71, v71, v94
	v_cvt_pk_fp8_f32 v4, v15, v20 op_sel:[0,0,1]
	v_med3_f32 v6, v6, s12, v154
	v_med3_f32 v15, v31, s12, v154
	v_add_f32_e32 v70, v70, v71
	v_cvt_pk_fp8_f32 v5, v6, v15 op_sel:[0,0,1]
	s_or_b32 s20, s0, 6
	v_add_f32_dpp v70, v70, v70 quad_perm:[1,0,3,2] row_mask:0xf bank_mask:0xf bound_ctrl:1
	s_mov_b32 s21, s1
	s_lshl_b64 s[8:9], s[20:21], 12
	v_add_f32_dpp v70, v70, v70 quad_perm:[2,3,0,1] row_mask:0xf bank_mask:0xf bound_ctrl:1
	s_lshl_b64 s[22:23], s[20:21], 13
	v_readlane_b32 s36, v253, 10
	v_add_f32_dpp v70, v70, v70 row_ror:4 row_mask:0xf bank_mask:0xf bound_ctrl:1
	v_readlane_b32 s37, v253, 11
	s_add_u32 s22, s36, s22
	v_add_f32_dpp v70, v70, v70 row_ror:8 row_mask:0xf bank_mask:0xf bound_ctrl:1
	global_store_dwordx2 v[12:13], v[4:5], off offset:1536
	v_lshl_add_u64 v[4:5], v[130:131], 0, s[8:9]
	s_addc_u32 s23, s37, s23
	v_readlane_b32 s3, v70, 16
	v_readlane_b32 s28, v70, 48
	global_load_dwordx4 v[88:91], v[4:5], off
	global_load_dwordx4 v[80:83], v[4:5], off offset:1024
	global_load_dwordx4 v[72:75], v[4:5], off offset:2048
	global_load_dwordx4 v[64:67], v[4:5], off offset:3072
	global_load_dwordx4 v[48:51], v122, s[22:23] offset:16
	global_load_dwordx4 v[56:59], v122, s[22:23]
	global_load_dwordx4 v[36:39], v122, s[22:23] offset:2064
	global_load_dwordx4 v[44:47], v122, s[22:23] offset:2048
	global_load_dwordx4 v[20:23], v149, s[22:23] offset:16
	global_load_dwordx4 v[28:31], v149, s[22:23]
	global_load_dwordx4 v[4:7], v150, s[22:23] offset:16
	global_load_dwordx4 v[12:15], v150, s[22:23]
	v_readlane_b32 s22, v70, 0
	v_readlane_b32 s23, v70, 32
	v_mov_b32_e32 v70, s3
	v_mov_b32_e32 v71, s28
	v_pk_add_f32 v[70:71], s[22:23], v[70:71]
	ds_read_b128 v[94:97], v144
	ds_read_b128 v[98:101], v144 offset:16
	v_add_f32_e32 v70, v70, v71
	v_fmamk_f32 v70, v70, 0x3a000000, v151
	v_cmp_gt_f32_e32 vcc, s11, v70
	v_mul_f32_e32 v71, 0x4b800000, v70
	v_readlane_b32 s38, v253, 12
	v_cndmask_b32_e32 v70, v70, v71, vcc
	v_rsq_f32_e32 v70, v70
	v_readlane_b32 s39, v253, 13
	v_readlane_b32 s40, v253, 14
	v_readlane_b32 s41, v253, 15
	v_mul_f32_e32 v71, 0x45800000, v70
	v_cndmask_b32_e32 v70, v70, v71, vcc
	v_mul_f32_e32 v71, v70, v102
	ds_read_b128 v[102:105], v144 offset:8192
	v_mul_f32_e32 v93, v70, v93
	v_readlane_b32 s42, v253, 16
	v_readlane_b32 s43, v253, 17
	v_readlane_b32 s44, v253, 18
	s_waitcnt lgkmcnt(0)
	v_mul_f32_e32 v71, v102, v71
	s_waitcnt vmcnt(26)
	v_fma_f32 v60, v94, v71, v60
	v_mul_f32_e32 v71, v70, v106
	v_mul_f32_e32 v94, v70, v107
	v_mul_f32_e32 v71, v103, v71
	v_mul_f32_e32 v94, v104, v94
	v_mul_f32_e32 v93, v105, v93
	v_fma_f32 v61, v95, v71, v61
	v_fma_f32 v62, v96, v94, v62
	v_fmac_f32_e32 v63, v97, v93
	ds_read_b128 v[94:97], v144 offset:8208
	v_mul_f32_e32 v93, v70, v108
	v_mul_f32_e32 v71, v61, v61
	v_fmac_f32_e32 v71, v60, v60
	v_fmac_f32_e32 v71, v62, v62
	s_waitcnt lgkmcnt(0)
	v_mul_f32_e32 v93, v93, v94
	v_fma_f32 v93, v98, v93, v52
	v_mul_f32_e32 v52, v70, v109
	v_mul_f32_e32 v52, v52, v95
	v_fma_f32 v94, v99, v52, v53
	v_mul_f32_e32 v52, v70, v110
	v_fmac_f32_e32 v71, v63, v63
	v_mul_f32_e32 v52, v52, v96
	v_fmac_f32_e32 v71, v93, v93
	v_fma_f32 v95, v100, v52, v54
	v_mul_f32_e32 v52, v70, v111
	v_fmac_f32_e32 v71, v94, v94
	v_mul_f32_e32 v52, v52, v97
	v_fmac_f32_e32 v71, v95, v95
	v_fmac_f32_e32 v55, v101, v52
	v_cvt_pk_bf16_f32 v52, v60, v61
	v_lshl_add_u64 v[60:61], v[132:133], 0, s[26:27]
	v_fmac_f32_e32 v71, v55, v55
	v_cvt_pk_bf16_f32 v53, v62, v63
	v_cvt_pk_bf16_f32 v54, v93, v94
	v_cvt_pk_bf16_f32 v55, v95, v55
	global_store_dwordx4 v[60:61], v[52:55], off
	ds_read_b128 v[94:97], v144 offset:2048
	ds_read_b128 v[98:101], v144 offset:2064
	ds_read_b128 v[102:105], v144 offset:10240
	v_mul_f32_e32 v62, v70, v112
	v_readlane_b32 s45, v253, 19
	v_readlane_b32 s46, v253, 20
	v_readlane_b32 s47, v253, 21
	s_waitcnt lgkmcnt(0)
	v_mul_f32_e32 v62, v62, v102
	s_waitcnt vmcnt(25)
	v_fma_f32 v40, v94, v62, v40
	v_mul_f32_e32 v62, v70, v113
	v_mul_f32_e32 v62, v62, v103
	v_fma_f32 v41, v95, v62, v41
	v_mul_f32_e32 v62, v70, v114
	v_mul_f32_e32 v62, v62, v104
	v_fma_f32 v42, v96, v62, v42
	v_mul_f32_e32 v62, v70, v115
	v_mul_f32_e32 v62, v62, v105
	v_fmac_f32_e32 v43, v97, v62
	ds_read_b128 v[94:97], v144 offset:10256
	v_mul_f32_e32 v62, v70, v116
	v_fmac_f32_e32 v71, v40, v40
	v_fmac_f32_e32 v71, v41, v41
	v_fmac_f32_e32 v71, v42, v42
	s_waitcnt lgkmcnt(0)
	v_mul_f32_e32 v62, v62, v94
	v_fma_f32 v62, v98, v62, v32
	v_mul_f32_e32 v32, v70, v117
	v_mul_f32_e32 v32, v32, v95
	v_fma_f32 v63, v99, v32, v33
	v_mul_f32_e32 v32, v70, v118
	v_fmac_f32_e32 v71, v43, v43
	v_mul_f32_e32 v32, v32, v96
	v_fmac_f32_e32 v71, v62, v62
	v_fma_f32 v93, v100, v32, v34
	v_mul_f32_e32 v32, v70, v119
	v_fmac_f32_e32 v71, v63, v63
	v_mul_f32_e32 v32, v32, v97
	v_fmac_f32_e32 v71, v93, v93
	v_fmac_f32_e32 v35, v101, v32
	v_fmac_f32_e32 v71, v35, v35
	v_cvt_pk_bf16_f32 v32, v40, v41
	v_cvt_pk_bf16_f32 v33, v42, v43
	v_cvt_pk_bf16_f32 v34, v62, v63
	v_cvt_pk_bf16_f32 v35, v93, v35
	global_store_dwordx4 v[60:61], v[32:35], off offset:1024
	ds_read_b128 v[40:43], v144 offset:4096
	ds_read_b128 v[94:97], v144 offset:4112
	ds_read_b128 v[98:101], v144 offset:12288
	v_mul_f32_e32 v62, v70, v129
	v_readlane_b32 s48, v253, 22
	v_readlane_b32 s49, v253, 23
	v_readlane_b32 s50, v253, 24
	s_waitcnt lgkmcnt(0)
	v_mul_f32_e32 v62, v62, v98
	s_waitcnt vmcnt(24)
	v_fma_f32 v24, v40, v62, v24
	v_mul_f32_e32 v40, v70, v157
	v_mul_f32_e32 v40, v40, v99
	v_fma_f32 v25, v41, v40, v25
	v_mul_f32_e32 v40, v70, v158
	v_mul_f32_e32 v40, v40, v100
	v_fma_f32 v26, v42, v40, v26
	v_mul_f32_e32 v40, v70, v159
	v_mul_f32_e32 v40, v40, v101
	v_fmac_f32_e32 v27, v43, v40
	ds_read_b128 v[40:43], v144 offset:12304
	v_mul_f32_e32 v62, v70, v160
	v_fmac_f32_e32 v71, v24, v24
	v_fmac_f32_e32 v71, v25, v25
	v_fmac_f32_e32 v71, v26, v26
	s_waitcnt lgkmcnt(0)
	v_mul_f32_e32 v40, v62, v40
	v_fma_f32 v40, v94, v40, v16
	v_mul_f32_e32 v16, v70, v92
	v_mul_f32_e32 v16, v16, v41
	v_fma_f32 v41, v95, v16, v17
	v_mul_f32_e32 v16, v70, v86
	v_fmac_f32_e32 v71, v27, v27
	v_mul_f32_e32 v16, v16, v42
	v_fmac_f32_e32 v71, v40, v40
	v_fma_f32 v42, v96, v16, v18
	v_mul_f32_e32 v16, v70, v85
	v_fmac_f32_e32 v71, v41, v41
	v_mul_f32_e32 v16, v16, v43
	v_fmac_f32_e32 v71, v42, v42
	v_fmac_f32_e32 v19, v97, v16
	v_fmac_f32_e32 v71, v19, v19
	v_cvt_pk_bf16_f32 v16, v24, v25
	v_cvt_pk_bf16_f32 v17, v26, v27
	v_cvt_pk_bf16_f32 v18, v40, v41
	v_cvt_pk_bf16_f32 v19, v42, v19
	global_store_dwordx4 v[60:61], v[16:19], off offset:2048
	ds_read_b128 v[24:27], v144 offset:6144
	ds_read_b128 v[40:43], v144 offset:6160
	ds_read_b128 v[92:95], v144 offset:14336
	v_mul_f32_e32 v62, v70, v87
	v_readlane_b32 s51, v253, 25
	s_waitcnt lgkmcnt(0)
	v_mul_f32_e32 v62, v62, v92
	s_waitcnt vmcnt(23)
	v_fma_f32 v62, v24, v62, v8
	v_mul_f32_e32 v8, v70, v84
	v_mul_f32_e32 v8, v8, v93
	v_fmac_f32_e32 v71, v62, v62
	v_fma_f32 v63, v25, v8, v9
	v_fmac_f32_e32 v71, v63, v63
	v_pk_mul_f32 v[8:9], v[70:71], v[76:77] op_sel_hi:[0,1]
	v_pk_mul_f32 v[8:9], v[8:9], v[94:95] op_sel:[1,0] op_sel_hi:[0,1]
	v_pk_fma_f32 v[24:25], v[26:27], v[8:9], v[10:11]
	s_nop 0
	v_pk_mul_f32 v[8:9], v[24:25], v[24:25]
	s_nop 0
	v_add_f32_e32 v8, v71, v8
	v_add_f32_e32 v71, v8, v9
	ds_read_b128 v[8:11], v144 offset:14352
	v_pk_mul_f32 v[26:27], v[70:71], v[78:79] op_sel_hi:[0,1]
	s_waitcnt lgkmcnt(0)
	v_pk_mul_f32 v[8:9], v[26:27], v[8:9] op_sel:[1,0] op_sel_hi:[0,1]
	v_pk_fma_f32 v[8:9], v[40:41], v[8:9], v[0:1]
	s_nop 0
	v_pk_mul_f32 v[0:1], v[8:9], v[8:9]
	s_nop 0
	v_add_f32_e32 v0, v71, v0
	v_add_f32_e32 v26, v0, v1
	v_pk_mul_f32 v[0:1], v[70:71], v[68:69] op_sel_hi:[0,1]
	v_pk_mul_f32 v[0:1], v[0:1], v[10:11] op_sel:[1,0] op_sel_hi:[0,1]
	v_pk_fma_f32 v[10:11], v[42:43], v[0:1], v[2:3]
	s_nop 0
	v_pk_mul_f32 v[0:1], v[10:11], v[10:11]
	s_nop 0
	v_add_f32_e32 v0, v26, v0
	v_add_f32_e32 v26, v0, v1
	v_cvt_pk_bf16_f32 v0, v62, v63
	v_cvt_pk_bf16_f32 v1, v24, v25
	v_cvt_pk_bf16_f32 v2, v8, v9
	v_cvt_pk_bf16_f32 v3, v10, v11
	global_store_dwordx4 v[60:61], v[0:3], off offset:3072
	s_nop 0
	v_add_f32_dpp v8, v26, v26 quad_perm:[1,0,3,2] row_mask:0xf bank_mask:0xf bound_ctrl:1
	s_nop 1
	v_add_f32_dpp v8, v8, v8 quad_perm:[2,3,0,1] row_mask:0xf bank_mask:0xf bound_ctrl:1
	s_nop 1
	v_add_f32_dpp v8, v8, v8 row_ror:4 row_mask:0xf bank_mask:0xf bound_ctrl:1
	s_nop 1
	v_add_f32_dpp v8, v8, v8 row_ror:8 row_mask:0xf bank_mask:0xf bound_ctrl:1
	s_nop 0
	v_readlane_b32 s3, v8, 16
	v_readlane_b32 s26, v8, 48
	v_readlane_b32 s22, v8, 0
	v_readlane_b32 s23, v8, 32
	v_mov_b32_e32 v8, s3
	v_mov_b32_e32 v9, s26
	v_pk_add_f32 v[8:9], s[22:23], v[8:9]
	s_nop 0
	v_add_f32_e32 v8, v8, v9
	v_fmamk_f32 v8, v8, 0x3a000000, v151
	v_cmp_gt_f32_e32 vcc, s11, v8
	v_mul_f32_e32 v9, 0x4b800000, v8
	s_nop 0
	v_cndmask_b32_e32 v8, v8, v9, vcc
	v_rsq_f32_e32 v8, v8
	s_nop 0
	v_mul_f32_e32 v9, 0x45800000, v8
	v_cndmask_b32_e32 v10, v8, v9, vcc
	s_and_saveexec_b64 s[22:23], s[6:7]
	v_mov_b32_e32 v8, s10
	ds_write_b32 v8, v10 offset:60692
	s_or_b64 exec, exec, s[22:23]
	v_lshlrev_b32_e32 v8, 16, v52
	v_and_b32_e32 v9, 0xffff0000, v52
	v_lshlrev_b32_e32 v11, 16, v53
	v_and_b32_e32 v60, 0xffff0000, v53
	v_lshlrev_b32_e32 v61, 16, v54
	v_and_b32_e32 v62, 0xffff0000, v54
	v_lshlrev_b32_e32 v63, 16, v55
	v_and_b32_e32 v68, 0xffff0000, v55
	ds_read_b128 v[24:27], v144 offset:16384
	ds_read_b128 v[40:43], v144 offset:16400
	ds_read_b128 v[52:55], v144 offset:32768
	v_mul_f32_e32 v8, v10, v8
	v_mul_f32_e32 v9, v10, v9
	v_mul_f32_e32 v11, v10, v11
	s_lshl_b64 s[22:23], s[24:25], 11
	s_waitcnt lgkmcnt(0)
	v_fma_f32 v8, v8, v24, v52
	v_mul_f32_e32 v24, v10, v60
	v_fma_f32 v9, v9, v25, v53
	v_fma_f32 v11, v11, v26, v54
	v_fmac_f32_e32 v55, v24, v27
	ds_read_b128 v[24:27], v144 offset:32784
	v_mul_f32_e32 v52, v10, v61
	v_med3_f32 v8, v8, s12, v154
	v_med3_f32 v9, v9, s12, v154
	v_med3_f32 v11, v11, s12, v154
	s_waitcnt lgkmcnt(0)
	v_fma_f32 v40, v52, v40, v24
	v_mul_f32_e32 v24, v10, v62
	v_fma_f32 v25, v24, v41, v25
	v_mul_f32_e32 v24, v10, v63
	v_fma_f32 v26, v24, v42, v26
	v_mul_f32_e32 v24, v10, v68
	v_fmac_f32_e32 v27, v24, v43
	v_mov_b32_e32 v24, 0
	v_cvt_pk_fp8_f32 v24, v8, v9
	v_med3_f32 v8, v40, s12, v154
	v_med3_f32 v9, v25, s12, v154
	v_mov_b32_e32 v25, 0
	v_cvt_pk_fp8_f32 v25, v8, v9
	v_med3_f32 v41, v55, s12, v154
	v_cvt_pk_fp8_f32 v24, v11, v41 op_sel:[0,0,1]
	v_med3_f32 v11, v26, s12, v154
	v_med3_f32 v26, v27, s12, v154
	v_cvt_pk_fp8_f32 v25, v11, v26 op_sel:[0,0,1]
	v_lshl_add_u64 v[8:9], v[134:135], 0, s[22:23]
	v_lshlrev_b32_e32 v11, 16, v32
	v_and_b32_e32 v40, 0xffff0000, v32
	global_store_dwordx2 v[8:9], v[24:25], off
	v_lshlrev_b32_e32 v41, 16, v33
	v_and_b32_e32 v42, 0xffff0000, v33
	v_lshlrev_b32_e32 v43, 16, v34
	v_and_b32_e32 v52, 0xffff0000, v34
	v_lshlrev_b32_e32 v53, 16, v35
	v_and_b32_e32 v54, 0xffff0000, v35
	ds_read_b128 v[24:27], v144 offset:18432
	ds_read_b128 v[32:35], v144 offset:34816
	v_mul_f32_e32 v11, v10, v11
	s_waitcnt vmcnt(16)
	v_and_b32_e32 v108, 0xffff0000, v88
	v_lshlrev_b32_e32 v104, 16, v88
	v_mul_f32_e32 v96, v108, v108
	s_waitcnt lgkmcnt(0)
	v_fma_f32 v11, v11, v24, v32
	v_mul_f32_e32 v24, v10, v40
	v_fma_f32 v32, v24, v25, v33
	v_mul_f32_e32 v24, v10, v41
	v_fma_f32 v33, v24, v26, v34
	v_mul_f32_e32 v24, v10, v42
	v_fmac_f32_e32 v35, v24, v27
	v_mul_f32_e32 v34, v10, v43
	ds_read_b128 v[24:27], v144 offset:18448
	ds_read_b128 v[40:43], v144 offset:34832
	v_med3_f32 v11, v11, s12, v154
	v_lshlrev_b32_e32 v109, 16, v89
	v_fmac_f32_e32 v96, v104, v104
	v_and_b32_e32 v89, 0xffff0000, v89
	s_waitcnt lgkmcnt(0)
	v_fma_f32 v34, v34, v24, v40
	v_mul_f32_e32 v24, v10, v52
	v_fma_f32 v25, v24, v25, v41
	v_mul_f32_e32 v24, v10, v53
	v_fma_f32 v26, v24, v26, v42
	v_mul_f32_e32 v24, v10, v54
	v_fmac_f32_e32 v43, v24, v27
	v_med3_f32 v27, v32, s12, v154
	v_mov_b32_e32 v24, 0
	v_cvt_pk_fp8_f32 v24, v11, v27
	v_med3_f32 v11, v34, s12, v154
	v_med3_f32 v27, v25, s12, v154
	v_mov_b32_e32 v25, 0
	v_cvt_pk_fp8_f32 v25, v11, v27
	v_med3_f32 v32, v33, s12, v154
	v_med3_f32 v33, v35, s12, v154
	v_cvt_pk_fp8_f32 v24, v32, v33 op_sel:[0,0,1]
	v_med3_f32 v26, v26, s12, v154
	v_med3_f32 v32, v43, s12, v154
	v_cvt_pk_fp8_f32 v25, v26, v32 op_sel:[0,0,1]
	v_lshlrev_b32_e32 v11, 16, v16
	v_and_b32_e32 v32, 0xffff0000, v16
	v_lshlrev_b32_e32 v33, 16, v17
	global_store_dwordx2 v[8:9], v[24:25], off offset:512
	v_and_b32_e32 v34, 0xffff0000, v17
	v_lshlrev_b32_e32 v35, 16, v18
	v_and_b32_e32 v40, 0xffff0000, v18
	v_lshlrev_b32_e32 v41, 16, v19
	v_and_b32_e32 v42, 0xffff0000, v19
	ds_read_b128 v[16:19], v144 offset:20480
	ds_read_b128 v[24:27], v144 offset:36864
	v_mul_f32_e32 v11, v10, v11
	v_fmac_f32_e32 v96, v109, v109
	v_lshlrev_b32_e32 v110, 16, v90
	v_fmac_f32_e32 v96, v89, v89
	s_waitcnt lgkmcnt(0)
	v_fma_f32 v11, v11, v16, v24
	v_mul_f32_e32 v16, v10, v32
	v_fma_f32 v24, v16, v17, v25
	v_mul_f32_e32 v16, v10, v33
	v_fma_f32 v25, v16, v18, v26
	v_mul_f32_e32 v16, v10, v34
	v_fmac_f32_e32 v27, v16, v19
	v_mul_f32_e32 v26, v10, v35
	ds_read_b128 v[16:19], v144 offset:20496
	ds_read_b128 v[32:35], v144 offset:36880
	v_med3_f32 v11, v11, s12, v154
	v_and_b32_e32 v90, 0xffff0000, v90
	v_fmac_f32_e32 v96, v110, v110
	v_lshlrev_b32_e32 v111, 16, v91
	s_waitcnt lgkmcnt(0)
	v_fma_f32 v26, v26, v16, v32
	v_mul_f32_e32 v16, v10, v40
	v_fma_f32 v17, v16, v17, v33
	v_mul_f32_e32 v16, v10, v41
	v_fma_f32 v18, v16, v18, v34
	v_mul_f32_e32 v16, v10, v42
	v_fmac_f32_e32 v35, v16, v19
	v_med3_f32 v19, v24, s12, v154
	v_mov_b32_e32 v16, 0
	v_cvt_pk_fp8_f32 v16, v11, v19
	v_med3_f32 v11, v26, s12, v154
	v_med3_f32 v19, v17, s12, v154
	v_mov_b32_e32 v17, 0
	v_cvt_pk_fp8_f32 v17, v11, v19
	v_med3_f32 v24, v25, s12, v154
	v_med3_f32 v25, v27, s12, v154
	v_cvt_pk_fp8_f32 v16, v24, v25 op_sel:[0,0,1]
	v_med3_f32 v18, v18, s12, v154
	v_med3_f32 v24, v35, s12, v154
	v_fmac_f32_e32 v96, v90, v90
	v_cvt_pk_fp8_f32 v17, v18, v24 op_sel:[0,0,1]
	v_and_b32_e32 v91, 0xffff0000, v91
	v_fmac_f32_e32 v96, v111, v111
	v_fmac_f32_e32 v96, v91, v91
	s_waitcnt vmcnt(16)
	v_lshlrev_b32_e32 v112, 16, v80
	v_and_b32_e32 v113, 0xffff0000, v80
	v_fmac_f32_e32 v96, v112, v112
	v_lshlrev_b32_e32 v114, 16, v81
	v_fmac_f32_e32 v96, v113, v113
	global_store_dwordx2 v[8:9], v[16:17], off offset:1024
	v_and_b32_e32 v115, 0xffff0000, v81
	v_fmac_f32_e32 v96, v114, v114
	v_lshlrev_b32_e32 v11, 16, v0
	v_and_b32_e32 v24, 0xffff0000, v0
	v_lshlrev_b32_e32 v25, 16, v1
	v_and_b32_e32 v26, 0xffff0000, v1
	v_lshlrev_b32_e32 v27, 16, v2
	v_and_b32_e32 v32, 0xffff0000, v2
	v_lshlrev_b32_e32 v33, 16, v3
	v_and_b32_e32 v34, 0xffff0000, v3
	ds_read_b128 v[0:3], v144 offset:22528
	ds_read_b128 v[16:19], v144 offset:38912
	v_lshlrev_b32_e32 v116, 16, v82
	v_fmac_f32_e32 v96, v115, v115
	v_and_b32_e32 v117, 0xffff0000, v82
	v_fmac_f32_e32 v96, v116, v116
	v_lshlrev_b32_e32 v118, 16, v83
	v_fmac_f32_e32 v96, v117, v117
	v_and_b32_e32 v119, 0xffff0000, v83
	v_fmac_f32_e32 v96, v118, v118
	v_mul_f32_e32 v11, v10, v11
	v_fmac_f32_e32 v96, v119, v119
	s_waitcnt vmcnt(16)
	v_lshlrev_b32_e32 v129, 16, v72
	s_waitcnt lgkmcnt(0)
	v_fma_f32 v11, v11, v0, v16
	v_mul_f32_e32 v0, v10, v24
	v_and_b32_e32 v157, 0xffff0000, v72
	v_fmac_f32_e32 v96, v129, v129
	v_fma_f32 v16, v0, v1, v17
	v_mul_f32_e32 v0, v10, v25
	v_lshlrev_b32_e32 v158, 16, v73
	v_fmac_f32_e32 v96, v157, v157
	v_fma_f32 v17, v0, v2, v18
	v_mul_f32_e32 v0, v10, v26
	v_and_b32_e32 v159, 0xffff0000, v73
	v_fmac_f32_e32 v96, v158, v158
	v_fmac_f32_e32 v19, v0, v3
	v_mul_f32_e32 v18, v10, v27
	ds_read_b128 v[0:3], v144 offset:22544
	ds_read_b128 v[24:27], v144 offset:38928
	v_lshlrev_b32_e32 v160, 16, v74
	v_fmac_f32_e32 v96, v159, v159
	v_and_b32_e32 v88, 0xffff0000, v74
	v_fmac_f32_e32 v96, v160, v160
	v_lshlrev_b32_e32 v82, 16, v75
	v_fmac_f32_e32 v96, v88, v88
	v_and_b32_e32 v81, 0xffff0000, v75
	v_fmac_f32_e32 v96, v82, v82
	v_fmac_f32_e32 v96, v81, v81
	s_waitcnt vmcnt(15)
	v_lshlrev_b32_e32 v83, 16, v64
	s_waitcnt lgkmcnt(0)
	v_fma_f32 v18, v18, v0, v24
	v_mul_f32_e32 v0, v10, v32
	v_and_b32_e32 v80, 0xffff0000, v64
	v_fmac_f32_e32 v96, v83, v83
	v_and_b32_e32 v72, 0xffff0000, v65
	v_lshlrev_b32_e32 v73, 16, v65
	v_fma_f32 v1, v0, v1, v25
	v_mul_f32_e32 v0, v10, v33
	v_fmac_f32_e32 v96, v80, v80
	v_pk_mul_f32 v[64:65], v[72:73], v[72:73]
	v_fma_f32 v2, v0, v2, v26
	v_mul_f32_e32 v0, v10, v34
	v_add_f32_e32 v65, v65, v96
	v_and_b32_e32 v74, 0xffff0000, v66
	v_lshlrev_b32_e32 v75, 16, v66
	v_fmac_f32_e32 v27, v0, v3
	v_med3_f32 v3, v11, s12, v154
	v_med3_f32 v10, v16, s12, v154
	v_mov_b32_e32 v0, 0
	v_add_f32_e32 v96, v64, v65
	v_pk_mul_f32 v[64:65], v[74:75], v[74:75]
	v_cvt_pk_fp8_f32 v0, v3, v10
	v_med3_f32 v3, v18, s12, v154
	v_med3_f32 v10, v1, s12, v154
	v_mov_b32_e32 v1, 0
	v_add_f32_e32 v65, v65, v96
	v_cvt_pk_fp8_f32 v1, v3, v10
	v_add_f32_e32 v96, v64, v65
	v_and_b32_e32 v64, 0xffff0000, v67
	v_lshlrev_b32_e32 v65, 16, v67
	v_pk_mul_f32 v[66:67], v[64:65], v[64:65]
	v_med3_f32 v11, v17, s12, v154
	v_med3_f32 v16, v19, s12, v154
	v_add_f32_e32 v67, v67, v96
	v_cvt_pk_fp8_f32 v0, v11, v16 op_sel:[0,0,1]
	v_med3_f32 v2, v2, s12, v154
	v_med3_f32 v11, v27, s12, v154
	v_add_f32_e32 v66, v66, v67
	v_cvt_pk_fp8_f32 v1, v2, v11 op_sel:[0,0,1]
	s_or_b32 s0, s0, 7
	v_add_f32_dpp v66, v66, v66 quad_perm:[1,0,3,2] row_mask:0xf bank_mask:0xf bound_ctrl:1
	s_lshl_b64 s[22:23], s[0:1], 12
	s_lshl_b64 s[24:25], s[0:1], 13
	v_add_f32_dpp v66, v66, v66 quad_perm:[2,3,0,1] row_mask:0xf bank_mask:0xf bound_ctrl:1
	v_readlane_b32 s36, v253, 10
	v_readlane_b32 s37, v253, 11
	v_add_f32_dpp v66, v66, v66 row_ror:4 row_mask:0xf bank_mask:0xf bound_ctrl:1
	s_add_u32 s24, s36, s24
	global_store_dwordx2 v[8:9], v[0:1], off offset:1536
	v_add_f32_dpp v66, v66, v66 row_ror:8 row_mask:0xf bank_mask:0xf bound_ctrl:1
	v_lshl_add_u64 v[0:1], v[130:131], 0, s[22:23]
	s_addc_u32 s25, s37, s25
	v_readlane_b32 s3, v66, 16
	v_readlane_b32 s26, v66, 48
	global_load_dwordx4 v[92:95], v[0:1], off
	global_load_dwordx4 v[84:87], v[0:1], off offset:1024
	global_load_dwordx4 v[76:79], v[0:1], off offset:2048
	global_load_dwordx4 v[68:71], v[0:1], off offset:3072
	global_load_dwordx4 v[52:55], v122, s[24:25] offset:16
	global_load_dwordx4 v[60:63], v122, s[24:25]
	global_load_dwordx4 v[32:35], v122, s[24:25] offset:2064
	global_load_dwordx4 v[40:43], v122, s[24:25] offset:2048
	global_load_dwordx4 v[16:19], v149, s[24:25] offset:16
	global_load_dwordx4 v[24:27], v149, s[24:25]
	global_load_dwordx4 v[0:3], v150, s[24:25] offset:16
	global_load_dwordx4 v[8:11], v150, s[24:25]
	v_readlane_b32 s24, v66, 0
	v_readlane_b32 s25, v66, 32
	v_mov_b32_e32 v66, s3
	v_mov_b32_e32 v67, s26
	v_pk_add_f32 v[66:67], s[24:25], v[66:67]
	ds_read_b128 v[96:99], v144
	ds_read_b128 v[100:103], v144 offset:16
	v_add_f32_e32 v66, v66, v67
	v_fmamk_f32 v66, v66, 0x3a000000, v151
	v_cmp_gt_f32_e32 vcc, s11, v66
	v_mul_f32_e32 v67, 0x4b800000, v66
	v_readlane_b32 s38, v253, 12
	v_cndmask_b32_e32 v66, v66, v67, vcc
	v_rsq_f32_e32 v66, v66
	v_readlane_b32 s39, v253, 13
	v_readlane_b32 s40, v253, 14
	v_readlane_b32 s41, v253, 15
	v_mul_f32_e32 v67, 0x45800000, v66
	v_cndmask_b32_e32 v66, v66, v67, vcc
	v_mul_f32_e32 v67, v66, v104
	ds_read_b128 v[104:107], v144 offset:8192
	v_mul_f32_e32 v89, v66, v89
	v_readlane_b32 s42, v253, 16
	v_readlane_b32 s43, v253, 17
	v_readlane_b32 s44, v253, 18
	s_waitcnt lgkmcnt(0)
	v_mul_f32_e32 v67, v104, v67
	s_waitcnt vmcnt(26)
	v_fma_f32 v56, v96, v67, v56
	v_mul_f32_e32 v67, v66, v108
	v_mul_f32_e32 v96, v66, v109
	v_mul_f32_e32 v67, v105, v67
	v_mul_f32_e32 v96, v106, v96
	v_mul_f32_e32 v89, v107, v89
	v_fma_f32 v57, v97, v67, v57
	v_fma_f32 v58, v98, v96, v58
	v_fmac_f32_e32 v59, v99, v89
	ds_read_b128 v[96:99], v144 offset:8208
	v_mul_f32_e32 v89, v66, v110
	v_mul_f32_e32 v67, v57, v57
	v_fmac_f32_e32 v67, v56, v56
	v_fmac_f32_e32 v67, v58, v58
	s_waitcnt lgkmcnt(0)
	v_mul_f32_e32 v89, v89, v96
	v_fma_f32 v89, v100, v89, v48
	v_mul_f32_e32 v48, v66, v90
	v_mul_f32_e32 v48, v48, v97
	v_fma_f32 v90, v101, v48, v49
	v_mul_f32_e32 v48, v66, v111
	v_fmac_f32_e32 v67, v59, v59
	v_mul_f32_e32 v48, v48, v98
	v_fmac_f32_e32 v67, v89, v89
	v_fma_f32 v96, v102, v48, v50
	v_mul_f32_e32 v48, v66, v91
	v_fmac_f32_e32 v67, v90, v90
	v_mul_f32_e32 v48, v48, v99
	v_fmac_f32_e32 v67, v96, v96
	v_fmac_f32_e32 v51, v103, v48
	v_cvt_pk_bf16_f32 v48, v56, v57
	v_lshl_add_u64 v[56:57], v[132:133], 0, s[8:9]
	v_fmac_f32_e32 v67, v51, v51
	v_cvt_pk_bf16_f32 v49, v58, v59
	v_cvt_pk_bf16_f32 v50, v89, v90
	v_cvt_pk_bf16_f32 v51, v96, v51
	global_store_dwordx4 v[56:57], v[48:51], off
	ds_read_b128 v[96:99], v144 offset:2048
	ds_read_b128 v[100:103], v144 offset:2064
	ds_read_b128 v[104:107], v144 offset:10240
	v_mul_f32_e32 v58, v66, v112
	v_readlane_b32 s45, v253, 19
	v_readlane_b32 s46, v253, 20
	v_readlane_b32 s47, v253, 21
	s_waitcnt lgkmcnt(0)
	v_mul_f32_e32 v58, v58, v104
	s_waitcnt vmcnt(25)
	v_fma_f32 v44, v96, v58, v44
	v_mul_f32_e32 v58, v66, v113
	v_mul_f32_e32 v58, v58, v105
	v_fma_f32 v45, v97, v58, v45
	v_mul_f32_e32 v58, v66, v114
	v_mul_f32_e32 v58, v58, v106
	v_fma_f32 v46, v98, v58, v46
	v_mul_f32_e32 v58, v66, v115
	v_mul_f32_e32 v58, v58, v107
	v_fmac_f32_e32 v47, v99, v58
	ds_read_b128 v[96:99], v144 offset:10256
	v_mul_f32_e32 v58, v66, v116
	v_fmac_f32_e32 v67, v44, v44
	v_fmac_f32_e32 v67, v45, v45
	v_fmac_f32_e32 v67, v46, v46
	s_waitcnt lgkmcnt(0)
	v_mul_f32_e32 v58, v58, v96
	v_fma_f32 v58, v100, v58, v36
	v_mul_f32_e32 v36, v66, v117
	v_mul_f32_e32 v36, v36, v97
	v_fma_f32 v59, v101, v36, v37
	v_mul_f32_e32 v36, v66, v118
	v_fmac_f32_e32 v67, v47, v47
	v_mul_f32_e32 v36, v36, v98
	v_fmac_f32_e32 v67, v58, v58
	v_fma_f32 v89, v102, v36, v38
	v_mul_f32_e32 v36, v66, v119
	v_fmac_f32_e32 v67, v59, v59
	v_mul_f32_e32 v36, v36, v99
	v_fmac_f32_e32 v67, v89, v89
	v_fmac_f32_e32 v39, v103, v36
	v_fmac_f32_e32 v67, v39, v39
	v_cvt_pk_bf16_f32 v36, v44, v45
	v_cvt_pk_bf16_f32 v37, v46, v47
	v_cvt_pk_bf16_f32 v38, v58, v59
	v_cvt_pk_bf16_f32 v39, v89, v39
	global_store_dwordx4 v[56:57], v[36:39], off offset:1024
	ds_read_b128 v[44:47], v144 offset:4096
	ds_read_b128 v[96:99], v144 offset:4112
	ds_read_b128 v[100:103], v144 offset:12288
	v_mul_f32_e32 v58, v66, v129
	v_readlane_b32 s48, v253, 22
	v_readlane_b32 s49, v253, 23
	v_readlane_b32 s50, v253, 24
	s_waitcnt lgkmcnt(0)
	v_mul_f32_e32 v58, v58, v100
	s_waitcnt vmcnt(24)
	v_fma_f32 v28, v44, v58, v28
	v_mul_f32_e32 v44, v66, v157
	v_mul_f32_e32 v44, v44, v101
	v_fma_f32 v29, v45, v44, v29
	v_mul_f32_e32 v44, v66, v158
	v_mul_f32_e32 v44, v44, v102
	v_fma_f32 v30, v46, v44, v30
	v_mul_f32_e32 v44, v66, v159
	v_mul_f32_e32 v44, v44, v103
	v_fmac_f32_e32 v31, v47, v44
	ds_read_b128 v[44:47], v144 offset:12304
	v_mul_f32_e32 v58, v66, v160
	v_fmac_f32_e32 v67, v28, v28
	v_fmac_f32_e32 v67, v29, v29
	v_fmac_f32_e32 v67, v30, v30
	s_waitcnt lgkmcnt(0)
	v_mul_f32_e32 v44, v58, v44
	v_fma_f32 v44, v96, v44, v20
	v_mul_f32_e32 v20, v66, v88
	v_mul_f32_e32 v20, v20, v45
	v_fma_f32 v45, v97, v20, v21
	v_mul_f32_e32 v20, v66, v82
	v_fmac_f32_e32 v67, v31, v31
	v_mul_f32_e32 v20, v20, v46
	v_fmac_f32_e32 v67, v44, v44
	v_fma_f32 v46, v98, v20, v22
	v_mul_f32_e32 v20, v66, v81
	v_fmac_f32_e32 v67, v45, v45
	v_mul_f32_e32 v20, v20, v47
	v_fmac_f32_e32 v67, v46, v46
	v_fmac_f32_e32 v23, v99, v20
	v_fmac_f32_e32 v67, v23, v23
	v_cvt_pk_bf16_f32 v20, v28, v29
	v_cvt_pk_bf16_f32 v21, v30, v31
	v_cvt_pk_bf16_f32 v22, v44, v45
	v_cvt_pk_bf16_f32 v23, v46, v23
	global_store_dwordx4 v[56:57], v[20:23], off offset:2048
	ds_read_b128 v[28:31], v144 offset:6144
	ds_read_b128 v[44:47], v144 offset:6160
	ds_read_b128 v[88:91], v144 offset:14336
	v_mul_f32_e32 v58, v66, v83
	v_readlane_b32 s51, v253, 25
	s_waitcnt lgkmcnt(0)
	v_mul_f32_e32 v58, v58, v88
	s_waitcnt vmcnt(23)
	v_fma_f32 v58, v28, v58, v12
	v_mul_f32_e32 v12, v66, v80
	v_mul_f32_e32 v12, v12, v89
	v_fmac_f32_e32 v67, v58, v58
	v_fma_f32 v59, v29, v12, v13
	v_fmac_f32_e32 v67, v59, v59
	v_pk_mul_f32 v[12:13], v[66:67], v[72:73] op_sel_hi:[0,1]
	v_pk_mul_f32 v[12:13], v[12:13], v[90:91] op_sel:[1,0] op_sel_hi:[0,1]
	v_pk_fma_f32 v[28:29], v[30:31], v[12:13], v[14:15]
	s_nop 0
	v_pk_mul_f32 v[12:13], v[28:29], v[28:29]
	s_nop 0
	v_add_f32_e32 v12, v67, v12
	v_add_f32_e32 v67, v12, v13
	ds_read_b128 v[12:15], v144 offset:14352
	v_pk_mul_f32 v[30:31], v[66:67], v[74:75] op_sel_hi:[0,1]
	s_waitcnt lgkmcnt(0)
	v_pk_mul_f32 v[12:13], v[30:31], v[12:13] op_sel:[1,0] op_sel_hi:[0,1]
	v_pk_fma_f32 v[12:13], v[44:45], v[12:13], v[4:5]
	s_nop 0
	v_pk_mul_f32 v[4:5], v[12:13], v[12:13]
	s_nop 0
	v_add_f32_e32 v4, v67, v4
	v_add_f32_e32 v30, v4, v5
	v_pk_mul_f32 v[4:5], v[66:67], v[64:65] op_sel_hi:[0,1]
	v_pk_mul_f32 v[4:5], v[4:5], v[14:15] op_sel:[1,0] op_sel_hi:[0,1]
	v_pk_fma_f32 v[14:15], v[46:47], v[4:5], v[6:7]
	s_nop 0
	v_pk_mul_f32 v[4:5], v[14:15], v[14:15]
	s_nop 0
	v_add_f32_e32 v4, v30, v4
	v_add_f32_e32 v30, v4, v5
	v_cvt_pk_bf16_f32 v4, v58, v59
	v_cvt_pk_bf16_f32 v5, v28, v29
	v_cvt_pk_bf16_f32 v6, v12, v13
	v_cvt_pk_bf16_f32 v7, v14, v15
	global_store_dwordx4 v[56:57], v[4:7], off offset:3072
	s_nop 0
	v_add_f32_dpp v12, v30, v30 quad_perm:[1,0,3,2] row_mask:0xf bank_mask:0xf bound_ctrl:1
	s_nop 1
	v_add_f32_dpp v12, v12, v12 quad_perm:[2,3,0,1] row_mask:0xf bank_mask:0xf bound_ctrl:1
	s_nop 1
	v_add_f32_dpp v12, v12, v12 row_ror:4 row_mask:0xf bank_mask:0xf bound_ctrl:1
	s_nop 1
	v_add_f32_dpp v12, v12, v12 row_ror:8 row_mask:0xf bank_mask:0xf bound_ctrl:1
	s_nop 0
	v_readlane_b32 s3, v12, 16
	v_readlane_b32 s24, v12, 48
	v_readlane_b32 s8, v12, 0
	v_readlane_b32 s9, v12, 32
	v_mov_b32_e32 v12, s3
	v_mov_b32_e32 v13, s24
	v_pk_add_f32 v[12:13], s[8:9], v[12:13]
	s_nop 0
	v_add_f32_e32 v12, v12, v13
	v_fmamk_f32 v12, v12, 0x3a000000, v151
	v_cmp_gt_f32_e32 vcc, s11, v12
	v_mul_f32_e32 v13, 0x4b800000, v12
	s_nop 0
	v_cndmask_b32_e32 v12, v12, v13, vcc
	v_rsq_f32_e32 v12, v12
	s_nop 0
	v_mul_f32_e32 v13, 0x45800000, v12
	v_cndmask_b32_e32 v28, v12, v13, vcc
	s_and_saveexec_b64 s[8:9], s[6:7]
	v_mov_b32_e32 v12, s10
	ds_write_b32 v12, v28 offset:60696
	s_or_b64 exec, exec, s[8:9]
	ds_read_b128 v[12:15], v144 offset:16384
	ds_read_b128 v[44:47], v144 offset:32768
	v_lshlrev_b32_e32 v29, 16, v48
	v_and_b32_e32 v30, 0xffff0000, v48
	v_lshlrev_b32_e32 v31, 16, v49
	v_and_b32_e32 v64, 0xffff0000, v49
	v_lshlrev_b32_e32 v65, 16, v50
	v_and_b32_e32 v66, 0xffff0000, v50
	v_lshlrev_b32_e32 v67, 16, v51
	v_and_b32_e32 v72, 0xffff0000, v51
	v_mul_f32_e32 v29, v28, v29
	ds_read_b128 v[48:51], v144 offset:16400
	ds_read_b128 v[56:59], v144 offset:32784
	s_waitcnt lgkmcnt(2)
	v_fma_f32 v12, v29, v12, v44
	v_mul_f32_e32 v29, v28, v30
	v_fma_f32 v13, v29, v13, v45
	v_mul_f32_e32 v29, v28, v31
	v_fma_f32 v14, v29, v14, v46
	v_mul_f32_e32 v29, v28, v64
	v_fmac_f32_e32 v47, v29, v15
	v_mul_f32_e32 v15, v28, v65
	v_mul_f32_e32 v29, v28, v66
	v_mul_f32_e32 v31, v28, v72
	s_waitcnt lgkmcnt(0)
	v_fma_f32 v15, v15, v48, v56
	v_fma_f32 v29, v29, v49, v57
	v_fmac_f32_e32 v59, v31, v51
	v_med3_f32 v12, v12, s12, v154
	v_med3_f32 v13, v13, s12, v154
	v_med3_f32 v31, v14, s12, v154
	v_mov_b32_e32 v14, 0
	v_cvt_pk_fp8_f32 v14, v12, v13
	v_med3_f32 v12, v15, s12, v154
	v_med3_f32 v13, v29, s12, v154
	v_mov_b32_e32 v15, 0
	v_cvt_pk_fp8_f32 v15, v12, v13
	v_mul_f32_e32 v30, v28, v67
	v_fma_f32 v30, v30, v50, v58
	v_med3_f32 v44, v47, s12, v154
	v_med3_f32 v12, v30, s12, v154
	v_med3_f32 v13, v59, s12, v154
	v_cvt_pk_fp8_f32 v14, v31, v44 op_sel:[0,0,1]
	v_cvt_pk_fp8_f32 v15, v12, v13 op_sel:[0,0,1]
	s_lshl_b64 s[8:9], s[20:21], 11
	v_lshl_add_u64 v[12:13], v[134:135], 0, s[8:9]
	v_lshlrev_b32_e32 v29, 16, v37
	global_store_dwordx2 v[12:13], v[14:15], off
	ds_read_b128 v[44:47], v144 offset:18432
	ds_read_b128 v[48:51], v144 offset:34816
	v_lshlrev_b32_e32 v14, 16, v36
	v_and_b32_e32 v15, 0xffff0000, v36
	v_and_b32_e32 v30, 0xffff0000, v37
	v_lshlrev_b32_e32 v31, 16, v38
	v_and_b32_e32 v64, 0xffff0000, v38
	v_lshlrev_b32_e32 v65, 16, v39
	v_and_b32_e32 v66, 0xffff0000, v39
	ds_read_b128 v[36:39], v144 offset:18448
	ds_read_b128 v[56:59], v144 offset:34832
	v_mul_f32_e32 v30, v28, v30
	v_mul_f32_e32 v14, v28, v14
	v_mul_f32_e32 v15, v28, v15
	s_waitcnt lgkmcnt(2)
	v_fmac_f32_e32 v51, v30, v47
	v_mul_f32_e32 v30, v28, v31
	v_mul_f32_e32 v31, v28, v64
	v_fma_f32 v14, v14, v44, v48
	v_fma_f32 v15, v15, v45, v49
	s_waitcnt lgkmcnt(0)
	v_fma_f32 v31, v31, v37, v57
	v_mul_f32_e32 v37, v28, v66
	v_fmac_f32_e32 v59, v37, v39
	v_med3_f32 v37, v14, s12, v154
	v_med3_f32 v15, v15, s12, v154
	v_mov_b32_e32 v14, 0
	v_fma_f32 v30, v30, v36, v56
	v_cvt_pk_fp8_f32 v14, v37, v15
	v_mul_f32_e32 v29, v28, v29
	v_med3_f32 v30, v30, s12, v154
	v_med3_f32 v31, v31, s12, v154
	v_mov_b32_e32 v15, 0
	v_fma_f32 v29, v29, v46, v50
	v_mul_f32_e32 v36, v28, v65
	v_cvt_pk_fp8_f32 v15, v30, v31
	v_fma_f32 v36, v36, v38, v58
	v_med3_f32 v29, v29, s12, v154
	v_med3_f32 v38, v51, s12, v154
	v_cvt_pk_fp8_f32 v14, v29, v38 op_sel:[0,0,1]
	v_med3_f32 v29, v36, s12, v154
	ds_read_b128 v[36:39], v144 offset:20480
	ds_read_b128 v[44:47], v144 offset:36864
	v_med3_f32 v30, v59, s12, v154
	v_cvt_pk_fp8_f32 v15, v29, v30 op_sel:[0,0,1]
	v_lshlrev_b32_e32 v29, 16, v20
	v_and_b32_e32 v30, 0xffff0000, v20
	v_lshlrev_b32_e32 v31, 16, v21
	v_and_b32_e32 v56, 0xffff0000, v21
	v_lshlrev_b32_e32 v57, 16, v22
	v_and_b32_e32 v58, 0xffff0000, v22
	v_lshlrev_b32_e32 v59, 16, v23
	v_and_b32_e32 v64, 0xffff0000, v23
	ds_read_b128 v[20:23], v144 offset:20496
	ds_read_b128 v[48:51], v144 offset:36880
	v_mul_f32_e32 v29, v28, v29
	s_waitcnt lgkmcnt(2)
	v_fma_f32 v29, v29, v36, v44
	v_mul_f32_e32 v36, v28, v56
	v_fmac_f32_e32 v47, v36, v39
	v_mul_f32_e32 v36, v28, v57
	s_waitcnt lgkmcnt(0)
	v_fma_f32 v20, v36, v20, v48
	v_mul_f32_e32 v36, v28, v58
	v_mul_f32_e32 v30, v28, v30
	v_mul_f32_e32 v31, v28, v31
	v_fma_f32 v21, v36, v21, v49
	v_mul_f32_e32 v36, v28, v59
	v_fma_f32 v30, v30, v37, v45
	v_fma_f32 v31, v31, v38, v46
	v_fma_f32 v22, v36, v22, v50
	v_mul_f32_e32 v36, v28, v64
	v_fmac_f32_e32 v51, v36, v23
	v_med3_f32 v23, v29, s12, v154
	v_med3_f32 v29, v30, s12, v154
	v_med3_f32 v36, v31, s12, v154
	v_mov_b32_e32 v30, 0
	v_med3_f32 v20, v20, s12, v154
	v_med3_f32 v21, v21, s12, v154
	v_mov_b32_e32 v31, 0
	v_cvt_pk_fp8_f32 v30, v23, v29
	v_cvt_pk_fp8_f32 v31, v20, v21
	v_med3_f32 v37, v47, s12, v154
	v_med3_f32 v20, v22, s12, v154
	v_med3_f32 v21, v51, s12, v154
	v_cvt_pk_fp8_f32 v30, v36, v37 op_sel:[0,0,1]
	v_cvt_pk_fp8_f32 v31, v20, v21 op_sel:[0,0,1]
	ds_read_b128 v[20:23], v144 offset:22528
	ds_read_b128 v[36:39], v144 offset:38912
	v_lshlrev_b32_e32 v29, 16, v4
	v_and_b32_e32 v48, 0xffff0000, v4
	v_lshlrev_b32_e32 v49, 16, v5
	v_and_b32_e32 v50, 0xffff0000, v5
	v_lshlrev_b32_e32 v51, 16, v6
	v_and_b32_e32 v56, 0xffff0000, v6
	v_lshlrev_b32_e32 v57, 16, v7
	v_and_b32_e32 v58, 0xffff0000, v7
	v_mul_f32_e32 v29, v28, v29
	ds_read_b128 v[4:7], v144 offset:22544
	ds_read_b128 v[44:47], v144 offset:38928
	s_waitcnt lgkmcnt(2)
	v_fma_f32 v20, v29, v20, v36
	v_mul_f32_e32 v29, v28, v48
	v_fma_f32 v21, v29, v21, v37
	v_mul_f32_e32 v29, v28, v49
	v_fma_f32 v22, v29, v22, v38
	v_mul_f32_e32 v29, v28, v50
	v_fmac_f32_e32 v39, v29, v23
	v_mul_f32_e32 v23, v28, v51
	s_waitcnt lgkmcnt(0)
	v_fma_f32 v23, v23, v4, v44
	v_mul_f32_e32 v4, v28, v56
	v_fma_f32 v5, v4, v5, v45
	v_mul_f32_e32 v4, v28, v57
	v_fma_f32 v6, v4, v6, v46
	v_mul_f32_e32 v4, v28, v58
	v_fmac_f32_e32 v47, v4, v7
	v_med3_f32 v7, v20, s12, v154
	v_med3_f32 v20, v21, s12, v154
	v_mov_b32_e32 v4, 0
	v_cvt_pk_fp8_f32 v4, v7, v20
	v_med3_f32 v7, v23, s12, v154
	v_med3_f32 v20, v5, s12, v154
	v_mov_b32_e32 v5, 0
	s_waitcnt vmcnt(16)
	v_and_b32_e32 v37, 0xffff0000, v92
	v_cvt_pk_fp8_f32 v5, v7, v20
	v_lshlrev_b32_e32 v36, 16, v92
	v_mul_f32_e32 v20, v37, v37
	v_lshlrev_b32_e32 v51, 16, v93
	v_fmac_f32_e32 v20, v36, v36
	v_and_b32_e32 v72, 0xffff0000, v93
	v_fmac_f32_e32 v20, v51, v51
	v_lshlrev_b32_e32 v73, 16, v94
	v_fmac_f32_e32 v20, v72, v72
	v_and_b32_e32 v74, 0xffff0000, v94
	v_fmac_f32_e32 v20, v73, v73
	v_lshlrev_b32_e32 v75, 16, v95
	v_fmac_f32_e32 v20, v74, v74
	v_and_b32_e32 v80, 0xffff0000, v95
	v_fmac_f32_e32 v20, v75, v75
	v_fmac_f32_e32 v20, v80, v80
	s_waitcnt vmcnt(15)
	v_lshlrev_b32_e32 v81, 16, v84
	v_and_b32_e32 v82, 0xffff0000, v84
	v_fmac_f32_e32 v20, v81, v81
	v_lshlrev_b32_e32 v83, 16, v85
	v_fmac_f32_e32 v20, v82, v82
	v_and_b32_e32 v84, 0xffff0000, v85
	v_fmac_f32_e32 v20, v83, v83
	v_lshlrev_b32_e32 v85, 16, v86
	v_fmac_f32_e32 v20, v84, v84
	v_and_b32_e32 v86, 0xffff0000, v86
	v_fmac_f32_e32 v20, v85, v85
	v_lshlrev_b32_e32 v88, 16, v87
	v_fmac_f32_e32 v20, v86, v86
	v_and_b32_e32 v87, 0xffff0000, v87
	v_fmac_f32_e32 v20, v88, v88
	v_fmac_f32_e32 v20, v87, v87
	s_waitcnt vmcnt(14)
	v_lshlrev_b32_e32 v89, 16, v76
	v_and_b32_e32 v50, 0xffff0000, v76
	v_fmac_f32_e32 v20, v89, v89
	v_lshlrev_b32_e32 v49, 16, v77
	v_fmac_f32_e32 v20, v50, v50
	v_and_b32_e32 v48, 0xffff0000, v77
	v_fmac_f32_e32 v20, v49, v49
	v_med3_f32 v7, v47, s12, v154
	v_lshlrev_b32_e32 v47, 16, v78
	v_fmac_f32_e32 v20, v48, v48
	v_and_b32_e32 v46, 0xffff0000, v78
	v_fmac_f32_e32 v20, v47, v47
	v_lshlrev_b32_e32 v45, 16, v79
	v_fmac_f32_e32 v20, v46, v46
	v_and_b32_e32 v44, 0xffff0000, v79
	v_fmac_f32_e32 v20, v45, v45
	v_med3_f32 v21, v22, s12, v154
	v_med3_f32 v22, v39, s12, v154
	v_fmac_f32_e32 v20, v44, v44
	s_waitcnt vmcnt(13)
	v_lshlrev_b32_e32 v39, 16, v68
	v_cvt_pk_fp8_f32 v4, v21, v22 op_sel:[0,0,1]
	v_med3_f32 v6, v6, s12, v154
	v_and_b32_e32 v38, 0xffff0000, v68
	v_fmac_f32_e32 v20, v39, v39
	v_and_b32_e32 v22, 0xffff0000, v69
	v_lshlrev_b32_e32 v23, 16, v69
	v_cvt_pk_fp8_f32 v5, v6, v7 op_sel:[0,0,1]
	v_fmac_f32_e32 v20, v38, v38
	v_pk_mul_f32 v[6:7], v[22:23], v[22:23]
	v_and_b32_e32 v28, 0xffff0000, v70
	v_add_f32_e32 v7, v7, v20
	v_lshlrev_b32_e32 v29, 16, v70
	v_add_f32_e32 v20, v6, v7
	v_pk_mul_f32 v[6:7], v[28:29], v[28:29]
	v_lshlrev_b32_e32 v21, 16, v71
	v_add_f32_e32 v7, v7, v20
	v_and_b32_e32 v20, 0xffff0000, v71
	v_add_f32_e32 v56, v6, v7
	v_pk_mul_f32 v[6:7], v[20:21], v[20:21]
	global_store_dwordx2 v[12:13], v[14:15], off offset:512
	global_store_dwordx2 v[12:13], v[30:31], off offset:1024
	global_store_dwordx2 v[12:13], v[4:5], off offset:1536
	v_add_f32_e32 v7, v7, v56
	v_add_f32_e32 v6, v6, v7
	s_nop 1
	v_add_f32_dpp v6, v6, v6 quad_perm:[1,0,3,2] row_mask:0xf bank_mask:0xf bound_ctrl:1
	s_nop 1
	v_add_f32_dpp v6, v6, v6 quad_perm:[2,3,0,1] row_mask:0xf bank_mask:0xf bound_ctrl:1
	s_nop 1
	v_add_f32_dpp v6, v6, v6 row_ror:4 row_mask:0xf bank_mask:0xf bound_ctrl:1
	s_nop 1
	v_add_f32_dpp v6, v6, v6 row_ror:8 row_mask:0xf bank_mask:0xf bound_ctrl:1
	s_nop 0
	v_readlane_b32 s3, v6, 16
	v_readlane_b32 s20, v6, 48
	v_readlane_b32 s8, v6, 0
	v_readlane_b32 s9, v6, 32
	v_mov_b32_e32 v6, s3
	v_mov_b32_e32 v7, s20
	v_pk_add_f32 v[6:7], s[8:9], v[6:7]
	s_nop 0
	v_add_f32_e32 v6, v6, v7
	v_fmamk_f32 v6, v6, 0x3a000000, v151
	v_mul_f32_e32 v7, 0x4b800000, v6
	v_cmp_gt_f32_e32 vcc, s11, v6
	s_nop 1
	v_cndmask_b32_e32 v6, v6, v7, vcc
	v_rsq_f32_e32 v6, v6
	s_nop 0
	v_mul_f32_e32 v4, 0x45800000, v6
	v_cndmask_b32_e32 v30, v6, v4, vcc
	ds_read_b128 v[4:7], v144 offset:8192
	ds_read_b128 v[12:15], v144
	ds_read_b128 v[56:59], v144 offset:16
	v_mul_f32_e32 v31, v30, v36
	ds_read_b128 v[64:67], v144 offset:8208
	s_waitcnt lgkmcnt(3)
	v_mul_f32_e32 v4, v4, v31
	s_waitcnt vmcnt(14) lgkmcnt(2)
	v_fma_f32 v4, v12, v4, v60
	v_mul_f32_e32 v12, v30, v37
	v_mul_f32_e32 v5, v5, v12
	v_mul_f32_e32 v12, v30, v51
	v_fma_f32 v5, v13, v5, v61
	v_mul_f32_e32 v6, v6, v12
	v_mul_f32_e32 v12, v30, v72
	v_mul_f32_e32 v31, v5, v5
	v_mul_f32_e32 v7, v7, v12
	v_fmac_f32_e32 v31, v4, v4
	v_fma_f32 v6, v14, v6, v62
	v_fmac_f32_e32 v63, v15, v7
	v_mul_f32_e32 v7, v30, v73
	v_fmac_f32_e32 v31, v6, v6
	s_waitcnt lgkmcnt(0)
	v_mul_f32_e32 v7, v7, v64
	v_mul_f32_e32 v12, v30, v74
	v_fmac_f32_e32 v31, v63, v63
	v_fma_f32 v7, v56, v7, v52
	v_mul_f32_e32 v12, v12, v65
	v_mul_f32_e32 v13, v30, v75
	v_fmac_f32_e32 v31, v7, v7
	v_fma_f32 v12, v57, v12, v53
	v_mul_f32_e32 v13, v13, v66
	v_mul_f32_e32 v14, v30, v80
	v_fmac_f32_e32 v31, v12, v12
	v_fma_f32 v13, v58, v13, v54
	v_mul_f32_e32 v14, v14, v67
	v_lshl_add_u64 v[36:37], v[132:133], 0, s[22:23]
	v_fmac_f32_e32 v31, v13, v13
	v_fmac_f32_e32 v55, v59, v14
	v_cvt_pk_bf16_f32 v4, v4, v5
	v_cvt_pk_bf16_f32 v5, v6, v63
	v_cvt_pk_bf16_f32 v6, v7, v12
	v_cvt_pk_bf16_f32 v7, v13, v55
	global_store_dwordx4 v[36:37], v[4:7], off
	v_fmac_f32_e32 v31, v55, v55
	ds_read_b128 v[12:15], v144 offset:10240
	ds_read_b128 v[52:55], v144 offset:2048
	ds_read_b128 v[56:59], v144 offset:2064
	v_mul_f32_e32 v51, v30, v81
	ds_read_b128 v[60:63], v144 offset:10256
	s_waitcnt lgkmcnt(3)
	v_mul_f32_e32 v12, v51, v12
	s_waitcnt vmcnt(13) lgkmcnt(2)
	v_fma_f32 v12, v52, v12, v40
	v_mul_f32_e32 v40, v30, v82
	v_mul_f32_e32 v13, v40, v13
	v_mul_f32_e32 v40, v30, v83
	v_mul_f32_e32 v14, v40, v14
	v_mul_f32_e32 v40, v30, v84
	v_mul_f32_e32 v15, v40, v15
	v_fmac_f32_e32 v43, v55, v15
	v_mul_f32_e32 v15, v30, v85
	s_waitcnt lgkmcnt(0)
	v_mul_f32_e32 v15, v15, v60
	v_fmac_f32_e32 v31, v12, v12
	v_fma_f32 v13, v53, v13, v41
	v_fma_f32 v15, v56, v15, v32
	v_mul_f32_e32 v32, v30, v86
	v_fmac_f32_e32 v31, v13, v13
	v_fma_f32 v14, v54, v14, v42
	v_mul_f32_e32 v32, v32, v61
	v_fmac_f32_e32 v31, v14, v14
	v_fma_f32 v32, v57, v32, v33
	v_mul_f32_e32 v33, v30, v88
	v_fmac_f32_e32 v31, v43, v43
	v_mul_f32_e32 v33, v33, v62
	v_fmac_f32_e32 v31, v15, v15
	v_fma_f32 v33, v58, v33, v34
	v_mul_f32_e32 v34, v30, v87
	v_fmac_f32_e32 v31, v32, v32
	v_mul_f32_e32 v34, v34, v63
	v_fmac_f32_e32 v31, v33, v33
	v_fmac_f32_e32 v35, v59, v34
	v_cvt_pk_bf16_f32 v12, v12, v13
	v_cvt_pk_bf16_f32 v13, v14, v43
	v_cvt_pk_bf16_f32 v14, v15, v32
	v_cvt_pk_bf16_f32 v15, v33, v35
	global_store_dwordx4 v[36:37], v[12:15], off offset:1024
	v_fmac_f32_e32 v31, v35, v35
	ds_read_b128 v[32:35], v144 offset:12288
	ds_read_b128 v[40:43], v144 offset:4096
	ds_read_b128 v[52:55], v144 offset:4112
	v_mul_f32_e32 v51, v30, v89
	ds_read_b128 v[56:59], v144 offset:12304
	s_waitcnt lgkmcnt(3)
	v_mul_f32_e32 v32, v51, v32
	s_waitcnt vmcnt(12) lgkmcnt(2)
	v_fma_f32 v24, v40, v32, v24
	v_mul_f32_e32 v32, v30, v50
	v_mul_f32_e32 v32, v32, v33
	v_fma_f32 v25, v41, v32, v25
	v_mul_f32_e32 v32, v30, v49
	v_mul_f32_e32 v32, v32, v34
	v_fma_f32 v26, v42, v32, v26
	v_mul_f32_e32 v32, v30, v48
	v_mul_f32_e32 v32, v32, v35
	v_fmac_f32_e32 v27, v43, v32
	v_mul_f32_e32 v32, v30, v47
	s_waitcnt lgkmcnt(0)
	v_mul_f32_e32 v32, v32, v56
	v_fmac_f32_e32 v31, v24, v24
	v_fma_f32 v32, v52, v32, v16
	v_mul_f32_e32 v16, v30, v46
	v_fmac_f32_e32 v31, v25, v25
	v_mul_f32_e32 v16, v16, v57
	v_fmac_f32_e32 v31, v26, v26
	v_fma_f32 v33, v53, v16, v17
	v_mul_f32_e32 v16, v30, v45
	v_fmac_f32_e32 v31, v27, v27
	v_mul_f32_e32 v16, v16, v58
	v_fmac_f32_e32 v31, v32, v32
	v_fma_f32 v34, v54, v16, v18
	v_mul_f32_e32 v16, v30, v44
	v_fmac_f32_e32 v31, v33, v33
	v_mul_f32_e32 v16, v16, v59
	v_fmac_f32_e32 v31, v34, v34
	v_fmac_f32_e32 v19, v55, v16
	v_fmac_f32_e32 v31, v19, v19
	v_cvt_pk_bf16_f32 v16, v24, v25
	v_cvt_pk_bf16_f32 v17, v26, v27
	v_cvt_pk_bf16_f32 v18, v32, v33
	v_cvt_pk_bf16_f32 v19, v34, v19
	global_store_dwordx4 v[36:37], v[16:19], off offset:2048
	ds_read_b128 v[24:27], v144 offset:14336
	ds_read_b128 v[32:35], v144 offset:6144
	ds_read_b128 v[40:43], v144 offset:6160
	v_mul_f32_e32 v39, v30, v39
	ds_read_b128 v[44:47], v144 offset:14352
	s_waitcnt lgkmcnt(3)
	v_mul_f32_e32 v24, v39, v24
	s_waitcnt vmcnt(11) lgkmcnt(2)
	v_fma_f32 v24, v32, v24, v8
	v_mul_f32_e32 v8, v30, v38
	v_mul_f32_e32 v8, v8, v25
	v_fmac_f32_e32 v31, v24, v24
	v_fma_f32 v25, v33, v8, v9
	v_fmac_f32_e32 v31, v25, v25
	v_pk_mul_f32 v[8:9], v[30:31], v[22:23] op_sel_hi:[0,1]
	v_pk_mul_f32 v[8:9], v[8:9], v[26:27] op_sel:[1,0] op_sel_hi:[0,1]
	v_pk_fma_f32 v[8:9], v[34:35], v[8:9], v[10:11]
	s_nop 0
	v_pk_mul_f32 v[10:11], v[8:9], v[8:9]
	s_nop 0
	v_add_f32_e32 v10, v31, v10
	v_add_f32_e32 v22, v10, v11
	v_pk_mul_f32 v[10:11], v[30:31], v[28:29] op_sel_hi:[0,1]
	s_waitcnt lgkmcnt(0)
	v_pk_mul_f32 v[10:11], v[10:11], v[44:45] op_sel:[1,0] op_sel_hi:[0,1]
	v_pk_fma_f32 v[10:11], v[40:41], v[10:11], v[0:1]
	s_nop 0
	v_pk_mul_f32 v[0:1], v[10:11], v[10:11]
	s_nop 0
	v_add_f32_e32 v0, v22, v0
	v_add_f32_e32 v22, v0, v1
	v_pk_mul_f32 v[0:1], v[30:31], v[20:21] op_sel_hi:[0,1]
	v_pk_mul_f32 v[0:1], v[0:1], v[46:47] op_sel:[1,0] op_sel_hi:[0,1]
	v_pk_fma_f32 v[20:21], v[42:43], v[0:1], v[2:3]
	s_nop 0
	v_pk_mul_f32 v[0:1], v[20:21], v[20:21]
	s_nop 0
	v_add_f32_e32 v0, v22, v0
	v_add_f32_e32 v2, v0, v1
	v_cvt_pk_bf16_f32 v0, v24, v25
	v_cvt_pk_bf16_f32 v1, v8, v9
	s_nop 1
	v_add_f32_dpp v2, v2, v2 quad_perm:[1,0,3,2] row_mask:0xf bank_mask:0xf bound_ctrl:1
	s_nop 1
	v_add_f32_dpp v2, v2, v2 quad_perm:[2,3,0,1] row_mask:0xf bank_mask:0xf bound_ctrl:1
	s_nop 1
	v_add_f32_dpp v2, v2, v2 row_ror:4 row_mask:0xf bank_mask:0xf bound_ctrl:1
	s_nop 1
	v_add_f32_dpp v2, v2, v2 row_ror:8 row_mask:0xf bank_mask:0xf bound_ctrl:1
	s_nop 0
	v_readlane_b32 s3, v2, 16
	v_readlane_b32 s20, v2, 48
	v_readlane_b32 s8, v2, 0
	v_readlane_b32 s9, v2, 32
	v_mov_b32_e32 v2, s3
	v_mov_b32_e32 v3, s20
	v_pk_add_f32 v[2:3], s[8:9], v[2:3]
	s_nop 0
	v_add_f32_e32 v2, v2, v3
	v_fmamk_f32 v2, v2, 0x3a000000, v151
	v_mul_f32_e32 v3, 0x4b800000, v2
	v_cmp_gt_f32_e32 vcc, s11, v2
	s_nop 1
	v_cndmask_b32_e32 v2, v2, v3, vcc
	v_rsq_f32_e32 v8, v2
	v_cvt_pk_bf16_f32 v2, v10, v11
	v_cvt_pk_bf16_f32 v3, v20, v21
	global_store_dwordx4 v[36:37], v[0:3], off offset:3072
	v_mul_f32_e32 v9, 0x45800000, v8
	v_cndmask_b32_e32 v10, v8, v9, vcc
	s_and_saveexec_b64 s[8:9], s[6:7]
	v_mov_b32_e32 v8, s10
	ds_write_b32 v8, v10 offset:60700
	s_or_b64 exec, exec, s[8:9]
	ds_read_b128 v[20:23], v144 offset:16384
	ds_read_b128 v[24:27], v144 offset:32768
	v_lshlrev_b32_e32 v8, 16, v4
	v_and_b32_e32 v9, 0xffff0000, v4
	v_lshlrev_b32_e32 v11, 16, v5
	v_and_b32_e32 v32, 0xffff0000, v5
	v_lshlrev_b32_e32 v33, 16, v6
	v_and_b32_e32 v34, 0xffff0000, v6
	v_lshlrev_b32_e32 v35, 16, v7
	v_and_b32_e32 v36, 0xffff0000, v7
	ds_read_b128 v[4:7], v144 offset:16400
	ds_read_b128 v[28:31], v144 offset:32784
	v_mul_f32_e32 v8, v10, v8
	s_waitcnt lgkmcnt(2)
	v_fma_f32 v8, v8, v20, v24
	v_mul_f32_e32 v20, v10, v32
	v_fmac_f32_e32 v27, v20, v23
	v_mul_f32_e32 v20, v10, v33
	s_waitcnt lgkmcnt(0)
	v_fma_f32 v20, v20, v4, v28
	v_mul_f32_e32 v4, v10, v34
	v_mul_f32_e32 v9, v10, v9
	v_fma_f32 v5, v4, v5, v29
	v_mul_f32_e32 v4, v10, v35
	v_fma_f32 v9, v9, v21, v25
	v_fma_f32 v6, v4, v6, v30
	v_mul_f32_e32 v4, v10, v36
	v_fmac_f32_e32 v31, v4, v7
	v_med3_f32 v7, v8, s12, v154
	v_med3_f32 v8, v9, s12, v154
	v_mov_b32_e32 v4, 0
	v_mul_f32_e32 v11, v10, v11
	v_cvt_pk_fp8_f32 v4, v7, v8
	v_fma_f32 v11, v11, v22, v26
	v_med3_f32 v9, v11, s12, v154
	v_med3_f32 v11, v27, s12, v154
	v_med3_f32 v7, v20, s12, v154
	ds_read_b128 v[20:23], v144 offset:18432
	ds_read_b128 v[24:27], v144 offset:34816
	v_med3_f32 v8, v5, s12, v154
	v_mov_b32_e32 v5, 0
	v_cvt_pk_fp8_f32 v5, v7, v8
	v_cvt_pk_fp8_f32 v4, v9, v11 op_sel:[0,0,1]
	v_med3_f32 v7, v31, s12, v154
	v_lshlrev_b32_e32 v8, 16, v12
	v_and_b32_e32 v9, 0xffff0000, v12
	v_lshlrev_b32_e32 v11, 16, v13
	v_and_b32_e32 v32, 0xffff0000, v13
	v_lshlrev_b32_e32 v33, 16, v14
	v_and_b32_e32 v34, 0xffff0000, v14
	v_lshlrev_b32_e32 v35, 16, v15
	v_and_b32_e32 v36, 0xffff0000, v15
	ds_read_b128 v[12:15], v144 offset:18448
	ds_read_b128 v[28:31], v144 offset:34832
	v_mul_f32_e32 v8, v10, v8
	s_waitcnt lgkmcnt(2)
	v_fma_f32 v8, v8, v20, v24
	v_mul_f32_e32 v20, v10, v32
	v_fmac_f32_e32 v27, v20, v23
	v_mul_f32_e32 v20, v10, v33
	s_waitcnt lgkmcnt(0)
	v_fma_f32 v12, v20, v12, v28
	v_mul_f32_e32 v20, v10, v34
	v_mul_f32_e32 v9, v10, v9
	v_fma_f32 v13, v20, v13, v29
	v_mul_f32_e32 v20, v10, v35
	v_fma_f32 v9, v9, v21, v25
	v_fma_f32 v14, v20, v14, v30
	v_mul_f32_e32 v20, v10, v36
	v_fmac_f32_e32 v31, v20, v15
	v_med3_f32 v15, v8, s12, v154
	v_med3_f32 v9, v9, s12, v154
	v_mov_b32_e32 v8, 0
	v_cvt_pk_fp8_f32 v8, v15, v9
	v_med3_f32 v12, v12, s12, v154
	v_med3_f32 v13, v13, s12, v154
	v_mov_b32_e32 v9, 0
	v_mul_f32_e32 v11, v10, v11
	v_cvt_pk_fp8_f32 v9, v12, v13
	v_fma_f32 v11, v11, v22, v26
	v_med3_f32 v11, v11, s12, v154
	v_med3_f32 v20, v27, s12, v154
	v_cvt_pk_fp8_f32 v8, v11, v20 op_sel:[0,0,1]
	v_med3_f32 v11, v14, s12, v154
	v_med3_f32 v12, v31, s12, v154
	v_cvt_pk_fp8_f32 v9, v11, v12 op_sel:[0,0,1]
	ds_read_b128 v[12:15], v144 offset:20480
	ds_read_b128 v[20:23], v144 offset:36864
	v_lshlrev_b32_e32 v11, 16, v16
	v_and_b32_e32 v28, 0xffff0000, v16
	v_lshlrev_b32_e32 v29, 16, v17
	v_and_b32_e32 v30, 0xffff0000, v17
	v_lshlrev_b32_e32 v31, 16, v18
	v_and_b32_e32 v32, 0xffff0000, v18
	v_lshlrev_b32_e32 v33, 16, v19
	v_and_b32_e32 v34, 0xffff0000, v19
	v_mul_f32_e32 v11, v10, v11
	ds_read_b128 v[16:19], v144 offset:20496
	ds_read_b128 v[24:27], v144 offset:36880
	s_waitcnt lgkmcnt(2)
	v_fma_f32 v11, v11, v12, v20
	v_mul_f32_e32 v12, v10, v28
	v_fma_f32 v12, v12, v13, v21
	v_mul_f32_e32 v13, v10, v29
	v_fma_f32 v13, v13, v14, v22
	v_mul_f32_e32 v14, v10, v30
	v_fmac_f32_e32 v23, v14, v15
	v_mul_f32_e32 v14, v10, v31
	v_mul_f32_e32 v15, v10, v32
	s_waitcnt lgkmcnt(0)
	v_fma_f32 v14, v14, v16, v24
	v_fma_f32 v15, v15, v17, v25
	v_med3_f32 v11, v11, s12, v154
	v_med3_f32 v12, v12, s12, v154
	v_mov_b32_e32 v24, 0
	v_cvt_pk_fp8_f32 v24, v11, v12
	v_med3_f32 v11, v14, s12, v154
	v_med3_f32 v12, v15, s12, v154
	v_mov_b32_e32 v25, 0
	v_cvt_pk_fp8_f32 v25, v11, v12
	v_mul_f32_e32 v16, v10, v33
	v_mul_f32_e32 v17, v10, v34
	v_fma_f32 v16, v16, v18, v26
	v_fmac_f32_e32 v27, v17, v19
	v_med3_f32 v13, v13, s12, v154
	v_med3_f32 v17, v23, s12, v154
	v_med3_f32 v11, v16, s12, v154
	v_med3_f32 v12, v27, s12, v154
	v_cvt_pk_fp8_f32 v24, v13, v17 op_sel:[0,0,1]
	v_cvt_pk_fp8_f32 v25, v11, v12 op_sel:[0,0,1]
	ds_read_b128 v[12:15], v144 offset:22528
	ds_read_b128 v[16:19], v144 offset:38912
	v_lshlrev_b32_e32 v11, 16, v0
	v_and_b32_e32 v26, 0xffff0000, v0
	v_lshlrev_b32_e32 v27, 16, v1
	v_and_b32_e32 v28, 0xffff0000, v1
	v_lshlrev_b32_e32 v29, 16, v2
	v_and_b32_e32 v30, 0xffff0000, v2
	v_lshlrev_b32_e32 v31, 16, v3
	v_and_b32_e32 v32, 0xffff0000, v3
	v_mul_f32_e32 v11, v10, v11
	ds_read_b128 v[0:3], v144 offset:22544
	ds_read_b128 v[20:23], v144 offset:38928
	s_waitcnt lgkmcnt(2)
	v_fma_f32 v11, v11, v12, v16
	v_mul_f32_e32 v12, v10, v26
	v_fma_f32 v12, v12, v13, v17
	v_mul_f32_e32 v13, v10, v27
	v_fma_f32 v13, v13, v14, v18
	v_mul_f32_e32 v14, v10, v28
	v_fmac_f32_e32 v19, v14, v15
	v_mul_f32_e32 v14, v10, v29
	s_waitcnt lgkmcnt(0)
	v_fma_f32 v14, v14, v0, v20
	v_mul_f32_e32 v0, v10, v30
	v_fma_f32 v1, v0, v1, v21
	v_mul_f32_e32 v0, v10, v31
	v_fma_f32 v2, v0, v2, v22
	v_mul_f32_e32 v0, v10, v32
	v_fmac_f32_e32 v23, v0, v3
	v_med3_f32 v3, v11, s12, v154
	v_med3_f32 v10, v12, s12, v154
	v_mov_b32_e32 v0, 0
	v_cvt_pk_fp8_f32 v0, v3, v10
	v_med3_f32 v3, v14, s12, v154
	v_med3_f32 v10, v1, s12, v154
	v_mov_b32_e32 v1, 0
	v_med3_f32 v6, v6, s12, v154
	v_cvt_pk_fp8_f32 v1, v3, v10
	v_cvt_pk_fp8_f32 v5, v6, v7 op_sel:[0,0,1]
	s_lshl_b64 s[0:1], s[0:1], 11
	v_med3_f32 v11, v13, s12, v154
	v_med3_f32 v12, v19, s12, v154
	v_med3_f32 v2, v2, s12, v154
	v_med3_f32 v3, v23, s12, v154
	v_lshl_add_u64 v[6:7], v[134:135], 0, s[0:1]
	v_cvt_pk_fp8_f32 v0, v11, v12 op_sel:[0,0,1]
	v_cvt_pk_fp8_f32 v1, v2, v3 op_sel:[0,0,1]
	global_store_dwordx2 v[6:7], v[4:5], off
	global_store_dwordx2 v[6:7], v[8:9], off offset:512
	global_store_dwordx2 v[6:7], v[24:25], off offset:1024
	global_store_dwordx2 v[6:7], v[0:1], off offset:1536
	s_mov_b32 s0, s2
	s_waitcnt vmcnt(0)
	s_barrier
	v_mbcnt_lo_u32_b32 v36, -1, 0
	v_mbcnt_hi_u32_b32 v36, -1, v36
	v_and_b32_e32 v37, 15, v36
	v_lshrrev_b32_e32 v38, 4, v36
	v_lshlrev_b32_e32 v39, 12, v37
	v_lshl_or_b32 v39, v38, 4, v39
	s_lshl_b32 s8, s86, 9
	v_add_u32_e32 v40, s8, v39
	v_mov_b32_e32 v41, 0
	s_ashr_i32 s1, s0, 31
	s_lshl_b64 s[0:1], s[0:1], 18
	s_add_u32 s0, s0, 0xb661c00
	s_addc_u32 s1, s1, 0
	s_add_u32 s0, s0, s92
	s_addc_u32 s1, s1, s93
	v_lshl_add_u64 v[64:65], s[0:1], 0, v[40:41]
	s_mov_b64 s[8:9], 0x10000
	v_lshl_add_u64 v[66:67], v[64:65], 0, s[8:9]
	v_lshl_add_u64 v[68:69], v[66:67], 0, s[8:9]
	v_lshl_add_u64 v[70:71], v[68:69], 0, s[8:9]
	s_add_u32 s0, s92, 0x3a0400
	s_addc_u32 s1, s93, 0
	v_lshl_add_u64 v[72:73], s[0:1], 0, v[40:41]
	v_lshl_add_u64 v[74:75], v[72:73], 0, s[8:9]
	v_lshl_add_u64 v[76:77], v[74:75], 0, s[8:9]
	v_lshl_add_u64 v[78:79], v[76:77], 0, s[8:9]
	s_lshl_b32 s8, s86, 10
	v_lshlrev_b32_e32 v32, 5, v38
	v_add_u32_e32 v32, s8, v32
	v_add_u32_e32 v32, 0x4000, v32
	v_lshlrev_b32_e32 v33, 2, v37
	s_lshl_b32 s8, s86, 13
	v_lshlrev_b32_e32 v34, 9, v38
	v_add_u32_e32 v34, s8, v34
	v_add_u32_e32 v34, v34, v33
	v_add_u32_e32 v34, 0x10000, v34
	ds_read_b32 v60, v33 offset:60672
	ds_read_b32 v61, v33 offset:60736
	ds_read_b32 v62, v33 offset:60800
	ds_read_b32 v63, v33 offset:60864
	v_mov_b32_e32 v0, 0
	v_mov_b32_e32 v1, 0
	v_mov_b32_e32 v2, 0
	v_mov_b32_e32 v3, 0
	v_mov_b32_e32 v4, 0
	v_mov_b32_e32 v5, 0
	v_mov_b32_e32 v6, 0
	v_mov_b32_e32 v7, 0
	v_mov_b32_e32 v8, 0
	v_mov_b32_e32 v9, 0
	v_mov_b32_e32 v10, 0
	v_mov_b32_e32 v11, 0
	v_mov_b32_e32 v12, 0
	v_mov_b32_e32 v13, 0
	v_mov_b32_e32 v14, 0
	v_mov_b32_e32 v15, 0
	v_mov_b32_e32 v16, 0
	v_mov_b32_e32 v17, 0
	v_mov_b32_e32 v18, 0
	v_mov_b32_e32 v19, 0
	v_mov_b32_e32 v20, 0
	v_mov_b32_e32 v21, 0
	v_mov_b32_e32 v22, 0
	v_mov_b32_e32 v23, 0
	v_mov_b32_e32 v24, 0
	v_mov_b32_e32 v25, 0
	v_mov_b32_e32 v26, 0
	v_mov_b32_e32 v27, 0
	v_mov_b32_e32 v28, 0
	v_mov_b32_e32 v29, 0
	v_mov_b32_e32 v30, 0
	v_mov_b32_e32 v31, 0
	global_load_dwordx4 v[80:83], v[64:65], off offset:0
	global_load_dwordx4 v[84:87], v[66:67], off offset:0
	global_load_dwordx4 v[88:91], v[68:69], off offset:0
	global_load_dwordx4 v[92:95], v[70:71], off offset:0
	global_load_dwordx4 v[96:99], v[72:73], off offset:0
	global_load_dwordx4 v[100:103], v[74:75], off offset:0
	global_load_dwordx4 v[104:107], v[76:77], off offset:0
	global_load_dwordx4 v[108:111], v[78:79], off offset:0
	global_load_dwordx4 v[112:115], v[64:65], off offset:64
	global_load_dwordx4 v[116:119], v[66:67], off offset:64
	global_load_dwordx4 v[164:167], v[68:69], off offset:64
	global_load_dwordx4 v[168:171], v[70:71], off offset:64
	global_load_dwordx4 v[172:175], v[72:73], off offset:64
	global_load_dwordx4 v[176:179], v[74:75], off offset:64
	global_load_dwordx4 v[180:183], v[76:77], off offset:64
	global_load_dwordx4 v[184:187], v[78:79], off offset:64
	global_load_dwordx4 v[188:191], v[64:65], off offset:128
	global_load_dwordx4 v[192:195], v[66:67], off offset:128
	global_load_dwordx4 v[196:199], v[68:69], off offset:128
	global_load_dwordx4 v[200:203], v[70:71], off offset:128
	global_load_dwordx4 v[204:207], v[72:73], off offset:128
	global_load_dwordx4 v[208:211], v[74:75], off offset:128
	global_load_dwordx4 v[212:215], v[76:77], off offset:128
	global_load_dwordx4 v[216:219], v[78:79], off offset:128
	global_load_dwordx4 v[220:223], v[64:65], off offset:192
	global_load_dwordx4 v[224:227], v[66:67], off offset:192
	global_load_dwordx4 v[228:231], v[68:69], off offset:192
	global_load_dwordx4 v[232:235], v[70:71], off offset:192
	global_load_dwordx4 v[236:239], v[72:73], off offset:192
	global_load_dwordx4 v[240:243], v[74:75], off offset:192
	global_load_dwordx4 v[244:247], v[76:77], off offset:192
	global_load_dwordx4 v[248:251], v[78:79], off offset:192
	ds_read_b128 v[44:47], v32 offset:0
	ds_read_b128 v[48:51], v32 offset:16
	ds_read_b128 v[52:55], v32 offset:16384
	ds_read_b128 v[56:59], v32 offset:16400
	s_waitcnt vmcnt(16)
	s_waitcnt lgkmcnt(0)
	v_lshlrev_b32_e32 v36, 16, v80
	v_and_b32_e32 v37, 0xffff0000, v80
	v_lshlrev_b32_e32 v38, 16, v81
	v_and_b32_e32 v39, 0xffff0000, v81
	v_lshlrev_b32_e32 v40, 16, v82
	v_and_b32_e32 v41, 0xffff0000, v82
	v_lshlrev_b32_e32 v42, 16, v83
	v_and_b32_e32 v43, 0xffff0000, v83
	v_mul_f32_e32 v36, v60, v36
	v_mul_f32_e32 v37, v60, v37
	v_mul_f32_e32 v38, v60, v38
	v_mul_f32_e32 v39, v60, v39
	v_mul_f32_e32 v40, v60, v40
	v_mul_f32_e32 v41, v60, v41
	v_mul_f32_e32 v42, v60, v42
	v_mul_f32_e32 v43, v60, v43
	v_fma_f32 v36, v44, v36, v52
	v_fma_f32 v37, v45, v37, v53
	v_fma_f32 v38, v46, v38, v54
	v_fma_f32 v39, v47, v39, v55
	v_fma_f32 v40, v48, v40, v56
	v_fma_f32 v41, v49, v41, v57
	v_fma_f32 v42, v50, v42, v58
	v_fma_f32 v43, v51, v43, v59
	v_cvt_pk_bf16_f32 v36, v36, v37
	v_cvt_pk_bf16_f32 v37, v38, v39
	v_cvt_pk_bf16_f32 v38, v40, v41
	v_cvt_pk_bf16_f32 v39, v42, v43
	s_nop 1
	v_mfma_f32_16x16x32_bf16 v[0:3], v[36:39], v[96:99], v[0:3]
	v_mfma_f32_16x16x32_bf16 v[4:7], v[36:39], v[100:103], v[4:7]
	v_mfma_f32_16x16x32_bf16 v[0:3], v[36:39], v[104:107], v[0:3]
	v_mfma_f32_16x16x32_bf16 v[4:7], v[36:39], v[108:111], v[4:7]
	s_nop 3
	v_lshlrev_b32_e32 v36, 16, v84
	v_and_b32_e32 v37, 0xffff0000, v84
	v_lshlrev_b32_e32 v38, 16, v85
	v_and_b32_e32 v39, 0xffff0000, v85
	v_lshlrev_b32_e32 v40, 16, v86
	v_and_b32_e32 v41, 0xffff0000, v86
	v_lshlrev_b32_e32 v42, 16, v87
	v_and_b32_e32 v43, 0xffff0000, v87
	v_mul_f32_e32 v36, v61, v36
	v_mul_f32_e32 v37, v61, v37
	v_mul_f32_e32 v38, v61, v38
	v_mul_f32_e32 v39, v61, v39
	v_mul_f32_e32 v40, v61, v40
	v_mul_f32_e32 v41, v61, v41
	v_mul_f32_e32 v42, v61, v42
	v_mul_f32_e32 v43, v61, v43
	v_fma_f32 v36, v44, v36, v52
	v_fma_f32 v37, v45, v37, v53
	v_fma_f32 v38, v46, v38, v54
	v_fma_f32 v39, v47, v39, v55
	v_fma_f32 v40, v48, v40, v56
	v_fma_f32 v41, v49, v41, v57
	v_fma_f32 v42, v50, v42, v58
	v_fma_f32 v43, v51, v43, v59
	v_cvt_pk_bf16_f32 v36, v36, v37
	v_cvt_pk_bf16_f32 v37, v38, v39
	v_cvt_pk_bf16_f32 v38, v40, v41
	v_cvt_pk_bf16_f32 v39, v42, v43
	s_nop 1
	v_mfma_f32_16x16x32_bf16 v[8:11], v[36:39], v[96:99], v[8:11]
	v_mfma_f32_16x16x32_bf16 v[12:15], v[36:39], v[100:103], v[12:15]
	v_mfma_f32_16x16x32_bf16 v[8:11], v[36:39], v[104:107], v[8:11]
	v_mfma_f32_16x16x32_bf16 v[12:15], v[36:39], v[108:111], v[12:15]
	s_nop 3
	v_lshlrev_b32_e32 v36, 16, v88
	v_and_b32_e32 v37, 0xffff0000, v88
	v_lshlrev_b32_e32 v38, 16, v89
	v_and_b32_e32 v39, 0xffff0000, v89
	v_lshlrev_b32_e32 v40, 16, v90
	v_and_b32_e32 v41, 0xffff0000, v90
	v_lshlrev_b32_e32 v42, 16, v91
	v_and_b32_e32 v43, 0xffff0000, v91
	v_mul_f32_e32 v36, v62, v36
	v_mul_f32_e32 v37, v62, v37
	v_mul_f32_e32 v38, v62, v38
	v_mul_f32_e32 v39, v62, v39
	v_mul_f32_e32 v40, v62, v40
	v_mul_f32_e32 v41, v62, v41
	v_mul_f32_e32 v42, v62, v42
	v_mul_f32_e32 v43, v62, v43
	v_fma_f32 v36, v44, v36, v52
	v_fma_f32 v37, v45, v37, v53
	v_fma_f32 v38, v46, v38, v54
	v_fma_f32 v39, v47, v39, v55
	v_fma_f32 v40, v48, v40, v56
	v_fma_f32 v41, v49, v41, v57
	v_fma_f32 v42, v50, v42, v58
	v_fma_f32 v43, v51, v43, v59
	v_cvt_pk_bf16_f32 v36, v36, v37
	v_cvt_pk_bf16_f32 v37, v38, v39
	v_cvt_pk_bf16_f32 v38, v40, v41
	v_cvt_pk_bf16_f32 v39, v42, v43
	s_nop 1
	v_mfma_f32_16x16x32_bf16 v[16:19], v[36:39], v[96:99], v[16:19]
	v_mfma_f32_16x16x32_bf16 v[20:23], v[36:39], v[100:103], v[20:23]
	v_mfma_f32_16x16x32_bf16 v[16:19], v[36:39], v[104:107], v[16:19]
	v_mfma_f32_16x16x32_bf16 v[20:23], v[36:39], v[108:111], v[20:23]
	s_nop 3
	v_lshlrev_b32_e32 v36, 16, v92
	v_and_b32_e32 v37, 0xffff0000, v92
	v_lshlrev_b32_e32 v38, 16, v93
	v_and_b32_e32 v39, 0xffff0000, v93
	v_lshlrev_b32_e32 v40, 16, v94
	v_and_b32_e32 v41, 0xffff0000, v94
	v_lshlrev_b32_e32 v42, 16, v95
	v_and_b32_e32 v43, 0xffff0000, v95
	v_mul_f32_e32 v36, v63, v36
	v_mul_f32_e32 v37, v63, v37
	v_mul_f32_e32 v38, v63, v38
	v_mul_f32_e32 v39, v63, v39
	v_mul_f32_e32 v40, v63, v40
	v_mul_f32_e32 v41, v63, v41
	v_mul_f32_e32 v42, v63, v42
	v_mul_f32_e32 v43, v63, v43
	v_fma_f32 v36, v44, v36, v52
	v_fma_f32 v37, v45, v37, v53
	v_fma_f32 v38, v46, v38, v54
	v_fma_f32 v39, v47, v39, v55
	v_fma_f32 v40, v48, v40, v56
	v_fma_f32 v41, v49, v41, v57
	v_fma_f32 v42, v50, v42, v58
	v_fma_f32 v43, v51, v43, v59
	ds_read_b128 v[44:47], v32 offset:128
	ds_read_b128 v[48:51], v32 offset:144
	ds_read_b128 v[52:55], v32 offset:16512
	ds_read_b128 v[56:59], v32 offset:16528
	v_cvt_pk_bf16_f32 v36, v36, v37
	v_cvt_pk_bf16_f32 v37, v38, v39
	v_cvt_pk_bf16_f32 v38, v40, v41
	v_cvt_pk_bf16_f32 v39, v42, v43
	s_nop 1
	v_mfma_f32_16x16x32_bf16 v[24:27], v[36:39], v[96:99], v[24:27]
	v_mfma_f32_16x16x32_bf16 v[28:31], v[36:39], v[100:103], v[28:31]
	v_mfma_f32_16x16x32_bf16 v[24:27], v[36:39], v[104:107], v[24:27]
	v_mfma_f32_16x16x32_bf16 v[28:31], v[36:39], v[108:111], v[28:31]
	s_nop 3
	s_waitcnt lgkmcnt(0)
	v_lshlrev_b32_e32 v36, 16, v112
	v_and_b32_e32 v37, 0xffff0000, v112
	v_lshlrev_b32_e32 v38, 16, v113
	v_and_b32_e32 v39, 0xffff0000, v113
	v_lshlrev_b32_e32 v40, 16, v114
	v_and_b32_e32 v41, 0xffff0000, v114
	v_lshlrev_b32_e32 v42, 16, v115
	v_and_b32_e32 v43, 0xffff0000, v115
	v_mul_f32_e32 v36, v60, v36
	v_mul_f32_e32 v37, v60, v37
	v_mul_f32_e32 v38, v60, v38
	v_mul_f32_e32 v39, v60, v39
	v_mul_f32_e32 v40, v60, v40
	v_mul_f32_e32 v41, v60, v41
	v_mul_f32_e32 v42, v60, v42
	v_mul_f32_e32 v43, v60, v43
	v_fma_f32 v36, v44, v36, v52
	v_fma_f32 v37, v45, v37, v53
	v_fma_f32 v38, v46, v38, v54
	v_fma_f32 v39, v47, v39, v55
	v_fma_f32 v40, v48, v40, v56
	v_fma_f32 v41, v49, v41, v57
	v_fma_f32 v42, v50, v42, v58
	v_fma_f32 v43, v51, v43, v59
	v_cvt_pk_bf16_f32 v36, v36, v37
	v_cvt_pk_bf16_f32 v37, v38, v39
	v_cvt_pk_bf16_f32 v38, v40, v41
	v_cvt_pk_bf16_f32 v39, v42, v43
	s_nop 1
	v_mfma_f32_16x16x32_bf16 v[0:3], v[36:39], v[172:175], v[0:3]
	v_mfma_f32_16x16x32_bf16 v[4:7], v[36:39], v[176:179], v[4:7]
	v_mfma_f32_16x16x32_bf16 v[0:3], v[36:39], v[180:183], v[0:3]
	v_mfma_f32_16x16x32_bf16 v[4:7], v[36:39], v[184:187], v[4:7]
	s_nop 3
	v_lshlrev_b32_e32 v36, 16, v116
	v_and_b32_e32 v37, 0xffff0000, v116
	v_lshlrev_b32_e32 v38, 16, v117
	v_and_b32_e32 v39, 0xffff0000, v117
	v_lshlrev_b32_e32 v40, 16, v118
	v_and_b32_e32 v41, 0xffff0000, v118
	v_lshlrev_b32_e32 v42, 16, v119
	v_and_b32_e32 v43, 0xffff0000, v119
	v_mul_f32_e32 v36, v61, v36
	v_mul_f32_e32 v37, v61, v37
	v_mul_f32_e32 v38, v61, v38
	v_mul_f32_e32 v39, v61, v39
	v_mul_f32_e32 v40, v61, v40
	v_mul_f32_e32 v41, v61, v41
	v_mul_f32_e32 v42, v61, v42
	v_mul_f32_e32 v43, v61, v43
	v_fma_f32 v36, v44, v36, v52
	v_fma_f32 v37, v45, v37, v53
	v_fma_f32 v38, v46, v38, v54
	v_fma_f32 v39, v47, v39, v55
	v_fma_f32 v40, v48, v40, v56
	v_fma_f32 v41, v49, v41, v57
	v_fma_f32 v42, v50, v42, v58
	v_fma_f32 v43, v51, v43, v59
	v_cvt_pk_bf16_f32 v36, v36, v37
	v_cvt_pk_bf16_f32 v37, v38, v39
	v_cvt_pk_bf16_f32 v38, v40, v41
	v_cvt_pk_bf16_f32 v39, v42, v43
	s_nop 1
	v_mfma_f32_16x16x32_bf16 v[8:11], v[36:39], v[172:175], v[8:11]
	v_mfma_f32_16x16x32_bf16 v[12:15], v[36:39], v[176:179], v[12:15]
	v_mfma_f32_16x16x32_bf16 v[8:11], v[36:39], v[180:183], v[8:11]
	v_mfma_f32_16x16x32_bf16 v[12:15], v[36:39], v[184:187], v[12:15]
	s_nop 3
	v_lshlrev_b32_e32 v36, 16, v164
	v_and_b32_e32 v37, 0xffff0000, v164
	v_lshlrev_b32_e32 v38, 16, v165
	v_and_b32_e32 v39, 0xffff0000, v165
	v_lshlrev_b32_e32 v40, 16, v166
	v_and_b32_e32 v41, 0xffff0000, v166
	v_lshlrev_b32_e32 v42, 16, v167
	v_and_b32_e32 v43, 0xffff0000, v167
	v_mul_f32_e32 v36, v62, v36
	v_mul_f32_e32 v37, v62, v37
	v_mul_f32_e32 v38, v62, v38
	v_mul_f32_e32 v39, v62, v39
	v_mul_f32_e32 v40, v62, v40
	v_mul_f32_e32 v41, v62, v41
	v_mul_f32_e32 v42, v62, v42
	v_mul_f32_e32 v43, v62, v43
	v_fma_f32 v36, v44, v36, v52
	v_fma_f32 v37, v45, v37, v53
	v_fma_f32 v38, v46, v38, v54
	v_fma_f32 v39, v47, v39, v55
	v_fma_f32 v40, v48, v40, v56
	v_fma_f32 v41, v49, v41, v57
	v_fma_f32 v42, v50, v42, v58
	v_fma_f32 v43, v51, v43, v59
	v_cvt_pk_bf16_f32 v36, v36, v37
	v_cvt_pk_bf16_f32 v37, v38, v39
	v_cvt_pk_bf16_f32 v38, v40, v41
	v_cvt_pk_bf16_f32 v39, v42, v43
	s_nop 1
	v_mfma_f32_16x16x32_bf16 v[16:19], v[36:39], v[172:175], v[16:19]
	v_mfma_f32_16x16x32_bf16 v[20:23], v[36:39], v[176:179], v[20:23]
	v_mfma_f32_16x16x32_bf16 v[16:19], v[36:39], v[180:183], v[16:19]
	v_mfma_f32_16x16x32_bf16 v[20:23], v[36:39], v[184:187], v[20:23]
	s_nop 3
	v_lshlrev_b32_e32 v36, 16, v168
	v_and_b32_e32 v37, 0xffff0000, v168
	v_lshlrev_b32_e32 v38, 16, v169
	v_and_b32_e32 v39, 0xffff0000, v169
	v_lshlrev_b32_e32 v40, 16, v170
	v_and_b32_e32 v41, 0xffff0000, v170
	v_lshlrev_b32_e32 v42, 16, v171
	v_and_b32_e32 v43, 0xffff0000, v171
	v_mul_f32_e32 v36, v63, v36
	v_mul_f32_e32 v37, v63, v37
	v_mul_f32_e32 v38, v63, v38
	v_mul_f32_e32 v39, v63, v39
	v_mul_f32_e32 v40, v63, v40
	v_mul_f32_e32 v41, v63, v41
	v_mul_f32_e32 v42, v63, v42
	v_mul_f32_e32 v43, v63, v43
	v_fma_f32 v36, v44, v36, v52
	v_fma_f32 v37, v45, v37, v53
	v_fma_f32 v38, v46, v38, v54
	v_fma_f32 v39, v47, v39, v55
	v_fma_f32 v40, v48, v40, v56
	v_fma_f32 v41, v49, v41, v57
	v_fma_f32 v42, v50, v42, v58
	v_fma_f32 v43, v51, v43, v59
	ds_read_b128 v[44:47], v32 offset:256
	ds_read_b128 v[48:51], v32 offset:272
	ds_read_b128 v[52:55], v32 offset:16640
	ds_read_b128 v[56:59], v32 offset:16656
	v_cvt_pk_bf16_f32 v36, v36, v37
	v_cvt_pk_bf16_f32 v37, v38, v39
	v_cvt_pk_bf16_f32 v38, v40, v41
	v_cvt_pk_bf16_f32 v39, v42, v43
	s_nop 1
	v_mfma_f32_16x16x32_bf16 v[24:27], v[36:39], v[172:175], v[24:27]
	v_mfma_f32_16x16x32_bf16 v[28:31], v[36:39], v[176:179], v[28:31]
	v_mfma_f32_16x16x32_bf16 v[24:27], v[36:39], v[180:183], v[24:27]
	v_mfma_f32_16x16x32_bf16 v[28:31], v[36:39], v[184:187], v[28:31]
	s_nop 3
	global_load_dwordx4 v[80:83], v[64:65], off offset:256
	global_load_dwordx4 v[84:87], v[66:67], off offset:256
	global_load_dwordx4 v[88:91], v[68:69], off offset:256
	global_load_dwordx4 v[92:95], v[70:71], off offset:256
	global_load_dwordx4 v[96:99], v[72:73], off offset:256
	global_load_dwordx4 v[100:103], v[74:75], off offset:256
	global_load_dwordx4 v[104:107], v[76:77], off offset:256
	global_load_dwordx4 v[108:111], v[78:79], off offset:256
	global_load_dwordx4 v[112:115], v[64:65], off offset:320
	global_load_dwordx4 v[116:119], v[66:67], off offset:320
	global_load_dwordx4 v[164:167], v[68:69], off offset:320
	global_load_dwordx4 v[168:171], v[70:71], off offset:320
	global_load_dwordx4 v[172:175], v[72:73], off offset:320
	global_load_dwordx4 v[176:179], v[74:75], off offset:320
	global_load_dwordx4 v[180:183], v[76:77], off offset:320
	global_load_dwordx4 v[184:187], v[78:79], off offset:320
	s_waitcnt vmcnt(16)
	s_waitcnt lgkmcnt(0)
	v_lshlrev_b32_e32 v36, 16, v188
	v_and_b32_e32 v37, 0xffff0000, v188
	v_lshlrev_b32_e32 v38, 16, v189
	v_and_b32_e32 v39, 0xffff0000, v189
	v_lshlrev_b32_e32 v40, 16, v190
	v_and_b32_e32 v41, 0xffff0000, v190
	v_lshlrev_b32_e32 v42, 16, v191
	v_and_b32_e32 v43, 0xffff0000, v191
	v_mul_f32_e32 v36, v60, v36
	v_mul_f32_e32 v37, v60, v37
	v_mul_f32_e32 v38, v60, v38
	v_mul_f32_e32 v39, v60, v39
	v_mul_f32_e32 v40, v60, v40
	v_mul_f32_e32 v41, v60, v41
	v_mul_f32_e32 v42, v60, v42
	v_mul_f32_e32 v43, v60, v43
	v_fma_f32 v36, v44, v36, v52
	v_fma_f32 v37, v45, v37, v53
	v_fma_f32 v38, v46, v38, v54
	v_fma_f32 v39, v47, v39, v55
	v_fma_f32 v40, v48, v40, v56
	v_fma_f32 v41, v49, v41, v57
	v_fma_f32 v42, v50, v42, v58
	v_fma_f32 v43, v51, v43, v59
	v_cvt_pk_bf16_f32 v36, v36, v37
	v_cvt_pk_bf16_f32 v37, v38, v39
	v_cvt_pk_bf16_f32 v38, v40, v41
	v_cvt_pk_bf16_f32 v39, v42, v43
	s_nop 1
	v_mfma_f32_16x16x32_bf16 v[0:3], v[36:39], v[204:207], v[0:3]
	v_mfma_f32_16x16x32_bf16 v[4:7], v[36:39], v[208:211], v[4:7]
	v_mfma_f32_16x16x32_bf16 v[0:3], v[36:39], v[212:215], v[0:3]
	v_mfma_f32_16x16x32_bf16 v[4:7], v[36:39], v[216:219], v[4:7]
	s_nop 3
	v_lshlrev_b32_e32 v36, 16, v192
	v_and_b32_e32 v37, 0xffff0000, v192
	v_lshlrev_b32_e32 v38, 16, v193
	v_and_b32_e32 v39, 0xffff0000, v193
	v_lshlrev_b32_e32 v40, 16, v194
	v_and_b32_e32 v41, 0xffff0000, v194
	v_lshlrev_b32_e32 v42, 16, v195
	v_and_b32_e32 v43, 0xffff0000, v195
	v_mul_f32_e32 v36, v61, v36
	v_mul_f32_e32 v37, v61, v37
	v_mul_f32_e32 v38, v61, v38
	v_mul_f32_e32 v39, v61, v39
	v_mul_f32_e32 v40, v61, v40
	v_mul_f32_e32 v41, v61, v41
	v_mul_f32_e32 v42, v61, v42
	v_mul_f32_e32 v43, v61, v43
	v_fma_f32 v36, v44, v36, v52
	v_fma_f32 v37, v45, v37, v53
	v_fma_f32 v38, v46, v38, v54
	v_fma_f32 v39, v47, v39, v55
	v_fma_f32 v40, v48, v40, v56
	v_fma_f32 v41, v49, v41, v57
	v_fma_f32 v42, v50, v42, v58
	v_fma_f32 v43, v51, v43, v59
	v_cvt_pk_bf16_f32 v36, v36, v37
	v_cvt_pk_bf16_f32 v37, v38, v39
	v_cvt_pk_bf16_f32 v38, v40, v41
	v_cvt_pk_bf16_f32 v39, v42, v43
	s_nop 1
	v_mfma_f32_16x16x32_bf16 v[8:11], v[36:39], v[204:207], v[8:11]
	v_mfma_f32_16x16x32_bf16 v[12:15], v[36:39], v[208:211], v[12:15]
	v_mfma_f32_16x16x32_bf16 v[8:11], v[36:39], v[212:215], v[8:11]
	v_mfma_f32_16x16x32_bf16 v[12:15], v[36:39], v[216:219], v[12:15]
	s_nop 3
	v_lshlrev_b32_e32 v36, 16, v196
	v_and_b32_e32 v37, 0xffff0000, v196
	v_lshlrev_b32_e32 v38, 16, v197
	v_and_b32_e32 v39, 0xffff0000, v197
	v_lshlrev_b32_e32 v40, 16, v198
	v_and_b32_e32 v41, 0xffff0000, v198
	v_lshlrev_b32_e32 v42, 16, v199
	v_and_b32_e32 v43, 0xffff0000, v199
	v_mul_f32_e32 v36, v62, v36
	v_mul_f32_e32 v37, v62, v37
	v_mul_f32_e32 v38, v62, v38
	v_mul_f32_e32 v39, v62, v39
	v_mul_f32_e32 v40, v62, v40
	v_mul_f32_e32 v41, v62, v41
	v_mul_f32_e32 v42, v62, v42
	v_mul_f32_e32 v43, v62, v43
	v_fma_f32 v36, v44, v36, v52
	v_fma_f32 v37, v45, v37, v53
	v_fma_f32 v38, v46, v38, v54
	v_fma_f32 v39, v47, v39, v55
	v_fma_f32 v40, v48, v40, v56
	v_fma_f32 v41, v49, v41, v57
	v_fma_f32 v42, v50, v42, v58
	v_fma_f32 v43, v51, v43, v59
	v_cvt_pk_bf16_f32 v36, v36, v37
	v_cvt_pk_bf16_f32 v37, v38, v39
	v_cvt_pk_bf16_f32 v38, v40, v41
	v_cvt_pk_bf16_f32 v39, v42, v43
	s_nop 1
	v_mfma_f32_16x16x32_bf16 v[16:19], v[36:39], v[204:207], v[16:19]
	v_mfma_f32_16x16x32_bf16 v[20:23], v[36:39], v[208:211], v[20:23]
	v_mfma_f32_16x16x32_bf16 v[16:19], v[36:39], v[212:215], v[16:19]
	v_mfma_f32_16x16x32_bf16 v[20:23], v[36:39], v[216:219], v[20:23]
	s_nop 3
	v_lshlrev_b32_e32 v36, 16, v200
	v_and_b32_e32 v37, 0xffff0000, v200
	v_lshlrev_b32_e32 v38, 16, v201
	v_and_b32_e32 v39, 0xffff0000, v201
	v_lshlrev_b32_e32 v40, 16, v202
	v_and_b32_e32 v41, 0xffff0000, v202
	v_lshlrev_b32_e32 v42, 16, v203
	v_and_b32_e32 v43, 0xffff0000, v203
	v_mul_f32_e32 v36, v63, v36
	v_mul_f32_e32 v37, v63, v37
	v_mul_f32_e32 v38, v63, v38
	v_mul_f32_e32 v39, v63, v39
	v_mul_f32_e32 v40, v63, v40
	v_mul_f32_e32 v41, v63, v41
	v_mul_f32_e32 v42, v63, v42
	v_mul_f32_e32 v43, v63, v43
	v_fma_f32 v36, v44, v36, v52
	v_fma_f32 v37, v45, v37, v53
	v_fma_f32 v38, v46, v38, v54
	v_fma_f32 v39, v47, v39, v55
	v_fma_f32 v40, v48, v40, v56
	v_fma_f32 v41, v49, v41, v57
	v_fma_f32 v42, v50, v42, v58
	v_fma_f32 v43, v51, v43, v59
	ds_read_b128 v[44:47], v32 offset:384
	ds_read_b128 v[48:51], v32 offset:400
	ds_read_b128 v[52:55], v32 offset:16768
	ds_read_b128 v[56:59], v32 offset:16784
	v_cvt_pk_bf16_f32 v36, v36, v37
	v_cvt_pk_bf16_f32 v37, v38, v39
	v_cvt_pk_bf16_f32 v38, v40, v41
	v_cvt_pk_bf16_f32 v39, v42, v43
	s_nop 1
	v_mfma_f32_16x16x32_bf16 v[24:27], v[36:39], v[204:207], v[24:27]
	v_mfma_f32_16x16x32_bf16 v[28:31], v[36:39], v[208:211], v[28:31]
	v_mfma_f32_16x16x32_bf16 v[24:27], v[36:39], v[212:215], v[24:27]
	v_mfma_f32_16x16x32_bf16 v[28:31], v[36:39], v[216:219], v[28:31]
	s_nop 3
	s_waitcnt lgkmcnt(0)
	v_lshlrev_b32_e32 v36, 16, v220
	v_and_b32_e32 v37, 0xffff0000, v220
	v_lshlrev_b32_e32 v38, 16, v221
	v_and_b32_e32 v39, 0xffff0000, v221
	v_lshlrev_b32_e32 v40, 16, v222
	v_and_b32_e32 v41, 0xffff0000, v222
	v_lshlrev_b32_e32 v42, 16, v223
	v_and_b32_e32 v43, 0xffff0000, v223
	v_mul_f32_e32 v36, v60, v36
	v_mul_f32_e32 v37, v60, v37
	v_mul_f32_e32 v38, v60, v38
	v_mul_f32_e32 v39, v60, v39
	v_mul_f32_e32 v40, v60, v40
	v_mul_f32_e32 v41, v60, v41
	v_mul_f32_e32 v42, v60, v42
	v_mul_f32_e32 v43, v60, v43
	v_fma_f32 v36, v44, v36, v52
	v_fma_f32 v37, v45, v37, v53
	v_fma_f32 v38, v46, v38, v54
	v_fma_f32 v39, v47, v39, v55
	v_fma_f32 v40, v48, v40, v56
	v_fma_f32 v41, v49, v41, v57
	v_fma_f32 v42, v50, v42, v58
	v_fma_f32 v43, v51, v43, v59
	v_cvt_pk_bf16_f32 v36, v36, v37
	v_cvt_pk_bf16_f32 v37, v38, v39
	v_cvt_pk_bf16_f32 v38, v40, v41
	v_cvt_pk_bf16_f32 v39, v42, v43
	s_nop 1
	v_mfma_f32_16x16x32_bf16 v[0:3], v[36:39], v[236:239], v[0:3]
	v_mfma_f32_16x16x32_bf16 v[4:7], v[36:39], v[240:243], v[4:7]
	v_mfma_f32_16x16x32_bf16 v[0:3], v[36:39], v[244:247], v[0:3]
	v_mfma_f32_16x16x32_bf16 v[4:7], v[36:39], v[248:251], v[4:7]
	s_nop 3
	v_lshlrev_b32_e32 v36, 16, v224
	v_and_b32_e32 v37, 0xffff0000, v224
	v_lshlrev_b32_e32 v38, 16, v225
	v_and_b32_e32 v39, 0xffff0000, v225
	v_lshlrev_b32_e32 v40, 16, v226
	v_and_b32_e32 v41, 0xffff0000, v226
	v_lshlrev_b32_e32 v42, 16, v227
	v_and_b32_e32 v43, 0xffff0000, v227
	v_mul_f32_e32 v36, v61, v36
	v_mul_f32_e32 v37, v61, v37
	v_mul_f32_e32 v38, v61, v38
	v_mul_f32_e32 v39, v61, v39
	v_mul_f32_e32 v40, v61, v40
	v_mul_f32_e32 v41, v61, v41
	v_mul_f32_e32 v42, v61, v42
	v_mul_f32_e32 v43, v61, v43
	v_fma_f32 v36, v44, v36, v52
	v_fma_f32 v37, v45, v37, v53
	v_fma_f32 v38, v46, v38, v54
	v_fma_f32 v39, v47, v39, v55
	v_fma_f32 v40, v48, v40, v56
	v_fma_f32 v41, v49, v41, v57
	v_fma_f32 v42, v50, v42, v58
	v_fma_f32 v43, v51, v43, v59
	v_cvt_pk_bf16_f32 v36, v36, v37
	v_cvt_pk_bf16_f32 v37, v38, v39
	v_cvt_pk_bf16_f32 v38, v40, v41
	v_cvt_pk_bf16_f32 v39, v42, v43
	s_nop 1
	v_mfma_f32_16x16x32_bf16 v[8:11], v[36:39], v[236:239], v[8:11]
	v_mfma_f32_16x16x32_bf16 v[12:15], v[36:39], v[240:243], v[12:15]
	v_mfma_f32_16x16x32_bf16 v[8:11], v[36:39], v[244:247], v[8:11]
	v_mfma_f32_16x16x32_bf16 v[12:15], v[36:39], v[248:251], v[12:15]
	s_nop 3
	v_lshlrev_b32_e32 v36, 16, v228
	v_and_b32_e32 v37, 0xffff0000, v228
	v_lshlrev_b32_e32 v38, 16, v229
	v_and_b32_e32 v39, 0xffff0000, v229
	v_lshlrev_b32_e32 v40, 16, v230
	v_and_b32_e32 v41, 0xffff0000, v230
	v_lshlrev_b32_e32 v42, 16, v231
	v_and_b32_e32 v43, 0xffff0000, v231
	v_mul_f32_e32 v36, v62, v36
	v_mul_f32_e32 v37, v62, v37
	v_mul_f32_e32 v38, v62, v38
	v_mul_f32_e32 v39, v62, v39
	v_mul_f32_e32 v40, v62, v40
	v_mul_f32_e32 v41, v62, v41
	v_mul_f32_e32 v42, v62, v42
	v_mul_f32_e32 v43, v62, v43
	v_fma_f32 v36, v44, v36, v52
	v_fma_f32 v37, v45, v37, v53
	v_fma_f32 v38, v46, v38, v54
	v_fma_f32 v39, v47, v39, v55
	v_fma_f32 v40, v48, v40, v56
	v_fma_f32 v41, v49, v41, v57
	v_fma_f32 v42, v50, v42, v58
	v_fma_f32 v43, v51, v43, v59
	v_cvt_pk_bf16_f32 v36, v36, v37
	v_cvt_pk_bf16_f32 v37, v38, v39
	v_cvt_pk_bf16_f32 v38, v40, v41
	v_cvt_pk_bf16_f32 v39, v42, v43
	s_nop 1
	v_mfma_f32_16x16x32_bf16 v[16:19], v[36:39], v[236:239], v[16:19]
	v_mfma_f32_16x16x32_bf16 v[20:23], v[36:39], v[240:243], v[20:23]
	v_mfma_f32_16x16x32_bf16 v[16:19], v[36:39], v[244:247], v[16:19]
	v_mfma_f32_16x16x32_bf16 v[20:23], v[36:39], v[248:251], v[20:23]
	s_nop 3
	v_lshlrev_b32_e32 v36, 16, v232
	v_and_b32_e32 v37, 0xffff0000, v232
	v_lshlrev_b32_e32 v38, 16, v233
	v_and_b32_e32 v39, 0xffff0000, v233
	v_lshlrev_b32_e32 v40, 16, v234
	v_and_b32_e32 v41, 0xffff0000, v234
	v_lshlrev_b32_e32 v42, 16, v235
	v_and_b32_e32 v43, 0xffff0000, v235
	v_mul_f32_e32 v36, v63, v36
	v_mul_f32_e32 v37, v63, v37
	v_mul_f32_e32 v38, v63, v38
	v_mul_f32_e32 v39, v63, v39
	v_mul_f32_e32 v40, v63, v40
	v_mul_f32_e32 v41, v63, v41
	v_mul_f32_e32 v42, v63, v42
	v_mul_f32_e32 v43, v63, v43
	v_fma_f32 v36, v44, v36, v52
	v_fma_f32 v37, v45, v37, v53
	v_fma_f32 v38, v46, v38, v54
	v_fma_f32 v39, v47, v39, v55
	v_fma_f32 v40, v48, v40, v56
	v_fma_f32 v41, v49, v41, v57
	v_fma_f32 v42, v50, v42, v58
	v_fma_f32 v43, v51, v43, v59
	ds_read_b128 v[44:47], v32 offset:512
	ds_read_b128 v[48:51], v32 offset:528
	ds_read_b128 v[52:55], v32 offset:16896
	ds_read_b128 v[56:59], v32 offset:16912
	v_cvt_pk_bf16_f32 v36, v36, v37
	v_cvt_pk_bf16_f32 v37, v38, v39
	v_cvt_pk_bf16_f32 v38, v40, v41
	v_cvt_pk_bf16_f32 v39, v42, v43
	s_nop 1
	v_mfma_f32_16x16x32_bf16 v[24:27], v[36:39], v[236:239], v[24:27]
	v_mfma_f32_16x16x32_bf16 v[28:31], v[36:39], v[240:243], v[28:31]
	v_mfma_f32_16x16x32_bf16 v[24:27], v[36:39], v[244:247], v[24:27]
	v_mfma_f32_16x16x32_bf16 v[28:31], v[36:39], v[248:251], v[28:31]
	s_nop 3
	global_load_dwordx4 v[188:191], v[64:65], off offset:384
	global_load_dwordx4 v[192:195], v[66:67], off offset:384
	global_load_dwordx4 v[196:199], v[68:69], off offset:384
	global_load_dwordx4 v[200:203], v[70:71], off offset:384
	global_load_dwordx4 v[204:207], v[72:73], off offset:384
	global_load_dwordx4 v[208:211], v[74:75], off offset:384
	global_load_dwordx4 v[212:215], v[76:77], off offset:384
	global_load_dwordx4 v[216:219], v[78:79], off offset:384
	global_load_dwordx4 v[220:223], v[64:65], off offset:448
	global_load_dwordx4 v[224:227], v[66:67], off offset:448
	global_load_dwordx4 v[228:231], v[68:69], off offset:448
	global_load_dwordx4 v[232:235], v[70:71], off offset:448
	global_load_dwordx4 v[236:239], v[72:73], off offset:448
	global_load_dwordx4 v[240:243], v[74:75], off offset:448
	global_load_dwordx4 v[244:247], v[76:77], off offset:448
	global_load_dwordx4 v[248:251], v[78:79], off offset:448
	s_waitcnt vmcnt(16)
	s_waitcnt lgkmcnt(0)
	v_lshlrev_b32_e32 v36, 16, v80
	v_and_b32_e32 v37, 0xffff0000, v80
	v_lshlrev_b32_e32 v38, 16, v81
	v_and_b32_e32 v39, 0xffff0000, v81
	v_lshlrev_b32_e32 v40, 16, v82
	v_and_b32_e32 v41, 0xffff0000, v82
	v_lshlrev_b32_e32 v42, 16, v83
	v_and_b32_e32 v43, 0xffff0000, v83
	v_mul_f32_e32 v36, v60, v36
	v_mul_f32_e32 v37, v60, v37
	v_mul_f32_e32 v38, v60, v38
	v_mul_f32_e32 v39, v60, v39
	v_mul_f32_e32 v40, v60, v40
	v_mul_f32_e32 v41, v60, v41
	v_mul_f32_e32 v42, v60, v42
	v_mul_f32_e32 v43, v60, v43
	v_fma_f32 v36, v44, v36, v52
	v_fma_f32 v37, v45, v37, v53
	v_fma_f32 v38, v46, v38, v54
	v_fma_f32 v39, v47, v39, v55
	v_fma_f32 v40, v48, v40, v56
	v_fma_f32 v41, v49, v41, v57
	v_fma_f32 v42, v50, v42, v58
	v_fma_f32 v43, v51, v43, v59
	v_cvt_pk_bf16_f32 v36, v36, v37
	v_cvt_pk_bf16_f32 v37, v38, v39
	v_cvt_pk_bf16_f32 v38, v40, v41
	v_cvt_pk_bf16_f32 v39, v42, v43
	s_nop 1
	v_mfma_f32_16x16x32_bf16 v[0:3], v[36:39], v[96:99], v[0:3]
	v_mfma_f32_16x16x32_bf16 v[4:7], v[36:39], v[100:103], v[4:7]
	v_mfma_f32_16x16x32_bf16 v[0:3], v[36:39], v[104:107], v[0:3]
	v_mfma_f32_16x16x32_bf16 v[4:7], v[36:39], v[108:111], v[4:7]
	s_nop 3
	v_lshlrev_b32_e32 v36, 16, v84
	v_and_b32_e32 v37, 0xffff0000, v84
	v_lshlrev_b32_e32 v38, 16, v85
	v_and_b32_e32 v39, 0xffff0000, v85
	v_lshlrev_b32_e32 v40, 16, v86
	v_and_b32_e32 v41, 0xffff0000, v86
	v_lshlrev_b32_e32 v42, 16, v87
	v_and_b32_e32 v43, 0xffff0000, v87
	v_mul_f32_e32 v36, v61, v36
	v_mul_f32_e32 v37, v61, v37
	v_mul_f32_e32 v38, v61, v38
	v_mul_f32_e32 v39, v61, v39
	v_mul_f32_e32 v40, v61, v40
	v_mul_f32_e32 v41, v61, v41
	v_mul_f32_e32 v42, v61, v42
	v_mul_f32_e32 v43, v61, v43
	v_fma_f32 v36, v44, v36, v52
	v_fma_f32 v37, v45, v37, v53
	v_fma_f32 v38, v46, v38, v54
	v_fma_f32 v39, v47, v39, v55
	v_fma_f32 v40, v48, v40, v56
	v_fma_f32 v41, v49, v41, v57
	v_fma_f32 v42, v50, v42, v58
	v_fma_f32 v43, v51, v43, v59
	v_cvt_pk_bf16_f32 v36, v36, v37
	v_cvt_pk_bf16_f32 v37, v38, v39
	v_cvt_pk_bf16_f32 v38, v40, v41
	v_cvt_pk_bf16_f32 v39, v42, v43
	s_nop 1
	v_mfma_f32_16x16x32_bf16 v[8:11], v[36:39], v[96:99], v[8:11]
	v_mfma_f32_16x16x32_bf16 v[12:15], v[36:39], v[100:103], v[12:15]
	v_mfma_f32_16x16x32_bf16 v[8:11], v[36:39], v[104:107], v[8:11]
	v_mfma_f32_16x16x32_bf16 v[12:15], v[36:39], v[108:111], v[12:15]
	s_nop 3
	v_lshlrev_b32_e32 v36, 16, v88
	v_and_b32_e32 v37, 0xffff0000, v88
	v_lshlrev_b32_e32 v38, 16, v89
	v_and_b32_e32 v39, 0xffff0000, v89
	v_lshlrev_b32_e32 v40, 16, v90
	v_and_b32_e32 v41, 0xffff0000, v90
	v_lshlrev_b32_e32 v42, 16, v91
	v_and_b32_e32 v43, 0xffff0000, v91
	v_mul_f32_e32 v36, v62, v36
	v_mul_f32_e32 v37, v62, v37
	v_mul_f32_e32 v38, v62, v38
	v_mul_f32_e32 v39, v62, v39
	v_mul_f32_e32 v40, v62, v40
	v_mul_f32_e32 v41, v62, v41
	v_mul_f32_e32 v42, v62, v42
	v_mul_f32_e32 v43, v62, v43
	v_fma_f32 v36, v44, v36, v52
	v_fma_f32 v37, v45, v37, v53
	v_fma_f32 v38, v46, v38, v54
	v_fma_f32 v39, v47, v39, v55
	v_fma_f32 v40, v48, v40, v56
	v_fma_f32 v41, v49, v41, v57
	v_fma_f32 v42, v50, v42, v58
	v_fma_f32 v43, v51, v43, v59
	v_cvt_pk_bf16_f32 v36, v36, v37
	v_cvt_pk_bf16_f32 v37, v38, v39
	v_cvt_pk_bf16_f32 v38, v40, v41
	v_cvt_pk_bf16_f32 v39, v42, v43
	s_nop 1
	v_mfma_f32_16x16x32_bf16 v[16:19], v[36:39], v[96:99], v[16:19]
	v_mfma_f32_16x16x32_bf16 v[20:23], v[36:39], v[100:103], v[20:23]
	v_mfma_f32_16x16x32_bf16 v[16:19], v[36:39], v[104:107], v[16:19]
	v_mfma_f32_16x16x32_bf16 v[20:23], v[36:39], v[108:111], v[20:23]
	s_nop 3
	v_lshlrev_b32_e32 v36, 16, v92
	v_and_b32_e32 v37, 0xffff0000, v92
	v_lshlrev_b32_e32 v38, 16, v93
	v_and_b32_e32 v39, 0xffff0000, v93
	v_lshlrev_b32_e32 v40, 16, v94
	v_and_b32_e32 v41, 0xffff0000, v94
	v_lshlrev_b32_e32 v42, 16, v95
	v_and_b32_e32 v43, 0xffff0000, v95
	v_mul_f32_e32 v36, v63, v36
	v_mul_f32_e32 v37, v63, v37
	v_mul_f32_e32 v38, v63, v38
	v_mul_f32_e32 v39, v63, v39
	v_mul_f32_e32 v40, v63, v40
	v_mul_f32_e32 v41, v63, v41
	v_mul_f32_e32 v42, v63, v42
	v_mul_f32_e32 v43, v63, v43
	v_fma_f32 v36, v44, v36, v52
	v_fma_f32 v37, v45, v37, v53
	v_fma_f32 v38, v46, v38, v54
	v_fma_f32 v39, v47, v39, v55
	v_fma_f32 v40, v48, v40, v56
	v_fma_f32 v41, v49, v41, v57
	v_fma_f32 v42, v50, v42, v58
	v_fma_f32 v43, v51, v43, v59
	ds_read_b128 v[44:47], v32 offset:640
	ds_read_b128 v[48:51], v32 offset:656
	ds_read_b128 v[52:55], v32 offset:17024
	ds_read_b128 v[56:59], v32 offset:17040
	v_cvt_pk_bf16_f32 v36, v36, v37
	v_cvt_pk_bf16_f32 v37, v38, v39
	v_cvt_pk_bf16_f32 v38, v40, v41
	v_cvt_pk_bf16_f32 v39, v42, v43
	s_nop 1
	v_mfma_f32_16x16x32_bf16 v[24:27], v[36:39], v[96:99], v[24:27]
	v_mfma_f32_16x16x32_bf16 v[28:31], v[36:39], v[100:103], v[28:31]
	v_mfma_f32_16x16x32_bf16 v[24:27], v[36:39], v[104:107], v[24:27]
	v_mfma_f32_16x16x32_bf16 v[28:31], v[36:39], v[108:111], v[28:31]
	s_nop 3
	s_waitcnt lgkmcnt(0)
	v_lshlrev_b32_e32 v36, 16, v112
	v_and_b32_e32 v37, 0xffff0000, v112
	v_lshlrev_b32_e32 v38, 16, v113
	v_and_b32_e32 v39, 0xffff0000, v113
	v_lshlrev_b32_e32 v40, 16, v114
	v_and_b32_e32 v41, 0xffff0000, v114
	v_lshlrev_b32_e32 v42, 16, v115
	v_and_b32_e32 v43, 0xffff0000, v115
	v_mul_f32_e32 v36, v60, v36
	v_mul_f32_e32 v37, v60, v37
	v_mul_f32_e32 v38, v60, v38
	v_mul_f32_e32 v39, v60, v39
	v_mul_f32_e32 v40, v60, v40
	v_mul_f32_e32 v41, v60, v41
	v_mul_f32_e32 v42, v60, v42
	v_mul_f32_e32 v43, v60, v43
	v_fma_f32 v36, v44, v36, v52
	v_fma_f32 v37, v45, v37, v53
	v_fma_f32 v38, v46, v38, v54
	v_fma_f32 v39, v47, v39, v55
	v_fma_f32 v40, v48, v40, v56
	v_fma_f32 v41, v49, v41, v57
	v_fma_f32 v42, v50, v42, v58
	v_fma_f32 v43, v51, v43, v59
	v_cvt_pk_bf16_f32 v36, v36, v37
	v_cvt_pk_bf16_f32 v37, v38, v39
	v_cvt_pk_bf16_f32 v38, v40, v41
	v_cvt_pk_bf16_f32 v39, v42, v43
	s_nop 1
	v_mfma_f32_16x16x32_bf16 v[0:3], v[36:39], v[172:175], v[0:3]
	v_mfma_f32_16x16x32_bf16 v[4:7], v[36:39], v[176:179], v[4:7]
	v_mfma_f32_16x16x32_bf16 v[0:3], v[36:39], v[180:183], v[0:3]
	v_mfma_f32_16x16x32_bf16 v[4:7], v[36:39], v[184:187], v[4:7]
	s_nop 3
	v_lshlrev_b32_e32 v36, 16, v116
	v_and_b32_e32 v37, 0xffff0000, v116
	v_lshlrev_b32_e32 v38, 16, v117
	v_and_b32_e32 v39, 0xffff0000, v117
	v_lshlrev_b32_e32 v40, 16, v118
	v_and_b32_e32 v41, 0xffff0000, v118
	v_lshlrev_b32_e32 v42, 16, v119
	v_and_b32_e32 v43, 0xffff0000, v119
	v_mul_f32_e32 v36, v61, v36
	v_mul_f32_e32 v37, v61, v37
	v_mul_f32_e32 v38, v61, v38
	v_mul_f32_e32 v39, v61, v39
	v_mul_f32_e32 v40, v61, v40
	v_mul_f32_e32 v41, v61, v41
	v_mul_f32_e32 v42, v61, v42
	v_mul_f32_e32 v43, v61, v43
	v_fma_f32 v36, v44, v36, v52
	v_fma_f32 v37, v45, v37, v53
	v_fma_f32 v38, v46, v38, v54
	v_fma_f32 v39, v47, v39, v55
	v_fma_f32 v40, v48, v40, v56
	v_fma_f32 v41, v49, v41, v57
	v_fma_f32 v42, v50, v42, v58
	v_fma_f32 v43, v51, v43, v59
	v_cvt_pk_bf16_f32 v36, v36, v37
	v_cvt_pk_bf16_f32 v37, v38, v39
	v_cvt_pk_bf16_f32 v38, v40, v41
	v_cvt_pk_bf16_f32 v39, v42, v43
	s_nop 1
	v_mfma_f32_16x16x32_bf16 v[8:11], v[36:39], v[172:175], v[8:11]
	v_mfma_f32_16x16x32_bf16 v[12:15], v[36:39], v[176:179], v[12:15]
	v_mfma_f32_16x16x32_bf16 v[8:11], v[36:39], v[180:183], v[8:11]
	v_mfma_f32_16x16x32_bf16 v[12:15], v[36:39], v[184:187], v[12:15]
	s_nop 3
	v_lshlrev_b32_e32 v36, 16, v164
	v_and_b32_e32 v37, 0xffff0000, v164
	v_lshlrev_b32_e32 v38, 16, v165
	v_and_b32_e32 v39, 0xffff0000, v165
	v_lshlrev_b32_e32 v40, 16, v166
	v_and_b32_e32 v41, 0xffff0000, v166
	v_lshlrev_b32_e32 v42, 16, v167
	v_and_b32_e32 v43, 0xffff0000, v167
	v_mul_f32_e32 v36, v62, v36
	v_mul_f32_e32 v37, v62, v37
	v_mul_f32_e32 v38, v62, v38
	v_mul_f32_e32 v39, v62, v39
	v_mul_f32_e32 v40, v62, v40
	v_mul_f32_e32 v41, v62, v41
	v_mul_f32_e32 v42, v62, v42
	v_mul_f32_e32 v43, v62, v43
	v_fma_f32 v36, v44, v36, v52
	v_fma_f32 v37, v45, v37, v53
	v_fma_f32 v38, v46, v38, v54
	v_fma_f32 v39, v47, v39, v55
	v_fma_f32 v40, v48, v40, v56
	v_fma_f32 v41, v49, v41, v57
	v_fma_f32 v42, v50, v42, v58
	v_fma_f32 v43, v51, v43, v59
	v_cvt_pk_bf16_f32 v36, v36, v37
	v_cvt_pk_bf16_f32 v37, v38, v39
	v_cvt_pk_bf16_f32 v38, v40, v41
	v_cvt_pk_bf16_f32 v39, v42, v43
	s_nop 1
	v_mfma_f32_16x16x32_bf16 v[16:19], v[36:39], v[172:175], v[16:19]
	v_mfma_f32_16x16x32_bf16 v[20:23], v[36:39], v[176:179], v[20:23]
	v_mfma_f32_16x16x32_bf16 v[16:19], v[36:39], v[180:183], v[16:19]
	v_mfma_f32_16x16x32_bf16 v[20:23], v[36:39], v[184:187], v[20:23]
	s_nop 3
	v_lshlrev_b32_e32 v36, 16, v168
	v_and_b32_e32 v37, 0xffff0000, v168
	v_lshlrev_b32_e32 v38, 16, v169
	v_and_b32_e32 v39, 0xffff0000, v169
	v_lshlrev_b32_e32 v40, 16, v170
	v_and_b32_e32 v41, 0xffff0000, v170
	v_lshlrev_b32_e32 v42, 16, v171
	v_and_b32_e32 v43, 0xffff0000, v171
	v_mul_f32_e32 v36, v63, v36
	v_mul_f32_e32 v37, v63, v37
	v_mul_f32_e32 v38, v63, v38
	v_mul_f32_e32 v39, v63, v39
	v_mul_f32_e32 v40, v63, v40
	v_mul_f32_e32 v41, v63, v41
	v_mul_f32_e32 v42, v63, v42
	v_mul_f32_e32 v43, v63, v43
	v_fma_f32 v36, v44, v36, v52
	v_fma_f32 v37, v45, v37, v53
	v_fma_f32 v38, v46, v38, v54
	v_fma_f32 v39, v47, v39, v55
	v_fma_f32 v40, v48, v40, v56
	v_fma_f32 v41, v49, v41, v57
	v_fma_f32 v42, v50, v42, v58
	v_fma_f32 v43, v51, v43, v59
	ds_read_b128 v[44:47], v32 offset:768
	ds_read_b128 v[48:51], v32 offset:784
	ds_read_b128 v[52:55], v32 offset:17152
	ds_read_b128 v[56:59], v32 offset:17168
	v_cvt_pk_bf16_f32 v36, v36, v37
	v_cvt_pk_bf16_f32 v37, v38, v39
	v_cvt_pk_bf16_f32 v38, v40, v41
	v_cvt_pk_bf16_f32 v39, v42, v43
	s_nop 1
	v_mfma_f32_16x16x32_bf16 v[24:27], v[36:39], v[172:175], v[24:27]
	v_mfma_f32_16x16x32_bf16 v[28:31], v[36:39], v[176:179], v[28:31]
	v_mfma_f32_16x16x32_bf16 v[24:27], v[36:39], v[180:183], v[24:27]
	v_mfma_f32_16x16x32_bf16 v[28:31], v[36:39], v[184:187], v[28:31]
	s_nop 3
	s_waitcnt vmcnt(0)
	s_waitcnt lgkmcnt(0)
	v_lshlrev_b32_e32 v36, 16, v188
	v_and_b32_e32 v37, 0xffff0000, v188
	v_lshlrev_b32_e32 v38, 16, v189
	v_and_b32_e32 v39, 0xffff0000, v189
	v_lshlrev_b32_e32 v40, 16, v190
	v_and_b32_e32 v41, 0xffff0000, v190
	v_lshlrev_b32_e32 v42, 16, v191
	v_and_b32_e32 v43, 0xffff0000, v191
	v_mul_f32_e32 v36, v60, v36
	v_mul_f32_e32 v37, v60, v37
	v_mul_f32_e32 v38, v60, v38
	v_mul_f32_e32 v39, v60, v39
	v_mul_f32_e32 v40, v60, v40
	v_mul_f32_e32 v41, v60, v41
	v_mul_f32_e32 v42, v60, v42
	v_mul_f32_e32 v43, v60, v43
	v_fma_f32 v36, v44, v36, v52
	v_fma_f32 v37, v45, v37, v53
	v_fma_f32 v38, v46, v38, v54
	v_fma_f32 v39, v47, v39, v55
	v_fma_f32 v40, v48, v40, v56
	v_fma_f32 v41, v49, v41, v57
	v_fma_f32 v42, v50, v42, v58
	v_fma_f32 v43, v51, v43, v59
	v_cvt_pk_bf16_f32 v36, v36, v37
	v_cvt_pk_bf16_f32 v37, v38, v39
	v_cvt_pk_bf16_f32 v38, v40, v41
	v_cvt_pk_bf16_f32 v39, v42, v43
	s_nop 1
	v_mfma_f32_16x16x32_bf16 v[0:3], v[36:39], v[204:207], v[0:3]
	v_mfma_f32_16x16x32_bf16 v[4:7], v[36:39], v[208:211], v[4:7]
	v_mfma_f32_16x16x32_bf16 v[0:3], v[36:39], v[212:215], v[0:3]
	v_mfma_f32_16x16x32_bf16 v[4:7], v[36:39], v[216:219], v[4:7]
	s_nop 3
	v_lshlrev_b32_e32 v36, 16, v192
	v_and_b32_e32 v37, 0xffff0000, v192
	v_lshlrev_b32_e32 v38, 16, v193
	v_and_b32_e32 v39, 0xffff0000, v193
	v_lshlrev_b32_e32 v40, 16, v194
	v_and_b32_e32 v41, 0xffff0000, v194
	v_lshlrev_b32_e32 v42, 16, v195
	v_and_b32_e32 v43, 0xffff0000, v195
	v_mul_f32_e32 v36, v61, v36
	v_mul_f32_e32 v37, v61, v37
	v_mul_f32_e32 v38, v61, v38
	v_mul_f32_e32 v39, v61, v39
	v_mul_f32_e32 v40, v61, v40
	v_mul_f32_e32 v41, v61, v41
	v_mul_f32_e32 v42, v61, v42
	v_mul_f32_e32 v43, v61, v43
	v_fma_f32 v36, v44, v36, v52
	v_fma_f32 v37, v45, v37, v53
	v_fma_f32 v38, v46, v38, v54
	v_fma_f32 v39, v47, v39, v55
	v_fma_f32 v40, v48, v40, v56
	v_fma_f32 v41, v49, v41, v57
	v_fma_f32 v42, v50, v42, v58
	v_fma_f32 v43, v51, v43, v59
	v_cvt_pk_bf16_f32 v36, v36, v37
	v_cvt_pk_bf16_f32 v37, v38, v39
	v_cvt_pk_bf16_f32 v38, v40, v41
	v_cvt_pk_bf16_f32 v39, v42, v43
	s_nop 1
	v_mfma_f32_16x16x32_bf16 v[8:11], v[36:39], v[204:207], v[8:11]
	v_mfma_f32_16x16x32_bf16 v[12:15], v[36:39], v[208:211], v[12:15]
	v_mfma_f32_16x16x32_bf16 v[8:11], v[36:39], v[212:215], v[8:11]
	v_mfma_f32_16x16x32_bf16 v[12:15], v[36:39], v[216:219], v[12:15]
	s_nop 3
	v_lshlrev_b32_e32 v36, 16, v196
	v_and_b32_e32 v37, 0xffff0000, v196
	v_lshlrev_b32_e32 v38, 16, v197
	v_and_b32_e32 v39, 0xffff0000, v197
	v_lshlrev_b32_e32 v40, 16, v198
	v_and_b32_e32 v41, 0xffff0000, v198
	v_lshlrev_b32_e32 v42, 16, v199
	v_and_b32_e32 v43, 0xffff0000, v199
	v_mul_f32_e32 v36, v62, v36
	v_mul_f32_e32 v37, v62, v37
	v_mul_f32_e32 v38, v62, v38
	v_mul_f32_e32 v39, v62, v39
	v_mul_f32_e32 v40, v62, v40
	v_mul_f32_e32 v41, v62, v41
	v_mul_f32_e32 v42, v62, v42
	v_mul_f32_e32 v43, v62, v43
	v_fma_f32 v36, v44, v36, v52
	v_fma_f32 v37, v45, v37, v53
	v_fma_f32 v38, v46, v38, v54
	v_fma_f32 v39, v47, v39, v55
	v_fma_f32 v40, v48, v40, v56
	v_fma_f32 v41, v49, v41, v57
	v_fma_f32 v42, v50, v42, v58
	v_fma_f32 v43, v51, v43, v59
	v_cvt_pk_bf16_f32 v36, v36, v37
	v_cvt_pk_bf16_f32 v37, v38, v39
	v_cvt_pk_bf16_f32 v38, v40, v41
	v_cvt_pk_bf16_f32 v39, v42, v43
	s_nop 1
	v_mfma_f32_16x16x32_bf16 v[16:19], v[36:39], v[204:207], v[16:19]
	v_mfma_f32_16x16x32_bf16 v[20:23], v[36:39], v[208:211], v[20:23]
	v_mfma_f32_16x16x32_bf16 v[16:19], v[36:39], v[212:215], v[16:19]
	v_mfma_f32_16x16x32_bf16 v[20:23], v[36:39], v[216:219], v[20:23]
	s_nop 3
	v_lshlrev_b32_e32 v36, 16, v200
	v_and_b32_e32 v37, 0xffff0000, v200
	v_lshlrev_b32_e32 v38, 16, v201
	v_and_b32_e32 v39, 0xffff0000, v201
	v_lshlrev_b32_e32 v40, 16, v202
	v_and_b32_e32 v41, 0xffff0000, v202
	v_lshlrev_b32_e32 v42, 16, v203
	v_and_b32_e32 v43, 0xffff0000, v203
	v_mul_f32_e32 v36, v63, v36
	v_mul_f32_e32 v37, v63, v37
	v_mul_f32_e32 v38, v63, v38
	v_mul_f32_e32 v39, v63, v39
	v_mul_f32_e32 v40, v63, v40
	v_mul_f32_e32 v41, v63, v41
	v_mul_f32_e32 v42, v63, v42
	v_mul_f32_e32 v43, v63, v43
	v_fma_f32 v36, v44, v36, v52
	v_fma_f32 v37, v45, v37, v53
	v_fma_f32 v38, v46, v38, v54
	v_fma_f32 v39, v47, v39, v55
	v_fma_f32 v40, v48, v40, v56
	v_fma_f32 v41, v49, v41, v57
	v_fma_f32 v42, v50, v42, v58
	v_fma_f32 v43, v51, v43, v59
	ds_read_b128 v[44:47], v32 offset:896
	ds_read_b128 v[48:51], v32 offset:912
	ds_read_b128 v[52:55], v32 offset:17280
	ds_read_b128 v[56:59], v32 offset:17296
	v_cvt_pk_bf16_f32 v36, v36, v37
	v_cvt_pk_bf16_f32 v37, v38, v39
	v_cvt_pk_bf16_f32 v38, v40, v41
	v_cvt_pk_bf16_f32 v39, v42, v43
	s_nop 1
	v_mfma_f32_16x16x32_bf16 v[24:27], v[36:39], v[204:207], v[24:27]
	v_mfma_f32_16x16x32_bf16 v[28:31], v[36:39], v[208:211], v[28:31]
	v_mfma_f32_16x16x32_bf16 v[24:27], v[36:39], v[212:215], v[24:27]
	v_mfma_f32_16x16x32_bf16 v[28:31], v[36:39], v[216:219], v[28:31]
	s_nop 3
	s_waitcnt lgkmcnt(0)
	v_lshlrev_b32_e32 v36, 16, v220
	v_and_b32_e32 v37, 0xffff0000, v220
	v_lshlrev_b32_e32 v38, 16, v221
	v_and_b32_e32 v39, 0xffff0000, v221
	v_lshlrev_b32_e32 v40, 16, v222
	v_and_b32_e32 v41, 0xffff0000, v222
	v_lshlrev_b32_e32 v42, 16, v223
	v_and_b32_e32 v43, 0xffff0000, v223
	v_mul_f32_e32 v36, v60, v36
	v_mul_f32_e32 v37, v60, v37
	v_mul_f32_e32 v38, v60, v38
	v_mul_f32_e32 v39, v60, v39
	v_mul_f32_e32 v40, v60, v40
	v_mul_f32_e32 v41, v60, v41
	v_mul_f32_e32 v42, v60, v42
	v_mul_f32_e32 v43, v60, v43
	v_fma_f32 v36, v44, v36, v52
	v_fma_f32 v37, v45, v37, v53
	v_fma_f32 v38, v46, v38, v54
	v_fma_f32 v39, v47, v39, v55
	v_fma_f32 v40, v48, v40, v56
	v_fma_f32 v41, v49, v41, v57
	v_fma_f32 v42, v50, v42, v58
	v_fma_f32 v43, v51, v43, v59
	v_cvt_pk_bf16_f32 v36, v36, v37
	v_cvt_pk_bf16_f32 v37, v38, v39
	v_cvt_pk_bf16_f32 v38, v40, v41
	v_cvt_pk_bf16_f32 v39, v42, v43
	s_nop 1
	v_mfma_f32_16x16x32_bf16 v[0:3], v[36:39], v[236:239], v[0:3]
	v_mfma_f32_16x16x32_bf16 v[4:7], v[36:39], v[240:243], v[4:7]
	v_mfma_f32_16x16x32_bf16 v[0:3], v[36:39], v[244:247], v[0:3]
	v_mfma_f32_16x16x32_bf16 v[4:7], v[36:39], v[248:251], v[4:7]
	s_nop 3
	v_lshlrev_b32_e32 v36, 16, v224
	v_and_b32_e32 v37, 0xffff0000, v224
	v_lshlrev_b32_e32 v38, 16, v225
	v_and_b32_e32 v39, 0xffff0000, v225
	v_lshlrev_b32_e32 v40, 16, v226
	v_and_b32_e32 v41, 0xffff0000, v226
	v_lshlrev_b32_e32 v42, 16, v227
	v_and_b32_e32 v43, 0xffff0000, v227
	v_mul_f32_e32 v36, v61, v36
	v_mul_f32_e32 v37, v61, v37
	v_mul_f32_e32 v38, v61, v38
	v_mul_f32_e32 v39, v61, v39
	v_mul_f32_e32 v40, v61, v40
	v_mul_f32_e32 v41, v61, v41
	v_mul_f32_e32 v42, v61, v42
	v_mul_f32_e32 v43, v61, v43
	v_fma_f32 v36, v44, v36, v52
	v_fma_f32 v37, v45, v37, v53
	v_fma_f32 v38, v46, v38, v54
	v_fma_f32 v39, v47, v39, v55
	v_fma_f32 v40, v48, v40, v56
	v_fma_f32 v41, v49, v41, v57
	v_fma_f32 v42, v50, v42, v58
	v_fma_f32 v43, v51, v43, v59
	v_cvt_pk_bf16_f32 v36, v36, v37
	v_cvt_pk_bf16_f32 v37, v38, v39
	v_cvt_pk_bf16_f32 v38, v40, v41
	v_cvt_pk_bf16_f32 v39, v42, v43
	s_nop 1
	v_mfma_f32_16x16x32_bf16 v[8:11], v[36:39], v[236:239], v[8:11]
	v_mfma_f32_16x16x32_bf16 v[12:15], v[36:39], v[240:243], v[12:15]
	v_mfma_f32_16x16x32_bf16 v[8:11], v[36:39], v[244:247], v[8:11]
	v_mfma_f32_16x16x32_bf16 v[12:15], v[36:39], v[248:251], v[12:15]
	s_nop 3
	v_lshlrev_b32_e32 v36, 16, v228
	v_and_b32_e32 v37, 0xffff0000, v228
	v_lshlrev_b32_e32 v38, 16, v229
	v_and_b32_e32 v39, 0xffff0000, v229
	v_lshlrev_b32_e32 v40, 16, v230
	v_and_b32_e32 v41, 0xffff0000, v230
	v_lshlrev_b32_e32 v42, 16, v231
	v_and_b32_e32 v43, 0xffff0000, v231
	v_mul_f32_e32 v36, v62, v36
	v_mul_f32_e32 v37, v62, v37
	v_mul_f32_e32 v38, v62, v38
	v_mul_f32_e32 v39, v62, v39
	v_mul_f32_e32 v40, v62, v40
	v_mul_f32_e32 v41, v62, v41
	v_mul_f32_e32 v42, v62, v42
	v_mul_f32_e32 v43, v62, v43
	v_fma_f32 v36, v44, v36, v52
	v_fma_f32 v37, v45, v37, v53
	v_fma_f32 v38, v46, v38, v54
	v_fma_f32 v39, v47, v39, v55
	v_fma_f32 v40, v48, v40, v56
	v_fma_f32 v41, v49, v41, v57
	v_fma_f32 v42, v50, v42, v58
	v_fma_f32 v43, v51, v43, v59
	v_cvt_pk_bf16_f32 v36, v36, v37
	v_cvt_pk_bf16_f32 v37, v38, v39
	v_cvt_pk_bf16_f32 v38, v40, v41
	v_cvt_pk_bf16_f32 v39, v42, v43
	s_nop 1
	v_mfma_f32_16x16x32_bf16 v[16:19], v[36:39], v[236:239], v[16:19]
	v_mfma_f32_16x16x32_bf16 v[20:23], v[36:39], v[240:243], v[20:23]
	v_mfma_f32_16x16x32_bf16 v[16:19], v[36:39], v[244:247], v[16:19]
	v_mfma_f32_16x16x32_bf16 v[20:23], v[36:39], v[248:251], v[20:23]
	s_nop 3
	v_lshlrev_b32_e32 v36, 16, v232
	v_and_b32_e32 v37, 0xffff0000, v232
	v_lshlrev_b32_e32 v38, 16, v233
	v_and_b32_e32 v39, 0xffff0000, v233
	v_lshlrev_b32_e32 v40, 16, v234
	v_and_b32_e32 v41, 0xffff0000, v234
	v_lshlrev_b32_e32 v42, 16, v235
	v_and_b32_e32 v43, 0xffff0000, v235
	v_mul_f32_e32 v36, v63, v36
	v_mul_f32_e32 v37, v63, v37
	v_mul_f32_e32 v38, v63, v38
	v_mul_f32_e32 v39, v63, v39
	v_mul_f32_e32 v40, v63, v40
	v_mul_f32_e32 v41, v63, v41
	v_mul_f32_e32 v42, v63, v42
	v_mul_f32_e32 v43, v63, v43
	v_fma_f32 v36, v44, v36, v52
	v_fma_f32 v37, v45, v37, v53
	v_fma_f32 v38, v46, v38, v54
	v_fma_f32 v39, v47, v39, v55
	v_fma_f32 v40, v48, v40, v56
	v_fma_f32 v41, v49, v41, v57
	v_fma_f32 v42, v50, v42, v58
	v_fma_f32 v43, v51, v43, v59
	v_cvt_pk_bf16_f32 v36, v36, v37
	v_cvt_pk_bf16_f32 v37, v38, v39
	v_cvt_pk_bf16_f32 v38, v40, v41
	v_cvt_pk_bf16_f32 v39, v42, v43
	s_nop 1
	v_mfma_f32_16x16x32_bf16 v[24:27], v[36:39], v[236:239], v[24:27]
	v_mfma_f32_16x16x32_bf16 v[28:31], v[36:39], v[240:243], v[28:31]
	v_mfma_f32_16x16x32_bf16 v[24:27], v[36:39], v[244:247], v[24:27]
	v_mfma_f32_16x16x32_bf16 v[28:31], v[36:39], v[248:251], v[28:31]
	s_nop 3
	s_nop 7
	s_nop 7
	ds_write_b32 v34, v0 offset:0
	ds_write_b32 v34, v1 offset:128
	ds_write_b32 v34, v2 offset:256
	ds_write_b32 v34, v3 offset:384
	ds_write_b32 v34, v4 offset:64
	ds_write_b32 v34, v5 offset:192
	ds_write_b32 v34, v6 offset:320
	ds_write_b32 v34, v7 offset:448
	ds_write_b32 v34, v8 offset:2048
	ds_write_b32 v34, v9 offset:2176
	ds_write_b32 v34, v10 offset:2304
	ds_write_b32 v34, v11 offset:2432
	ds_write_b32 v34, v12 offset:2112
	ds_write_b32 v34, v13 offset:2240
	ds_write_b32 v34, v14 offset:2368
	ds_write_b32 v34, v15 offset:2496
	ds_write_b32 v34, v16 offset:4096
	ds_write_b32 v34, v17 offset:4224
	ds_write_b32 v34, v18 offset:4352
	ds_write_b32 v34, v19 offset:4480
	ds_write_b32 v34, v20 offset:4160
	ds_write_b32 v34, v21 offset:4288
	ds_write_b32 v34, v22 offset:4416
	ds_write_b32 v34, v23 offset:4544
	ds_write_b32 v34, v24 offset:6144
	ds_write_b32 v34, v25 offset:6272
	ds_write_b32 v34, v26 offset:6400
	ds_write_b32 v34, v27 offset:6528
	ds_write_b32 v34, v28 offset:6208
	ds_write_b32 v34, v29 offset:6336
	ds_write_b32 v34, v30 offset:6464
	ds_write_b32 v34, v31 offset:6592
	s_waitcnt lgkmcnt(0)
	s_barrier
	v_lshlrev_b32_e32 v33, 4, v120
	v_add_u32_e32 v32, 0x10000, v33
	ds_read_b128 v[36:39], v32 offset:0
	ds_read_b128 v[40:43], v32 offset:8192
	ds_read_b128 v[44:47], v32 offset:16384
	ds_read_b128 v[48:51], v32 offset:24576
	ds_read_b128 v[52:55], v32 offset:32768
	ds_read_b128 v[56:59], v32 offset:40960
	ds_read_b128 v[60:63], v32 offset:49152
	ds_read_b128 v[0:3], v32 offset:57344
	s_waitcnt lgkmcnt(0)
	v_add_f32_e32 v36, v36, v40
	v_add_f32_e32 v37, v37, v41
	v_add_f32_e32 v38, v38, v42
	v_add_f32_e32 v39, v39, v43
	v_add_f32_e32 v36, v36, v44
	v_add_f32_e32 v37, v37, v45
	v_add_f32_e32 v38, v38, v46
	v_add_f32_e32 v39, v39, v47
	v_add_f32_e32 v36, v36, v48
	v_add_f32_e32 v37, v37, v49
	v_add_f32_e32 v38, v38, v50
	v_add_f32_e32 v39, v39, v51
	v_add_f32_e32 v36, v36, v52
	v_add_f32_e32 v37, v37, v53
	v_add_f32_e32 v38, v38, v54
	v_add_f32_e32 v39, v39, v55
	v_add_f32_e32 v36, v36, v56
	v_add_f32_e32 v37, v37, v57
	v_add_f32_e32 v38, v38, v58
	v_add_f32_e32 v39, v39, v59
	v_add_f32_e32 v36, v36, v60
	v_add_f32_e32 v37, v37, v61
	v_add_f32_e32 v38, v38, v62
	v_add_f32_e32 v39, v39, v63
	v_add_f32_e32 v36, v36, v0
	v_add_f32_e32 v37, v37, v1
	v_add_f32_e32 v38, v38, v2
	v_add_f32_e32 v39, v39, v3
	v_mov_b32_e32 v40, 0
	v_mov_b32_e32 v41, 0
	v_mov_b32_e32 v42, 0
	v_mov_b32_e32 v43, 0
	ds_write_b128 v33, v[36:39] offset:40960
	ds_write_b128 v33, v[40:43] offset:49152
	s_mov_b32 s88, s2
	s_waitcnt lgkmcnt(0)
	s_barrier
	s_and_saveexec_b64 s[8:9], s[52:53]
	s_cbranch_execz .LBB0_1076
	ds_read_b128 v[0:3], v143 offset:40960
	ds_read_b128 v[4:7], v143 offset:40976
	ds_read_b128 v[8:11], v143 offset:40992
	ds_read_b128 v[28:31], v143 offset:41008
	ds_read_b128 v[12:15], v143 offset:49152
	global_load_dwordx4 v[32:35], v123, s[68:69] offset:48
	global_load_dwordx4 v[36:39], v123, s[68:69] offset:32
	global_load_dwordx4 v[16:19], v123, s[68:69] offset:16
	global_load_dwordx4 v[20:23], v123, s[68:69]
	s_mov_b32 s20, 0xff800000
	s_mov_b32 s3, s34
	s_mov_b64 s[18:19], s[16:17]
	s_waitcnt lgkmcnt(0)
	v_add_f32_e32 v0, v0, v12
	s_mov_b64 s[16:17], s[4:5]
	s_mov_b64 s[4:5], s[52:53]
	s_ashr_i32 s89, s88, 31
	s_waitcnt vmcnt(0)
	v_add_f32_e32 v27, v0, v20
	v_add_f32_e32 v0, v1, v13
	v_add_f32_e32 v26, v0, v21
	v_add_f32_e32 v0, v2, v14
	v_add_f32_e32 v25, v0, v22
	v_add_f32_e32 v0, v3, v15
	v_add_f32_e32 v24, v0, v23
	ds_read_b128 v[0:3], v143 offset:49168
	v_cmp_lg_f32_e32 vcc, s20, v27
	s_waitcnt lgkmcnt(0)
	v_add_f32_e32 v0, v4, v0
	v_add_f32_e32 v23, v0, v16
	v_add_f32_e32 v0, v5, v1
	v_add_f32_e32 v22, v0, v17
	v_add_f32_e32 v0, v6, v2
	v_add_f32_e32 v21, v0, v18
	v_add_f32_e32 v0, v7, v3
	v_add_f32_e32 v20, v0, v19
	ds_read_b128 v[0:3], v143 offset:49184
	s_waitcnt lgkmcnt(0)
	v_add_f32_e32 v0, v8, v0
	v_add_f32_e32 v19, v0, v36
	v_add_f32_e32 v0, v9, v1
	v_add_f32_e32 v18, v0, v37
	v_add_f32_e32 v0, v10, v2
	v_add_f32_e32 v17, v0, v38
	v_add_f32_e32 v0, v11, v3
	v_add_f32_e32 v16, v0, v39
	ds_read_b128 v[0:3], v143 offset:49200
	s_waitcnt lgkmcnt(0)
	v_add_f32_e32 v0, v28, v0
	v_add_f32_e32 v15, v0, v32
	v_add_f32_e32 v0, v29, v1
	v_add_f32_e32 v14, v0, v33
	v_add_f32_e32 v0, v30, v2
	v_add_f32_e32 v13, v0, v34
	v_add_f32_e32 v0, v31, v3
	v_add_f32_e32 v12, v0, v35
	ds_read_b128 v[32:35], v143 offset:41024
	ds_read_b128 v[36:39], v143 offset:49216
	global_load_dwordx4 v[0:3], v123, s[68:69] offset:112
	global_load_dwordx4 v[4:7], v123, s[68:69] offset:96
	global_load_dwordx4 v[8:11], v123, s[68:69] offset:80
	global_load_dwordx4 v[40:43], v123, s[68:69] offset:64
	s_waitcnt lgkmcnt(0)
	v_add_f32_e32 v28, v32, v36
	s_waitcnt vmcnt(0)
	v_add_f32_e32 v31, v28, v40
	v_add_f32_e32 v28, v33, v37
	v_add_f32_e32 v30, v28, v41
	v_add_f32_e32 v28, v34, v38
	v_add_f32_e32 v29, v28, v42
	v_add_f32_e32 v28, v35, v39
	ds_read_b128 v[34:37], v143 offset:41040
	ds_read_b128 v[38:41], v143 offset:49232
	v_add_f32_e32 v28, v28, v43
	s_waitcnt lgkmcnt(0)
	v_add_f32_e32 v32, v34, v38
	v_add_f32_e32 v33, v32, v8
	v_add_f32_e32 v8, v35, v39
	v_add_f32_e32 v32, v8, v9
	v_add_f32_e32 v8, v36, v40
	v_add_f32_e32 v9, v8, v10
	v_add_f32_e32 v8, v37, v41
	ds_read_b128 v[34:37], v143 offset:41056
	ds_read_b128 v[38:41], v143 offset:49248
	v_add_f32_e32 v8, v8, v11
	s_waitcnt lgkmcnt(0)
	v_add_f32_e32 v10, v34, v38
	v_add_f32_e32 v11, v10, v4
	v_add_f32_e32 v4, v35, v39
	v_add_f32_e32 v10, v4, v5
	v_add_f32_e32 v4, v36, v40
	v_add_f32_e32 v5, v4, v6
	v_add_f32_e32 v4, v37, v41
	ds_read_b128 v[36:39], v143 offset:41072
	ds_read_b128 v[40:43], v143 offset:49264
	v_add_f32_e32 v4, v4, v7
	s_waitcnt lgkmcnt(0)
	v_add_f32_e32 v6, v36, v40
	v_add_f32_e32 v36, v6, v0
	v_add_f32_e32 v0, v37, v41
	v_add_f32_e32 v35, v0, v1
	v_add_f32_e32 v0, v38, v42
	v_add_f32_e32 v2, v0, v2
	v_add_f32_e32 v0, v39, v43
	v_add_f32_e32 v1, v0, v3
	v_cndmask_b32_e32 v0, v155, v27, vcc
	v_cmp_gt_f32_e32 vcc, v26, v0
	s_nop 1
	v_cndmask_b32_e32 v0, v0, v26, vcc
	v_cndmask_b32_e64 v3, 0, 1, vcc
	v_cmp_gt_f32_e32 vcc, v25, v0
	s_nop 1
	v_cndmask_b32_e32 v0, v0, v25, vcc
	v_cndmask_b32_e64 v3, v3, 2, vcc
	v_cmp_gt_f32_e32 vcc, v24, v0
	s_nop 1
	v_cndmask_b32_e32 v0, v0, v24, vcc
	v_cndmask_b32_e64 v3, v3, 3, vcc
	v_cmp_gt_f32_e32 vcc, v23, v0
	s_nop 1
	v_cndmask_b32_e32 v0, v0, v23, vcc
	v_cndmask_b32_e64 v3, v3, 4, vcc
	v_cmp_gt_f32_e32 vcc, v22, v0
	s_nop 1
	v_cndmask_b32_e32 v0, v0, v22, vcc
	v_cndmask_b32_e64 v3, v3, 5, vcc
	v_cmp_gt_f32_e32 vcc, v21, v0
	s_nop 1
	v_cndmask_b32_e32 v0, v0, v21, vcc
	v_cndmask_b32_e64 v3, v3, 6, vcc
	v_cmp_gt_f32_e32 vcc, v20, v0
	s_nop 1
	v_cndmask_b32_e32 v0, v0, v20, vcc
	v_cndmask_b32_e64 v3, v3, 7, vcc
	v_cmp_gt_f32_e32 vcc, v19, v0
	s_nop 1
	v_cndmask_b32_e32 v0, v0, v19, vcc
	v_cndmask_b32_e64 v3, v3, 8, vcc
	v_cmp_gt_f32_e32 vcc, v18, v0
	s_nop 1
	v_cndmask_b32_e32 v0, v0, v18, vcc
	v_cndmask_b32_e64 v3, v3, 9, vcc
	v_cmp_gt_f32_e32 vcc, v17, v0
	s_nop 1
	v_cndmask_b32_e32 v0, v0, v17, vcc
	v_cndmask_b32_e64 v3, v3, 10, vcc
	v_cmp_gt_f32_e32 vcc, v16, v0
	s_nop 1
	v_cndmask_b32_e32 v0, v0, v16, vcc
	v_cndmask_b32_e64 v3, v3, 11, vcc
	v_cmp_gt_f32_e32 vcc, v15, v0
	s_nop 1
	v_cndmask_b32_e32 v0, v0, v15, vcc
	v_cndmask_b32_e64 v3, v3, 12, vcc
	v_cmp_gt_f32_e32 vcc, v14, v0
	s_nop 1
	v_cndmask_b32_e32 v0, v0, v14, vcc
	v_cndmask_b32_e64 v3, v3, 13, vcc
	v_cmp_gt_f32_e32 vcc, v13, v0
	s_nop 1
	v_cndmask_b32_e32 v0, v0, v13, vcc
	v_cndmask_b32_e64 v3, v3, 14, vcc
	v_cmp_gt_f32_e32 vcc, v12, v0
	s_nop 1
	v_cndmask_b32_e32 v0, v0, v12, vcc
	v_cndmask_b32_e64 v3, v3, 15, vcc
	v_cmp_gt_f32_e32 vcc, v31, v0
	s_nop 1
	v_cndmask_b32_e32 v0, v0, v31, vcc
	v_cndmask_b32_e64 v3, v3, 16, vcc
	v_cmp_gt_f32_e32 vcc, v30, v0
	s_nop 1
	v_cndmask_b32_e32 v0, v0, v30, vcc
	v_cndmask_b32_e64 v3, v3, 17, vcc
	v_cmp_gt_f32_e32 vcc, v29, v0
	s_nop 1
	v_cndmask_b32_e32 v0, v0, v29, vcc
	v_cndmask_b32_e64 v3, v3, 18, vcc
	v_cmp_gt_f32_e32 vcc, v28, v0
	s_nop 1
	v_cndmask_b32_e32 v0, v0, v28, vcc
	v_cndmask_b32_e64 v3, v3, 19, vcc
	v_cmp_gt_f32_e32 vcc, v33, v0
	s_nop 1
	v_cndmask_b32_e32 v0, v0, v33, vcc
	v_cndmask_b32_e64 v3, v3, 20, vcc
	v_cmp_gt_f32_e32 vcc, v32, v0
	s_nop 1
	v_cndmask_b32_e32 v0, v0, v32, vcc
	v_cndmask_b32_e64 v3, v3, 21, vcc
	v_cmp_gt_f32_e32 vcc, v9, v0
	s_nop 1
	v_cndmask_b32_e32 v0, v0, v9, vcc
	v_cndmask_b32_e64 v3, v3, 22, vcc
	v_cmp_gt_f32_e32 vcc, v8, v0
	s_nop 1
	v_cndmask_b32_e32 v0, v0, v8, vcc
	v_cndmask_b32_e64 v3, v3, 23, vcc
	v_cmp_gt_f32_e32 vcc, v11, v0
	s_nop 1
	v_cndmask_b32_e32 v0, v0, v11, vcc
	v_cndmask_b32_e64 v3, v3, 24, vcc
	v_cmp_gt_f32_e32 vcc, v10, v0
	s_nop 1
	v_cndmask_b32_e32 v0, v0, v10, vcc
	v_cndmask_b32_e64 v3, v3, 25, vcc
	v_cmp_gt_f32_e32 vcc, v5, v0
	s_nop 1
	v_cndmask_b32_e32 v0, v0, v5, vcc
	v_cndmask_b32_e64 v3, v3, 26, vcc
	v_cmp_gt_f32_e32 vcc, v4, v0
	s_nop 1
	v_cndmask_b32_e32 v0, v0, v4, vcc
	v_cndmask_b32_e64 v3, v3, 27, vcc
	v_cmp_gt_f32_e32 vcc, v36, v0
	s_nop 1
	v_cndmask_b32_e32 v0, v0, v36, vcc
	v_cndmask_b32_e64 v3, v3, 28, vcc
	v_cmp_gt_f32_e32 vcc, v35, v0
	s_nop 1
	v_cndmask_b32_e32 v0, v0, v35, vcc
	v_cndmask_b32_e64 v3, v3, 29, vcc
	v_cmp_gt_f32_e32 vcc, v2, v0
	s_nop 1
	v_cndmask_b32_e32 v0, v0, v2, vcc
	v_cndmask_b32_e64 v3, v3, 30, vcc
	v_cmp_gt_f32_e32 vcc, v1, v0
	s_nop 1
	v_cndmask_b32_e64 v6, v3, 31, vcc
	v_cndmask_b32_e32 v0, v0, v1, vcc
	v_cmp_eq_u32_e64 s[0:1], 0, v6
	v_cmp_nlg_f32_e32 vcc, s20, v27
	v_lshlrev_b32_e64 v34, v6, 1
	s_or_b64 s[0:1], s[0:1], vcc
	v_cndmask_b32_e64 v3, v27, v155, s[0:1]
	v_and_b32_e32 v7, 2, v34
	v_cmp_eq_u32_e64 s[0:1], 0, v7
	v_cmp_gt_f32_e64 s[20:21], v26, v3
	s_and_b64 s[0:1], s[0:1], s[20:21]
	v_cndmask_b32_e64 v3, v3, v26, s[0:1]
	v_and_b32_e32 v37, 4, v34
	v_cndmask_b32_e64 v7, 0, 1, s[0:1]
	v_cmp_eq_u32_e64 s[0:1], 0, v37
	v_cmp_gt_f32_e64 s[20:21], v25, v3
	s_and_b64 s[0:1], s[0:1], s[20:21]
	v_cndmask_b32_e64 v3, v3, v25, s[0:1]
	v_and_b32_e32 v37, 8, v34
	v_cndmask_b32_e64 v7, v7, 2, s[0:1]
	v_cmp_eq_u32_e64 s[0:1], 0, v37
	v_cmp_gt_f32_e64 s[20:21], v24, v3
	s_and_b64 s[0:1], s[0:1], s[20:21]
	v_cndmask_b32_e64 v3, v3, v24, s[0:1]
	v_and_b32_e32 v37, 16, v34
	v_cndmask_b32_e64 v7, v7, 3, s[0:1]
	v_cmp_eq_u32_e64 s[0:1], 0, v37
	v_cmp_gt_f32_e64 s[20:21], v23, v3
	s_and_b64 s[0:1], s[0:1], s[20:21]
	v_cndmask_b32_e64 v3, v3, v23, s[0:1]
	v_and_b32_e32 v37, 32, v34
	v_cndmask_b32_e64 v7, v7, 4, s[0:1]
	v_cmp_eq_u32_e64 s[0:1], 0, v37
	v_cmp_gt_f32_e64 s[20:21], v22, v3
	s_and_b64 s[0:1], s[0:1], s[20:21]
	v_cndmask_b32_e64 v3, v3, v22, s[0:1]
	v_and_b32_e32 v37, 64, v34
	v_cndmask_b32_e64 v7, v7, 5, s[0:1]
	v_cmp_eq_u32_e64 s[0:1], 0, v37
	v_cmp_gt_f32_e64 s[20:21], v21, v3
	s_and_b64 s[0:1], s[0:1], s[20:21]
	v_cndmask_b32_e64 v3, v3, v21, s[0:1]
	v_and_b32_e32 v37, 0x80, v34
	v_cndmask_b32_e64 v7, v7, 6, s[0:1]
	v_cmp_eq_u32_e64 s[0:1], 0, v37
	v_cmp_gt_f32_e64 s[20:21], v20, v3
	s_and_b64 s[0:1], s[0:1], s[20:21]
	v_cndmask_b32_e64 v3, v3, v20, s[0:1]
	v_and_b32_e32 v37, 0x100, v34
	v_cndmask_b32_e64 v7, v7, 7, s[0:1]
	v_cmp_eq_u32_e64 s[0:1], 0, v37
	v_cmp_gt_f32_e64 s[20:21], v19, v3
	s_and_b64 s[0:1], s[0:1], s[20:21]
	v_cndmask_b32_e64 v3, v3, v19, s[0:1]
	v_and_b32_e32 v37, 0x200, v34
	v_cndmask_b32_e64 v7, v7, 8, s[0:1]
	v_cmp_eq_u32_e64 s[0:1], 0, v37
	v_cmp_gt_f32_e64 s[20:21], v18, v3
	s_and_b64 s[0:1], s[0:1], s[20:21]
	v_cndmask_b32_e64 v3, v3, v18, s[0:1]
	v_and_b32_e32 v37, 0x400, v34
	v_cndmask_b32_e64 v7, v7, 9, s[0:1]
	v_cmp_eq_u32_e64 s[0:1], 0, v37
	v_cmp_gt_f32_e64 s[20:21], v17, v3
	s_and_b64 s[0:1], s[0:1], s[20:21]
	v_cndmask_b32_e64 v3, v3, v17, s[0:1]
	v_and_b32_e32 v37, 0x800, v34
	v_cndmask_b32_e64 v7, v7, 10, s[0:1]
	v_cmp_eq_u32_e64 s[0:1], 0, v37
	v_cmp_gt_f32_e64 s[20:21], v16, v3
	s_and_b64 s[0:1], s[0:1], s[20:21]
	v_cndmask_b32_e64 v3, v3, v16, s[0:1]
	v_and_b32_e32 v37, 0x1000, v34
	v_cndmask_b32_e64 v7, v7, 11, s[0:1]
	v_cmp_eq_u32_e64 s[0:1], 0, v37
	v_cmp_gt_f32_e64 s[20:21], v15, v3
	s_and_b64 s[0:1], s[0:1], s[20:21]
	v_cndmask_b32_e64 v3, v3, v15, s[0:1]
	v_and_b32_e32 v37, 0x2000, v34
	v_cndmask_b32_e64 v7, v7, 12, s[0:1]
	v_cmp_eq_u32_e64 s[0:1], 0, v37
	v_cmp_gt_f32_e64 s[20:21], v14, v3
	s_and_b64 s[0:1], s[0:1], s[20:21]
	v_cndmask_b32_e64 v3, v3, v14, s[0:1]
	v_and_b32_e32 v37, 0x4000, v34
	v_cndmask_b32_e64 v7, v7, 13, s[0:1]
	v_cmp_eq_u32_e64 s[0:1], 0, v37
	v_cmp_gt_f32_e64 s[20:21], v13, v3
	s_and_b64 s[0:1], s[0:1], s[20:21]
	v_cndmask_b32_e64 v3, v3, v13, s[0:1]
	v_and_b32_e32 v37, 0x8000, v34
	v_cndmask_b32_e64 v7, v7, 14, s[0:1]
	v_cmp_eq_u32_e64 s[0:1], 0, v37
	v_cmp_gt_f32_e64 s[20:21], v12, v3
	s_and_b64 s[0:1], s[0:1], s[20:21]
	v_cndmask_b32_e64 v3, v3, v12, s[0:1]
	v_and_b32_e32 v37, 0x10000, v34
	v_cndmask_b32_e64 v7, v7, 15, s[0:1]
	v_cmp_eq_u32_e64 s[0:1], 0, v37
	v_cmp_gt_f32_e64 s[20:21], v31, v3
	s_and_b64 s[0:1], s[0:1], s[20:21]
	v_cndmask_b32_e64 v3, v3, v31, s[0:1]
	v_and_b32_e32 v37, 0x20000, v34
	v_cndmask_b32_e64 v7, v7, 16, s[0:1]
	v_cmp_eq_u32_e64 s[0:1], 0, v37
	v_cmp_gt_f32_e64 s[20:21], v30, v3
	s_and_b64 s[0:1], s[0:1], s[20:21]
	v_cndmask_b32_e64 v3, v3, v30, s[0:1]
	v_and_b32_e32 v37, 0x40000, v34
	v_cndmask_b32_e64 v7, v7, 17, s[0:1]
	v_cmp_eq_u32_e64 s[0:1], 0, v37
	v_cmp_gt_f32_e64 s[20:21], v29, v3
	s_and_b64 s[0:1], s[0:1], s[20:21]
	v_cndmask_b32_e64 v3, v3, v29, s[0:1]
	v_and_b32_e32 v37, 0x80000, v34
	v_cndmask_b32_e64 v7, v7, 18, s[0:1]
	v_cmp_eq_u32_e64 s[0:1], 0, v37
	v_cmp_gt_f32_e64 s[20:21], v28, v3
	s_and_b64 s[0:1], s[0:1], s[20:21]
	v_cndmask_b32_e64 v3, v3, v28, s[0:1]
	v_and_b32_e32 v37, 0x100000, v34
	v_cndmask_b32_e64 v7, v7, 19, s[0:1]
	v_cmp_eq_u32_e64 s[0:1], 0, v37
	v_cmp_gt_f32_e64 s[20:21], v33, v3
	s_and_b64 s[0:1], s[0:1], s[20:21]
	v_cndmask_b32_e64 v3, v3, v33, s[0:1]
	v_and_b32_e32 v37, 0x200000, v34
	v_cndmask_b32_e64 v7, v7, 20, s[0:1]
	v_cmp_eq_u32_e64 s[0:1], 0, v37
	v_cmp_gt_f32_e64 s[20:21], v32, v3
	s_and_b64 s[0:1], s[0:1], s[20:21]
	v_cndmask_b32_e64 v3, v3, v32, s[0:1]
	v_and_b32_e32 v37, 0x400000, v34
	v_cndmask_b32_e64 v7, v7, 21, s[0:1]
	v_cmp_eq_u32_e64 s[0:1], 0, v37
	v_cmp_gt_f32_e64 s[20:21], v9, v3
	s_and_b64 s[0:1], s[0:1], s[20:21]
	v_cndmask_b32_e64 v3, v3, v9, s[0:1]
	v_and_b32_e32 v37, 0x800000, v34
	v_cndmask_b32_e64 v7, v7, 22, s[0:1]
	v_cmp_eq_u32_e64 s[0:1], 0, v37
	v_cmp_gt_f32_e64 s[20:21], v8, v3
	s_and_b64 s[0:1], s[0:1], s[20:21]
	v_cndmask_b32_e64 v3, v3, v8, s[0:1]
	v_and_b32_e32 v37, 0x1000000, v34
	v_cndmask_b32_e64 v7, v7, 23, s[0:1]
	v_cmp_eq_u32_e64 s[0:1], 0, v37
	v_cmp_gt_f32_e64 s[20:21], v11, v3
	s_and_b64 s[0:1], s[0:1], s[20:21]
	v_cndmask_b32_e64 v3, v3, v11, s[0:1]
	v_and_b32_e32 v37, 0x2000000, v34
	v_cndmask_b32_e64 v7, v7, 24, s[0:1]
	v_cmp_eq_u32_e64 s[0:1], 0, v37
	v_cmp_gt_f32_e64 s[20:21], v10, v3
	s_and_b64 s[0:1], s[0:1], s[20:21]
	v_cndmask_b32_e64 v3, v3, v10, s[0:1]
	v_and_b32_e32 v37, 0x4000000, v34
	v_cndmask_b32_e64 v7, v7, 25, s[0:1]
	v_cmp_eq_u32_e64 s[0:1], 0, v37
	v_cmp_gt_f32_e64 s[20:21], v5, v3
	s_and_b64 s[0:1], s[0:1], s[20:21]
	v_cndmask_b32_e64 v3, v3, v5, s[0:1]
	v_and_b32_e32 v37, 0x8000000, v34
	v_cndmask_b32_e64 v7, v7, 26, s[0:1]
	v_cmp_eq_u32_e64 s[0:1], 0, v37
	v_cmp_gt_f32_e64 s[20:21], v4, v3
	s_and_b64 s[0:1], s[0:1], s[20:21]
	v_cndmask_b32_e64 v3, v3, v4, s[0:1]
	v_and_b32_e32 v37, 0x10000000, v34
	v_cndmask_b32_e64 v7, v7, 27, s[0:1]
	v_cmp_eq_u32_e64 s[0:1], 0, v37
	v_cmp_gt_f32_e64 s[20:21], v36, v3
	s_and_b64 s[0:1], s[0:1], s[20:21]
	v_cndmask_b32_e64 v3, v3, v36, s[0:1]
	v_and_b32_e32 v37, 0x20000000, v34
	v_cndmask_b32_e64 v7, v7, 28, s[0:1]
	v_cmp_eq_u32_e64 s[0:1], 0, v37
	v_cmp_gt_f32_e64 s[20:21], v35, v3
	s_and_b64 s[0:1], s[0:1], s[20:21]
	v_cndmask_b32_e64 v3, v3, v35, s[0:1]
	v_and_b32_e32 v37, 2.0, v34
	v_cndmask_b32_e64 v7, v7, 29, s[0:1]
	v_cmp_eq_u32_e64 s[0:1], 0, v37
	v_cmp_gt_f32_e64 s[20:21], v2, v3
	s_and_b64 s[0:1], s[0:1], s[20:21]
	v_cndmask_b32_e64 v3, v3, v2, s[0:1]
	v_cndmask_b32_e64 v7, v7, 30, s[0:1]
	v_cmp_ne_u32_e64 s[0:1], 31, v6
	v_cmp_gt_f32_e64 s[20:21], v1, v3
	s_and_b64 s[0:1], s[0:1], s[20:21]
	v_cndmask_b32_e64 v7, v7, 31, s[0:1]
	v_lshl_or_b32 v37, 1, v7, v34
	v_and_b32_e32 v34, 1, v37
	v_cndmask_b32_e64 v3, v3, v1, s[0:1]
	v_cmp_eq_u32_e64 s[0:1], 1, v34
	s_or_b64 s[0:1], s[0:1], vcc
	v_and_b32_e32 v38, 2, v37
	v_cndmask_b32_e64 v34, v27, v155, s[0:1]
	v_cmp_eq_u32_e64 s[0:1], 0, v38
	v_cmp_gt_f32_e64 s[20:21], v26, v34
	s_and_b64 s[0:1], s[0:1], s[20:21]
	v_cndmask_b32_e64 v34, v34, v26, s[0:1]
	v_and_b32_e32 v39, 4, v37
	v_cndmask_b32_e64 v38, 0, 1, s[0:1]
	v_cmp_eq_u32_e64 s[0:1], 0, v39
	v_cmp_gt_f32_e64 s[20:21], v25, v34
	s_and_b64 s[0:1], s[0:1], s[20:21]
	v_cndmask_b32_e64 v34, v34, v25, s[0:1]
	v_and_b32_e32 v39, 8, v37
	v_cndmask_b32_e64 v38, v38, 2, s[0:1]
	v_cmp_eq_u32_e64 s[0:1], 0, v39
	v_cmp_gt_f32_e64 s[20:21], v24, v34
	s_and_b64 s[0:1], s[0:1], s[20:21]
	v_cndmask_b32_e64 v34, v34, v24, s[0:1]
	v_and_b32_e32 v39, 16, v37
	v_cndmask_b32_e64 v38, v38, 3, s[0:1]
	v_cmp_eq_u32_e64 s[0:1], 0, v39
	v_cmp_gt_f32_e64 s[20:21], v23, v34
	s_and_b64 s[0:1], s[0:1], s[20:21]
	v_cndmask_b32_e64 v34, v34, v23, s[0:1]
	v_and_b32_e32 v39, 32, v37
	v_cndmask_b32_e64 v38, v38, 4, s[0:1]
	v_cmp_eq_u32_e64 s[0:1], 0, v39
	v_cmp_gt_f32_e64 s[20:21], v22, v34
	s_and_b64 s[0:1], s[0:1], s[20:21]
	v_cndmask_b32_e64 v34, v34, v22, s[0:1]
	v_and_b32_e32 v39, 64, v37
	v_cndmask_b32_e64 v38, v38, 5, s[0:1]
	v_cmp_eq_u32_e64 s[0:1], 0, v39
	v_cmp_gt_f32_e64 s[20:21], v21, v34
	s_and_b64 s[0:1], s[0:1], s[20:21]
	v_cndmask_b32_e64 v34, v34, v21, s[0:1]
	v_and_b32_e32 v39, 0x80, v37
	v_cndmask_b32_e64 v38, v38, 6, s[0:1]
	v_cmp_eq_u32_e64 s[0:1], 0, v39
	v_cmp_gt_f32_e64 s[20:21], v20, v34
	s_and_b64 s[0:1], s[0:1], s[20:21]
	v_cndmask_b32_e64 v34, v34, v20, s[0:1]
	v_and_b32_e32 v39, 0x100, v37
	v_cndmask_b32_e64 v38, v38, 7, s[0:1]
	v_cmp_eq_u32_e64 s[0:1], 0, v39
	v_cmp_gt_f32_e64 s[20:21], v19, v34
	s_and_b64 s[0:1], s[0:1], s[20:21]
	v_cndmask_b32_e64 v34, v34, v19, s[0:1]
	v_and_b32_e32 v39, 0x200, v37
	v_cndmask_b32_e64 v38, v38, 8, s[0:1]
	v_cmp_eq_u32_e64 s[0:1], 0, v39
	v_cmp_gt_f32_e64 s[20:21], v18, v34
	s_and_b64 s[0:1], s[0:1], s[20:21]
	v_cndmask_b32_e64 v34, v34, v18, s[0:1]
	v_and_b32_e32 v39, 0x400, v37
	v_cndmask_b32_e64 v38, v38, 9, s[0:1]
	v_cmp_eq_u32_e64 s[0:1], 0, v39
	v_cmp_gt_f32_e64 s[20:21], v17, v34
	s_and_b64 s[0:1], s[0:1], s[20:21]
	v_cndmask_b32_e64 v34, v34, v17, s[0:1]
	v_and_b32_e32 v39, 0x800, v37
	v_cndmask_b32_e64 v38, v38, 10, s[0:1]
	v_cmp_eq_u32_e64 s[0:1], 0, v39
	v_cmp_gt_f32_e64 s[20:21], v16, v34
	s_and_b64 s[0:1], s[0:1], s[20:21]
	v_cndmask_b32_e64 v34, v34, v16, s[0:1]
	v_and_b32_e32 v39, 0x1000, v37
	v_cndmask_b32_e64 v38, v38, 11, s[0:1]
	v_cmp_eq_u32_e64 s[0:1], 0, v39
	v_cmp_gt_f32_e64 s[20:21], v15, v34
	s_and_b64 s[0:1], s[0:1], s[20:21]
	v_cndmask_b32_e64 v34, v34, v15, s[0:1]
	v_and_b32_e32 v39, 0x2000, v37
	v_cndmask_b32_e64 v38, v38, 12, s[0:1]
	v_cmp_eq_u32_e64 s[0:1], 0, v39
	v_cmp_gt_f32_e64 s[20:21], v14, v34
	s_and_b64 s[0:1], s[0:1], s[20:21]
	v_cndmask_b32_e64 v34, v34, v14, s[0:1]
	v_and_b32_e32 v39, 0x4000, v37
	v_cndmask_b32_e64 v38, v38, 13, s[0:1]
	v_cmp_eq_u32_e64 s[0:1], 0, v39
	v_cmp_gt_f32_e64 s[20:21], v13, v34
	s_and_b64 s[0:1], s[0:1], s[20:21]
	v_cndmask_b32_e64 v34, v34, v13, s[0:1]
	v_and_b32_e32 v39, 0x8000, v37
	v_cndmask_b32_e64 v38, v38, 14, s[0:1]
	v_cmp_eq_u32_e64 s[0:1], 0, v39
	v_cmp_gt_f32_e64 s[20:21], v12, v34
	s_and_b64 s[0:1], s[0:1], s[20:21]
	v_cndmask_b32_e64 v34, v34, v12, s[0:1]
	v_and_b32_e32 v39, 0x10000, v37
	v_cndmask_b32_e64 v38, v38, 15, s[0:1]
	v_cmp_eq_u32_e64 s[0:1], 0, v39
	v_cmp_gt_f32_e64 s[20:21], v31, v34
	s_and_b64 s[0:1], s[0:1], s[20:21]
	v_cndmask_b32_e64 v34, v34, v31, s[0:1]
	v_and_b32_e32 v39, 0x20000, v37
	v_cndmask_b32_e64 v38, v38, 16, s[0:1]
	v_cmp_eq_u32_e64 s[0:1], 0, v39
	v_cmp_gt_f32_e64 s[20:21], v30, v34
	s_and_b64 s[0:1], s[0:1], s[20:21]
	v_cndmask_b32_e64 v34, v34, v30, s[0:1]
	v_and_b32_e32 v39, 0x40000, v37
	v_cndmask_b32_e64 v38, v38, 17, s[0:1]
	v_cmp_eq_u32_e64 s[0:1], 0, v39
	v_cmp_gt_f32_e64 s[20:21], v29, v34
	s_and_b64 s[0:1], s[0:1], s[20:21]
	v_cndmask_b32_e64 v34, v34, v29, s[0:1]
	v_and_b32_e32 v39, 0x80000, v37
	v_cndmask_b32_e64 v38, v38, 18, s[0:1]
	v_cmp_eq_u32_e64 s[0:1], 0, v39
	v_cmp_gt_f32_e64 s[20:21], v28, v34
	s_and_b64 s[0:1], s[0:1], s[20:21]
	v_cndmask_b32_e64 v34, v34, v28, s[0:1]
	v_and_b32_e32 v39, 0x100000, v37
	v_cndmask_b32_e64 v38, v38, 19, s[0:1]
	v_cmp_eq_u32_e64 s[0:1], 0, v39
	v_cmp_gt_f32_e64 s[20:21], v33, v34
	s_and_b64 s[0:1], s[0:1], s[20:21]
	v_cndmask_b32_e64 v34, v34, v33, s[0:1]
	v_and_b32_e32 v39, 0x200000, v37
	v_cndmask_b32_e64 v38, v38, 20, s[0:1]
	v_cmp_eq_u32_e64 s[0:1], 0, v39
	v_cmp_gt_f32_e64 s[20:21], v32, v34
	s_and_b64 s[0:1], s[0:1], s[20:21]
	v_cndmask_b32_e64 v34, v34, v32, s[0:1]
	v_and_b32_e32 v39, 0x400000, v37
	v_cndmask_b32_e64 v38, v38, 21, s[0:1]
	v_cmp_eq_u32_e64 s[0:1], 0, v39
	v_cmp_gt_f32_e64 s[20:21], v9, v34
	s_and_b64 s[0:1], s[0:1], s[20:21]
	v_cndmask_b32_e64 v34, v34, v9, s[0:1]
	v_and_b32_e32 v39, 0x800000, v37
	v_cndmask_b32_e64 v38, v38, 22, s[0:1]
	v_cmp_eq_u32_e64 s[0:1], 0, v39
	v_cmp_gt_f32_e64 s[20:21], v8, v34
	s_and_b64 s[0:1], s[0:1], s[20:21]
	v_cndmask_b32_e64 v34, v34, v8, s[0:1]
	v_and_b32_e32 v39, 0x1000000, v37
	v_cndmask_b32_e64 v38, v38, 23, s[0:1]
	v_cmp_eq_u32_e64 s[0:1], 0, v39
	v_cmp_gt_f32_e64 s[20:21], v11, v34
	s_and_b64 s[0:1], s[0:1], s[20:21]
	v_cndmask_b32_e64 v34, v34, v11, s[0:1]
	v_and_b32_e32 v39, 0x2000000, v37
	v_cndmask_b32_e64 v38, v38, 24, s[0:1]
	v_cmp_eq_u32_e64 s[0:1], 0, v39
	v_cmp_gt_f32_e64 s[20:21], v10, v34
	s_and_b64 s[0:1], s[0:1], s[20:21]
	v_cndmask_b32_e64 v34, v34, v10, s[0:1]
	v_and_b32_e32 v39, 0x4000000, v37
	v_cndmask_b32_e64 v38, v38, 25, s[0:1]
	v_cmp_eq_u32_e64 s[0:1], 0, v39
	v_cmp_gt_f32_e64 s[20:21], v5, v34
	s_and_b64 s[0:1], s[0:1], s[20:21]
	v_cndmask_b32_e64 v34, v34, v5, s[0:1]
	v_and_b32_e32 v39, 0x8000000, v37
	v_cndmask_b32_e64 v38, v38, 26, s[0:1]
	v_cmp_eq_u32_e64 s[0:1], 0, v39
	v_cmp_gt_f32_e64 s[20:21], v4, v34
	s_and_b64 s[0:1], s[0:1], s[20:21]
	v_cndmask_b32_e64 v34, v34, v4, s[0:1]
	v_and_b32_e32 v39, 0x10000000, v37
	v_cndmask_b32_e64 v38, v38, 27, s[0:1]
	v_cmp_eq_u32_e64 s[0:1], 0, v39
	v_cmp_gt_f32_e64 s[20:21], v36, v34
	s_and_b64 s[0:1], s[0:1], s[20:21]
	v_cndmask_b32_e64 v34, v34, v36, s[0:1]
	v_and_b32_e32 v39, 0x20000000, v37
	v_cndmask_b32_e64 v38, v38, 28, s[0:1]
	v_cmp_eq_u32_e64 s[0:1], 0, v39
	v_cmp_gt_f32_e64 s[20:21], v35, v34
	s_and_b64 s[0:1], s[0:1], s[20:21]
	v_cndmask_b32_e64 v34, v34, v35, s[0:1]
	v_and_b32_e32 v39, 2.0, v37
	v_cndmask_b32_e64 v38, v38, 29, s[0:1]
	v_cmp_eq_u32_e64 s[0:1], 0, v39
	v_cmp_gt_f32_e64 s[20:21], v2, v34
	s_and_b64 s[0:1], s[0:1], s[20:21]
	v_cndmask_b32_e64 v39, v34, v2, s[0:1]
	v_cndmask_b32_e64 v38, v38, 30, s[0:1]
	v_cmp_lt_i32_e64 s[0:1], -1, v37
	v_cmp_gt_f32_e64 s[20:21], v1, v39
	s_and_b64 s[0:1], s[0:1], s[20:21]
	v_cndmask_b32_e64 v34, v38, 31, s[0:1]
	v_cndmask_b32_e64 v38, v39, v1, s[0:1]
	v_lshlrev_b32_e64 v39, v34, 1
	v_or_b32_e32 v40, v39, v37
	v_and_b32_e32 v41, 1, v40
	v_cmp_eq_u32_e64 s[0:1], 1, v41
	s_or_b64 vcc, s[0:1], vcc
	v_cndmask_b32_e32 v27, v27, v155, vcc
	v_bitop3_b32 v41, v39, 2, v37 bitop3:0xc8
	v_cmp_eq_u32_e32 vcc, 0, v41
	v_cmp_gt_f32_e64 s[0:1], v26, v27
	s_and_b64 s[20:21], vcc, s[0:1]
	v_cndmask_b32_e64 v26, v27, v26, s[20:21]
	v_bitop3_b32 v27, v39, 4, v37 bitop3:0xc8
	v_cmp_eq_u32_e32 vcc, 0, v27
	v_cmp_gt_f32_e64 s[0:1], v25, v26
	s_and_b64 s[22:23], vcc, s[0:1]
	v_cndmask_b32_e64 v25, v26, v25, s[22:23]
	v_bitop3_b32 v26, v39, 8, v37 bitop3:0xc8
	v_cmp_eq_u32_e32 vcc, 0, v26
	v_cmp_gt_f32_e64 s[0:1], v24, v25
	s_and_b64 s[24:25], vcc, s[0:1]
	v_cndmask_b32_e64 v24, v25, v24, s[24:25]
	v_bitop3_b32 v25, v39, 16, v37 bitop3:0xc8
	v_cmp_eq_u32_e32 vcc, 0, v25
	v_cmp_gt_f32_e64 s[0:1], v23, v24
	s_and_b64 s[26:27], vcc, s[0:1]
	v_cndmask_b32_e64 v23, v24, v23, s[26:27]
	v_bitop3_b32 v24, v39, 32, v37 bitop3:0xc8
	v_cmp_eq_u32_e32 vcc, 0, v24
	v_cmp_gt_f32_e64 s[0:1], v22, v23
	s_and_b64 s[28:29], vcc, s[0:1]
	v_cndmask_b32_e64 v22, v23, v22, s[28:29]
	v_bitop3_b32 v23, v39, 64, v37 bitop3:0xc8
	v_cmp_eq_u32_e32 vcc, 0, v23
	v_cmp_gt_f32_e64 s[0:1], v21, v22
	s_and_b64 s[30:31], vcc, s[0:1]
	s_movk_i32 s0, 0x80
	v_cndmask_b32_e64 v21, v22, v21, s[30:31]
	v_bitop3_b32 v22, v39, s0, v37 bitop3:0xc8
	v_cmp_eq_u32_e32 vcc, 0, v22
	v_cmp_gt_f32_e64 s[0:1], v20, v21
	s_and_b64 s[34:35], vcc, s[0:1]
	v_cndmask_b32_e64 v20, v21, v20, s[34:35]
	v_bitop3_b32 v21, v39, s33, v37 bitop3:0xc8
	v_cmp_eq_u32_e32 vcc, 0, v21
	v_cmp_gt_f32_e64 s[0:1], v19, v20
	s_and_b64 s[36:37], vcc, s[0:1]
	s_movk_i32 s0, 0x200
	v_cndmask_b32_e64 v19, v20, v19, s[36:37]
	v_bitop3_b32 v20, v39, s0, v37 bitop3:0xc8
	v_cmp_eq_u32_e32 vcc, 0, v20
	v_cmp_gt_f32_e64 s[0:1], v18, v19
	s_and_b64 s[38:39], vcc, s[0:1]
	s_movk_i32 s0, 0x400
	v_cndmask_b32_e64 v18, v19, v18, s[38:39]
	v_bitop3_b32 v19, v39, s0, v37 bitop3:0xc8
	v_cmp_eq_u32_e32 vcc, 0, v19
	v_cmp_gt_f32_e64 s[0:1], v17, v18
	s_and_b64 s[40:41], vcc, s[0:1]
	s_movk_i32 s0, 0x800
	v_cndmask_b32_e64 v17, v18, v17, s[40:41]
	v_bitop3_b32 v18, v39, s0, v37 bitop3:0xc8
	v_cmp_eq_u32_e32 vcc, 0, v18
	v_cmp_gt_f32_e64 s[0:1], v16, v17
	s_and_b64 s[42:43], vcc, s[0:1]
	s_movk_i32 s0, 0x1000
	v_cndmask_b32_e64 v16, v17, v16, s[42:43]
	v_bitop3_b32 v17, v39, s0, v37 bitop3:0xc8
	v_cmp_eq_u32_e32 vcc, 0, v17
	v_cmp_gt_f32_e64 s[0:1], v15, v16
	s_and_b64 s[44:45], vcc, s[0:1]
	s_movk_i32 s0, 0x2000
	v_cndmask_b32_e64 v15, v16, v15, s[44:45]
	v_bitop3_b32 v16, v39, s0, v37 bitop3:0xc8
	v_cmp_eq_u32_e32 vcc, 0, v16
	v_cmp_gt_f32_e64 s[0:1], v14, v15
	s_and_b64 s[46:47], vcc, s[0:1]
	s_movk_i32 s0, 0x4000
	v_cndmask_b32_e64 v14, v15, v14, s[46:47]
	v_bitop3_b32 v15, v39, s0, v37 bitop3:0xc8
	v_cmp_eq_u32_e32 vcc, 0, v15
	v_cmp_gt_f32_e64 s[0:1], v13, v14
	s_and_b64 s[48:49], vcc, s[0:1]
	s_mov_b32 s0, 0x8000
	v_cndmask_b32_e64 v13, v14, v13, s[48:49]
	v_bitop3_b32 v14, v39, s0, v37 bitop3:0xc8
	v_cmp_eq_u32_e32 vcc, 0, v14
	v_cmp_gt_f32_e64 s[0:1], v12, v13
	s_and_b64 s[50:51], vcc, s[0:1]
	s_mov_b32 s0, 0x10000
	v_cndmask_b32_e64 v12, v13, v12, s[50:51]
	v_bitop3_b32 v13, v39, s0, v37 bitop3:0xc8
	v_cmp_eq_u32_e32 vcc, 0, v13
	v_cmp_gt_f32_e64 s[0:1], v31, v12
	s_and_b64 s[52:53], vcc, s[0:1]
	s_mov_b32 s0, 0x20000
	v_cndmask_b32_e64 v12, v12, v31, s[52:53]
	v_bitop3_b32 v13, v39, s0, v37 bitop3:0xc8
	v_cmp_eq_u32_e32 vcc, 0, v13
	v_cmp_gt_f32_e64 s[0:1], v30, v12
	s_and_b64 s[54:55], vcc, s[0:1]
	s_mov_b32 s0, 0x40000
	v_cndmask_b32_e64 v12, v12, v30, s[54:55]
	v_bitop3_b32 v13, v39, s0, v37 bitop3:0xc8
	v_cmp_eq_u32_e32 vcc, 0, v13
	v_cmp_gt_f32_e64 s[0:1], v29, v12
	s_and_b64 s[56:57], vcc, s[0:1]
	s_mov_b32 s0, 0x80000
	v_cndmask_b32_e64 v12, v12, v29, s[56:57]
	v_bitop3_b32 v13, v39, s0, v37 bitop3:0xc8
	v_cmp_eq_u32_e32 vcc, 0, v13
	v_cmp_gt_f32_e64 s[0:1], v28, v12
	s_and_b64 s[58:59], vcc, s[0:1]
	s_mov_b32 s0, 0x100000
	v_cndmask_b32_e64 v12, v12, v28, s[58:59]
	v_bitop3_b32 v13, v39, s0, v37 bitop3:0xc8
	v_cmp_eq_u32_e32 vcc, 0, v13
	v_cmp_gt_f32_e64 s[0:1], v33, v12
	s_and_b64 s[60:61], vcc, s[0:1]
	s_mov_b32 s0, 0x200000
	v_cndmask_b32_e64 v12, v12, v33, s[60:61]
	v_bitop3_b32 v13, v39, s0, v37 bitop3:0xc8
	v_cmp_eq_u32_e32 vcc, 0, v13
	v_cmp_gt_f32_e64 s[0:1], v32, v12
	s_and_b64 s[62:63], vcc, s[0:1]
	s_mov_b32 s0, 0x400000
	v_cndmask_b32_e64 v12, v12, v32, s[62:63]
	v_bitop3_b32 v13, v39, s0, v37 bitop3:0xc8
	v_cmp_eq_u32_e32 vcc, 0, v13
	v_cmp_gt_f32_e64 s[0:1], v9, v12
	s_and_b64 s[64:65], vcc, s[0:1]
	v_cndmask_b32_e64 v9, v12, v9, s[64:65]
	v_bitop3_b32 v12, v39, s11, v37 bitop3:0xc8
	v_cmp_eq_u32_e32 vcc, 0, v12
	v_cmp_gt_f32_e64 s[0:1], v8, v9
	s_and_b64 s[66:67], vcc, s[0:1]
	s_mov_b32 s0, 0x1000000
	v_cndmask_b32_e64 v8, v9, v8, s[66:67]
	v_bitop3_b32 v9, v39, s0, v37 bitop3:0xc8
	v_cmp_eq_u32_e32 vcc, 0, v9
	v_cmp_gt_f32_e64 s[0:1], v11, v8
	s_and_b64 s[68:69], vcc, s[0:1]
	s_brev_b32 s0, 64
	v_cndmask_b32_e64 v8, v8, v11, s[68:69]
	v_bitop3_b32 v9, v39, s0, v37 bitop3:0xc8
	v_cmp_eq_u32_e32 vcc, 0, v9
	v_cmp_gt_f32_e64 s[0:1], v10, v8
	s_and_b64 s[70:71], vcc, s[0:1]
	s_brev_b32 s0, 32
	v_cndmask_b32_e64 v8, v8, v10, s[70:71]
	v_bitop3_b32 v9, v39, s0, v37 bitop3:0xc8
	v_cmp_eq_u32_e32 vcc, 0, v9
	v_cmp_gt_f32_e64 s[0:1], v5, v8
	s_and_b64 s[72:73], vcc, s[0:1]
	s_brev_b32 s0, 16
	v_cndmask_b32_e64 v5, v8, v5, s[72:73]
	v_bitop3_b32 v8, v39, s0, v37 bitop3:0xc8
	v_cmp_eq_u32_e32 vcc, 0, v8
	v_cmp_gt_f32_e64 s[0:1], v4, v5
	s_and_b64 s[76:77], vcc, s[0:1]
	s_brev_b32 s0, 8
	v_cndmask_b32_e64 v4, v5, v4, s[76:77]
	v_bitop3_b32 v5, v39, s0, v37 bitop3:0xc8
	v_cmp_eq_u32_e32 vcc, 0, v5
	v_cmp_gt_f32_e64 s[0:1], v36, v4
	s_and_b64 s[74:75], vcc, s[0:1]
	s_brev_b32 s0, 4
	v_cndmask_b32_e64 v4, v4, v36, s[74:75]
	v_bitop3_b32 v5, v39, s0, v37 bitop3:0xc8
	v_cmp_eq_u32_e32 vcc, 0, v5
	v_cmp_gt_f32_e64 s[0:1], v35, v4
	s_and_b64 s[78:79], vcc, s[0:1]
	v_cndmask_b32_e64 v4, v4, v35, s[78:79]
	v_bitop3_b32 v5, v39, 2.0, v37 bitop3:0xc8
	v_cmp_eq_u32_e32 vcc, 0, v5
	v_cmp_gt_f32_e64 s[0:1], v2, v4
	s_and_b64 s[80:81], vcc, s[0:1]
	v_cndmask_b32_e64 v2, v4, v2, s[80:81]
	v_cmp_lt_i32_e32 vcc, -1, v40
	v_cmp_gt_f32_e64 s[0:1], v1, v2
	s_and_b64 s[82:83], vcc, s[0:1]
	v_cndmask_b32_e64 v1, v2, v1, s[82:83]
	v_sub_f32_e32 v2, v0, v0
	v_mul_f32_e32 v4, 0x3fb8aa3b, v2
	s_mov_b32 s0, 0x3fb8aa3b
	v_fma_f32 v5, v2, s0, -v4
	v_rndne_f32_e32 v8, v4
	v_fmac_f32_e32 v5, 0x32a5705f, v2
	v_sub_f32_e32 v4, v4, v8
	v_add_f32_e32 v4, v4, v5
	v_exp_f32_e32 v4, v4
	v_cvt_i32_f32_e32 v5, v8
	s_mov_b32 s1, 0xc2ce8ed0
	v_cmp_ngt_f32_e32 vcc, s1, v2
	v_ldexp_f32 v4, v4, v5
	s_nop 0
	v_cndmask_b32_e32 v4, 0, v4, vcc
	v_cmp_nlt_f32_e32 vcc, s13, v2
	v_sub_f32_e32 v2, v3, v0
	v_mul_f32_e32 v3, 0x3fb8aa3b, v2
	v_cndmask_b32_e32 v12, v156, v4, vcc
	v_fma_f32 v4, v2, s0, -v3
	v_rndne_f32_e32 v5, v3
	v_fmac_f32_e32 v4, 0x32a5705f, v2
	v_sub_f32_e32 v3, v3, v5
	v_add_f32_e32 v3, v3, v4
	v_exp_f32_e32 v3, v3
	v_cvt_i32_f32_e32 v4, v5
	v_cmp_ngt_f32_e32 vcc, s1, v2
	v_ldexp_f32 v3, v3, v4
	s_nop 0
	v_cndmask_b32_e32 v3, 0, v3, vcc
	v_cmp_nlt_f32_e32 vcc, s13, v2
	s_nop 1
	v_cndmask_b32_e32 v9, v156, v3, vcc
	v_sub_f32_e32 v3, v38, v0
	v_mul_f32_e32 v4, 0x3fb8aa3b, v3
	v_fma_f32 v5, v3, s0, -v4
	v_rndne_f32_e32 v8, v4
	v_fmac_f32_e32 v5, 0x32a5705f, v3
	v_sub_f32_e32 v4, v4, v8
	v_add_f32_e32 v4, v4, v5
	v_exp_f32_e32 v4, v4
	v_cvt_i32_f32_e32 v5, v8
	v_cmp_ngt_f32_e32 vcc, s1, v3
	v_sub_f32_e32 v0, v1, v0
	v_mul_f32_e32 v1, 0x3fb8aa3b, v0
	v_ldexp_f32 v4, v4, v5
	v_cndmask_b32_e32 v4, 0, v4, vcc
	v_cmp_nlt_f32_e32 vcc, s13, v3
	v_fma_f32 v3, v0, s0, -v1
	v_fmac_f32_e32 v3, 0x32a5705f, v0
	v_cndmask_b32_e32 v8, v156, v4, vcc
	v_rndne_f32_e32 v4, v1
	v_sub_f32_e32 v1, v1, v4
	v_add_f32_e32 v1, v1, v3
	v_exp_f32_e32 v1, v1
	v_cvt_i32_f32_e32 v3, v4
	v_cmp_ngt_f32_e32 vcc, s1, v0
	s_lshl_b64 s[0:1], s[88:89], 8
	v_add_f32_e32 v2, v12, v9
	v_ldexp_f32 v1, v1, v3
	v_cndmask_b32_e32 v1, 0, v1, vcc
	v_cmp_nlt_f32_e32 vcc, s13, v0
	v_lshl_add_u64 v[4:5], s[0:1], 0, v[124:125]
	v_readlane_b32 s0, v253, 4
	v_add_f32_e32 v2, v2, v8
	v_cndmask_b32_e32 v10, v156, v1, vcc
	v_lshlrev_b64 v[0:1], 2, v[4:5]
	v_readlane_b32 s1, v253, 5
	v_add_f32_e32 v11, v2, v10
	s_nop 0
	v_lshl_add_u64 v[2:3], s[0:1], 0, v[0:1]
	global_store_dword v[2:3], v6, off
	v_div_scale_f32 v2, s[0:1], v11, v11, v12
	v_rcp_f32_e32 v3, v2
	v_readlane_b32 s0, v252, 4
	v_readlane_b32 s1, v252, 5
	v_fma_f32 v13, -v2, v3, 1.0
	v_fmac_f32_e32 v3, v13, v3
	v_div_scale_f32 v13, vcc, v12, v11, v12
	v_mul_f32_e32 v14, v13, v3
	v_fma_f32 v15, -v2, v14, v13
	v_fmac_f32_e32 v14, v15, v3
	v_fma_f32 v2, -v2, v14, v13
	v_div_fmas_f32 v2, v2, v3, v14
	v_div_fixup_f32 v12, v2, v11, v12
	v_lshl_add_u64 v[2:3], s[0:1], 0, v[0:1]
	v_readlane_b32 s0, v252, 12
	v_readlane_b32 s1, v252, 13
	global_store_dword v[2:3], v12, off
	s_andn2_b64 vcc, exec, s[0:1]
	v_cndmask_b32_e64 v2, 0, 1, s[0:1]
	v_cmp_ne_u32_e64 s[84:85], 1, v2
	v_lshl_add_u64 v[2:3], v[4:5], 2, s[94:95]
	s_cbranch_vccnz .LBB0_1061
	global_load_dword v6, v[2:3], off
